# GEMM load segments: m0 write moved ahead of the DMA address add so the s_nop before each LDS-DMA is no longer needed (122 sites)
# speedup vs baseline: 1.0086x; 1.0027x over previous
.Lnobar_e1o:
.LBB0_417:
	s_add_u32 s28, s6, 0xfffc0080
	s_addc_u32 s29, s7, -1
	s_add_i32 s43, 0, 0x10000
	s_cmp_eq_u32 s42, 12
	s_cselect_b32 s31, s5, s29
	s_cselect_b32 s30, s8, s28
	s_cselect_b32 s29, s9, s33
	s_cselect_b32 s28, s21, s23
	s_add_i32 s63, 0, 0x14000
	v_add_u32_e32 v142, s43, v186
	v_add_u32_e32 v168, s63, v186
	ds_read_b128 v[130:133], v142
	ds_read_b128 v[134:137], v142 offset:1024
	ds_read_b128 v[138:141], v142 offset:2048
	ds_read_b128 v[142:145], v142 offset:3072
	ds_read_b128 v[146:149], v168
	ds_read_b128 v[150:153], v168 offset:1024
	ds_read_b128 v[154:157], v168 offset:2048
	ds_read_b128 v[168:171], v168 offset:3072
	v_lshl_add_u64 v[216:217], s[6:7], 0, v[166:167]
	s_add_i32 m0, s45, 0xc000
	ds_read_b128 v[172:175], v188
	ds_read_b128 v[176:179], v188 offset:1024
	ds_read_b128 v[180:183], v188 offset:2048
	ds_read_b128 v[190:193], v188 offset:3072
	ds_read_b128 v[194:197], v188 offset:4096
	ds_read_b128 v[198:201], v188 offset:5120
	ds_read_b128 v[202:205], v188 offset:6144
	ds_read_b128 v[206:209], v188 offset:7168
	global_load_lds_dwordx4 v[216:217], off
	s_add_i32 m0, s45, 0xe000
	v_lshl_add_u64 v[216:217], s[6:7], 0, v[164:165]
	global_load_lds_dwordx4 v[216:217], off
	s_waitcnt vmcnt(8)
	s_waitcnt lgkmcnt(0)
	s_barrier
	s_setprio 1
	s_waitcnt lgkmcnt(0)
	v_mfma_f32_16x16x32_bf16 v[126:129], v[130:133], v[172:175], v[126:129]
	v_mfma_f32_16x16x32_bf16 v[122:125], v[138:141], v[172:175], v[122:125]
	v_mfma_f32_16x16x32_bf16 v[114:117], v[130:133], v[180:183], v[114:117]
	v_mfma_f32_16x16x32_bf16 v[106:109], v[138:141], v[180:183], v[106:109]
	v_mfma_f32_16x16x32_bf16 v[98:101], v[130:133], v[194:197], v[98:101]
	v_mfma_f32_16x16x32_bf16 v[90:93], v[138:141], v[194:197], v[90:93]
	v_mfma_f32_16x16x32_bf16 v[82:85], v[130:133], v[202:205], v[82:85]
	v_mfma_f32_16x16x32_bf16 v[74:77], v[138:141], v[202:205], v[74:77]
	v_mfma_f32_16x16x32_bf16 v[126:129], v[134:137], v[176:179], v[126:129]
	v_mfma_f32_16x16x32_bf16 v[122:125], v[142:145], v[176:179], v[122:125]
	v_mfma_f32_16x16x32_bf16 v[114:117], v[134:137], v[190:193], v[114:117]
	v_mfma_f32_16x16x32_bf16 v[106:109], v[142:145], v[190:193], v[106:109]
	v_mfma_f32_16x16x32_bf16 v[98:101], v[134:137], v[198:201], v[98:101]
	v_mfma_f32_16x16x32_bf16 v[90:93], v[142:145], v[198:201], v[90:93]
	v_mfma_f32_16x16x32_bf16 v[82:85], v[134:137], v[206:209], v[82:85]
	v_mfma_f32_16x16x32_bf16 v[74:77], v[142:145], v[206:209], v[74:77]
	s_setprio 0
	s_setprio 1
	v_mfma_f32_16x16x32_bf16 v[118:121], v[146:149], v[172:175], v[118:121]
	v_mfma_f32_16x16x32_bf16 v[110:113], v[154:157], v[172:175], v[110:113]
	v_mfma_f32_16x16x32_bf16 v[102:105], v[146:149], v[180:183], v[102:105]
	v_mfma_f32_16x16x32_bf16 v[94:97], v[154:157], v[180:183], v[94:97]
	v_mfma_f32_16x16x32_bf16 v[86:89], v[146:149], v[194:197], v[86:89]
	v_mfma_f32_16x16x32_bf16 v[78:81], v[154:157], v[194:197], v[78:81]
	v_mfma_f32_16x16x32_bf16 v[70:73], v[146:149], v[202:205], v[70:73]
	v_mfma_f32_16x16x32_bf16 v[66:69], v[154:157], v[202:205], v[66:69]
	v_mfma_f32_16x16x32_bf16 v[118:121], v[150:153], v[176:179], v[118:121]
	v_mfma_f32_16x16x32_bf16 v[110:113], v[168:171], v[176:179], v[110:113]
	v_mfma_f32_16x16x32_bf16 v[102:105], v[150:153], v[190:193], v[102:105]
	v_mfma_f32_16x16x32_bf16 v[94:97], v[168:171], v[190:193], v[94:97]
	v_mfma_f32_16x16x32_bf16 v[86:89], v[150:153], v[198:201], v[86:89]
	v_mfma_f32_16x16x32_bf16 v[78:81], v[168:171], v[198:201], v[78:81]
	v_mfma_f32_16x16x32_bf16 v[70:73], v[150:153], v[206:209], v[70:73]
	v_mfma_f32_16x16x32_bf16 v[66:69], v[168:171], v[206:209], v[66:69]
	s_setprio 0
	s_barrier
	s_add_i32 s43, s43, s44
	v_lshl_add_u64 v[216:217], s[28:29], 0, v[0:1]
	s_mov_b32 m0, s43
	ds_read_b128 v[172:175], v188 offset:16384
	ds_read_b128 v[176:179], v188 offset:17408
	ds_read_b128 v[180:183], v188 offset:18432
	ds_read_b128 v[190:193], v188 offset:19456
	ds_read_b128 v[194:197], v188 offset:20480
	ds_read_b128 v[198:201], v188 offset:21504
	ds_read_b128 v[202:205], v188 offset:22528
	ds_read_b128 v[206:209], v188 offset:23552
	global_load_lds_dwordx4 v[216:217], off
	s_add_i32 m0, s43, 0x2000
	s_add_u32 s58, s28, 0x40000
	v_lshl_add_u64 v[218:219], s[28:29], 0, v[158:159]
	s_addc_u32 s59, s29, 0
	s_add_i32 s43, s63, s44
	global_load_lds_dwordx4 v[218:219], off
	v_lshl_add_u64 v[220:221], s[58:59], 0, v[0:1]
	s_mov_b32 m0, s43
	v_lshl_add_u64 v[222:223], s[30:31], 0, v[160:161]
	global_load_lds_dwordx4 v[220:221], off
	s_add_i32 m0, s43, 0x2000
	v_lshl_add_u64 v[220:221], s[58:59], 0, v[158:159]
	global_load_lds_dwordx4 v[220:221], off
	s_mov_b32 m0, s45
	v_lshl_add_u64 v[220:221], s[30:31], 0, v[162:163]
	global_load_lds_dwordx4 v[220:221], off
	s_mov_b32 m0, s46
	s_nop 0
	global_load_lds_dwordx4 v[222:223], off
	s_waitcnt vmcnt(8)
	s_waitcnt lgkmcnt(0)
	s_barrier
	s_setprio 1
	s_waitcnt lgkmcnt(0)
	v_mfma_f32_16x16x32_bf16 v[62:65], v[130:133], v[172:175], v[62:65]
	v_mfma_f32_16x16x32_bf16 v[58:61], v[138:141], v[172:175], v[58:61]
	v_mfma_f32_16x16x32_bf16 v[50:53], v[130:133], v[180:183], v[50:53]
	v_mfma_f32_16x16x32_bf16 v[42:45], v[138:141], v[180:183], v[42:45]
	v_mfma_f32_16x16x32_bf16 v[34:37], v[130:133], v[194:197], v[34:37]
	v_mfma_f32_16x16x32_bf16 v[26:29], v[138:141], v[194:197], v[26:29]
	v_mfma_f32_16x16x32_bf16 v[18:21], v[130:133], v[202:205], v[18:21]
	v_mfma_f32_16x16x32_bf16 v[10:13], v[138:141], v[202:205], v[10:13]
	v_mfma_f32_16x16x32_bf16 v[62:65], v[134:137], v[176:179], v[62:65]
	v_mfma_f32_16x16x32_bf16 v[58:61], v[142:145], v[176:179], v[58:61]
	v_mfma_f32_16x16x32_bf16 v[50:53], v[134:137], v[190:193], v[50:53]
	v_mfma_f32_16x16x32_bf16 v[42:45], v[142:145], v[190:193], v[42:45]
	v_mfma_f32_16x16x32_bf16 v[34:37], v[134:137], v[198:201], v[34:37]
	v_mfma_f32_16x16x32_bf16 v[26:29], v[142:145], v[198:201], v[26:29]
	v_mfma_f32_16x16x32_bf16 v[18:21], v[134:137], v[206:209], v[18:21]
	v_mfma_f32_16x16x32_bf16 v[10:13], v[142:145], v[206:209], v[10:13]
	s_setprio 0
	s_setprio 1
	v_mfma_f32_16x16x32_bf16 v[54:57], v[146:149], v[172:175], v[54:57]
	v_mfma_f32_16x16x32_bf16 v[46:49], v[154:157], v[172:175], v[46:49]
	v_mfma_f32_16x16x32_bf16 v[38:41], v[146:149], v[180:183], v[38:41]
	v_mfma_f32_16x16x32_bf16 v[30:33], v[154:157], v[180:183], v[30:33]
	v_mfma_f32_16x16x32_bf16 v[22:25], v[146:149], v[194:197], v[22:25]
	v_mfma_f32_16x16x32_bf16 v[14:17], v[154:157], v[194:197], v[14:17]
	v_mfma_f32_16x16x32_bf16 v[6:9], v[146:149], v[202:205], v[6:9]
	v_mfma_f32_16x16x32_bf16 v[2:5], v[154:157], v[202:205], v[2:5]
	v_mfma_f32_16x16x32_bf16 v[54:57], v[150:153], v[176:179], v[54:57]
	v_mfma_f32_16x16x32_bf16 v[46:49], v[168:171], v[176:179], v[46:49]
	v_mfma_f32_16x16x32_bf16 v[38:41], v[150:153], v[190:193], v[38:41]
	v_mfma_f32_16x16x32_bf16 v[30:33], v[168:171], v[190:193], v[30:33]
	v_mfma_f32_16x16x32_bf16 v[22:25], v[150:153], v[198:201], v[22:25]
	v_mfma_f32_16x16x32_bf16 v[14:17], v[168:171], v[198:201], v[14:17]
	v_mfma_f32_16x16x32_bf16 v[6:9], v[150:153], v[206:209], v[6:9]
	v_mfma_f32_16x16x32_bf16 v[2:5], v[168:171], v[206:209], v[2:5]
	s_setprio 0
	s_barrier
	s_add_i32 s43, 0, 0x18000
	s_add_i32 s58, 0, 0x1c000
	v_add_u32_e32 v142, s43, v186
	v_add_u32_e32 v168, s58, v186
	ds_read_b128 v[130:133], v142
	ds_read_b128 v[134:137], v142 offset:1024
	ds_read_b128 v[138:141], v142 offset:2048
	ds_read_b128 v[142:145], v142 offset:3072
	ds_read_b128 v[146:149], v168
	ds_read_b128 v[150:153], v168 offset:1024
	ds_read_b128 v[154:157], v168 offset:2048
	ds_read_b128 v[168:171], v168 offset:3072
	s_add_u32 s30, s30, 0x40000
	s_addc_u32 s31, s31, 0
	s_mov_b32 m0, s47
	v_lshl_add_u64 v[224:225], s[30:31], 0, v[162:163]
	ds_read_b128 v[172:175], v188 offset:32768
	ds_read_b128 v[176:179], v188 offset:33792
	ds_read_b128 v[180:183], v188 offset:34816
	ds_read_b128 v[190:193], v188 offset:35840
	ds_read_b128 v[194:197], v188 offset:36864
	ds_read_b128 v[198:201], v188 offset:37888
	ds_read_b128 v[202:205], v188 offset:38912
	ds_read_b128 v[206:209], v188 offset:39936
	global_load_lds_dwordx4 v[224:225], off
	s_mov_b32 m0, s48
	v_lshl_add_u64 v[224:225], s[30:31], 0, v[160:161]
	global_load_lds_dwordx4 v[224:225], off
	s_waitcnt vmcnt(8)
	s_waitcnt lgkmcnt(0)
	s_barrier
	s_setprio 1
	s_waitcnt lgkmcnt(0)
	v_mfma_f32_16x16x32_bf16 v[126:129], v[130:133], v[172:175], v[126:129]
	v_mfma_f32_16x16x32_bf16 v[122:125], v[138:141], v[172:175], v[122:125]
	v_mfma_f32_16x16x32_bf16 v[114:117], v[130:133], v[180:183], v[114:117]
	v_mfma_f32_16x16x32_bf16 v[106:109], v[138:141], v[180:183], v[106:109]
	v_mfma_f32_16x16x32_bf16 v[98:101], v[130:133], v[194:197], v[98:101]
	v_mfma_f32_16x16x32_bf16 v[90:93], v[138:141], v[194:197], v[90:93]
	v_mfma_f32_16x16x32_bf16 v[82:85], v[130:133], v[202:205], v[82:85]
	v_mfma_f32_16x16x32_bf16 v[74:77], v[138:141], v[202:205], v[74:77]
	v_mfma_f32_16x16x32_bf16 v[126:129], v[134:137], v[176:179], v[126:129]
	v_mfma_f32_16x16x32_bf16 v[122:125], v[142:145], v[176:179], v[122:125]
	v_mfma_f32_16x16x32_bf16 v[114:117], v[134:137], v[190:193], v[114:117]
	v_mfma_f32_16x16x32_bf16 v[106:109], v[142:145], v[190:193], v[106:109]
	v_mfma_f32_16x16x32_bf16 v[98:101], v[134:137], v[198:201], v[98:101]
	v_mfma_f32_16x16x32_bf16 v[90:93], v[142:145], v[198:201], v[90:93]
	v_mfma_f32_16x16x32_bf16 v[82:85], v[134:137], v[206:209], v[82:85]
	v_mfma_f32_16x16x32_bf16 v[74:77], v[142:145], v[206:209], v[74:77]
	s_setprio 0
	s_setprio 1
	v_mfma_f32_16x16x32_bf16 v[118:121], v[146:149], v[172:175], v[118:121]
	v_mfma_f32_16x16x32_bf16 v[110:113], v[154:157], v[172:175], v[110:113]
	v_mfma_f32_16x16x32_bf16 v[102:105], v[146:149], v[180:183], v[102:105]
	v_mfma_f32_16x16x32_bf16 v[94:97], v[154:157], v[180:183], v[94:97]
	v_mfma_f32_16x16x32_bf16 v[86:89], v[146:149], v[194:197], v[86:89]
	v_mfma_f32_16x16x32_bf16 v[78:81], v[154:157], v[194:197], v[78:81]
	v_mfma_f32_16x16x32_bf16 v[70:73], v[146:149], v[202:205], v[70:73]
	v_mfma_f32_16x16x32_bf16 v[66:69], v[154:157], v[202:205], v[66:69]
	v_mfma_f32_16x16x32_bf16 v[118:121], v[150:153], v[176:179], v[118:121]
	v_mfma_f32_16x16x32_bf16 v[110:113], v[168:171], v[176:179], v[110:113]
	v_mfma_f32_16x16x32_bf16 v[102:105], v[150:153], v[190:193], v[102:105]
	v_mfma_f32_16x16x32_bf16 v[94:97], v[168:171], v[190:193], v[94:97]
	v_mfma_f32_16x16x32_bf16 v[86:89], v[150:153], v[198:201], v[86:89]
	v_mfma_f32_16x16x32_bf16 v[78:81], v[168:171], v[198:201], v[78:81]
	v_mfma_f32_16x16x32_bf16 v[70:73], v[150:153], v[206:209], v[70:73]
	v_mfma_f32_16x16x32_bf16 v[66:69], v[168:171], v[206:209], v[66:69]
	s_setprio 0
	s_barrier
	s_add_i32 s30, s43, s44
	v_lshl_add_u64 v[216:217], v[216:217], 0, s[56:57]
	s_mov_b32 m0, s30
	ds_read_b128 v[172:175], v188 offset:49152
	ds_read_b128 v[176:179], v188 offset:50176
	ds_read_b128 v[180:183], v188 offset:51200
	ds_read_b128 v[190:193], v188 offset:52224
	ds_read_b128 v[194:197], v188 offset:53248
	ds_read_b128 v[198:201], v188 offset:54272
	ds_read_b128 v[202:205], v188 offset:55296
	ds_read_b128 v[206:209], v188 offset:56320
	global_load_lds_dwordx4 v[216:217], off
	s_add_i32 m0, s30, 0x2000
	s_add_u32 s28, s28, 0x40080
	v_lshl_add_u64 v[216:217], v[218:219], 0, s[56:57]
	s_addc_u32 s29, s29, 0
	s_add_i32 s30, s58, s44
	global_load_lds_dwordx4 v[216:217], off
	s_mov_b32 m0, s30
	v_lshl_add_u64 v[216:217], s[28:29], 0, v[0:1]
	global_load_lds_dwordx4 v[216:217], off
	s_add_i32 m0, s30, 0x2000
	v_lshl_add_u64 v[216:217], s[28:29], 0, v[158:159]
	global_load_lds_dwordx4 v[216:217], off
	s_mov_b32 m0, s49
	v_lshl_add_u64 v[216:217], v[220:221], 0, s[56:57]
	global_load_lds_dwordx4 v[216:217], off
	s_mov_b32 m0, s52
	v_lshl_add_u64 v[216:217], v[222:223], 0, s[56:57]
	global_load_lds_dwordx4 v[216:217], off
	s_waitcnt vmcnt(8)
	s_waitcnt lgkmcnt(0)
	s_barrier
	s_setprio 1
	s_waitcnt lgkmcnt(0)
	v_mfma_f32_16x16x32_bf16 v[62:65], v[130:133], v[172:175], v[62:65]
	v_mfma_f32_16x16x32_bf16 v[58:61], v[138:141], v[172:175], v[58:61]
	v_mfma_f32_16x16x32_bf16 v[50:53], v[130:133], v[180:183], v[50:53]
	v_mfma_f32_16x16x32_bf16 v[42:45], v[138:141], v[180:183], v[42:45]
	v_mfma_f32_16x16x32_bf16 v[34:37], v[130:133], v[194:197], v[34:37]
	v_mfma_f32_16x16x32_bf16 v[26:29], v[138:141], v[194:197], v[26:29]
	v_mfma_f32_16x16x32_bf16 v[18:21], v[130:133], v[202:205], v[18:21]
	v_mfma_f32_16x16x32_bf16 v[10:13], v[138:141], v[202:205], v[10:13]
	v_mfma_f32_16x16x32_bf16 v[62:65], v[134:137], v[176:179], v[62:65]
	v_mfma_f32_16x16x32_bf16 v[58:61], v[142:145], v[176:179], v[58:61]
	v_mfma_f32_16x16x32_bf16 v[50:53], v[134:137], v[190:193], v[50:53]
	v_mfma_f32_16x16x32_bf16 v[42:45], v[142:145], v[190:193], v[42:45]
	v_mfma_f32_16x16x32_bf16 v[34:37], v[134:137], v[198:201], v[34:37]
	v_mfma_f32_16x16x32_bf16 v[26:29], v[142:145], v[198:201], v[26:29]
	v_mfma_f32_16x16x32_bf16 v[18:21], v[134:137], v[206:209], v[18:21]
	v_mfma_f32_16x16x32_bf16 v[10:13], v[142:145], v[206:209], v[10:13]
	s_setprio 0
	s_setprio 1
	v_mfma_f32_16x16x32_bf16 v[54:57], v[146:149], v[172:175], v[54:57]
	v_mfma_f32_16x16x32_bf16 v[46:49], v[154:157], v[172:175], v[46:49]
	v_mfma_f32_16x16x32_bf16 v[38:41], v[146:149], v[180:183], v[38:41]
	v_mfma_f32_16x16x32_bf16 v[30:33], v[154:157], v[180:183], v[30:33]
	v_mfma_f32_16x16x32_bf16 v[22:25], v[146:149], v[194:197], v[22:25]
	v_mfma_f32_16x16x32_bf16 v[14:17], v[154:157], v[194:197], v[14:17]
	v_mfma_f32_16x16x32_bf16 v[6:9], v[146:149], v[202:205], v[6:9]
	v_mfma_f32_16x16x32_bf16 v[2:5], v[154:157], v[202:205], v[2:5]
	v_mfma_f32_16x16x32_bf16 v[54:57], v[150:153], v[176:179], v[54:57]
	v_mfma_f32_16x16x32_bf16 v[46:49], v[168:171], v[176:179], v[46:49]
	v_mfma_f32_16x16x32_bf16 v[38:41], v[150:153], v[190:193], v[38:41]
	v_mfma_f32_16x16x32_bf16 v[30:33], v[168:171], v[190:193], v[30:33]
	v_mfma_f32_16x16x32_bf16 v[22:25], v[150:153], v[198:201], v[22:25]
	v_mfma_f32_16x16x32_bf16 v[14:17], v[168:171], v[198:201], v[14:17]
	v_mfma_f32_16x16x32_bf16 v[6:9], v[150:153], v[206:209], v[6:9]
	v_mfma_f32_16x16x32_bf16 v[2:5], v[168:171], v[206:209], v[2:5]
	s_setprio 0
	s_barrier
	s_add_i32 s42, s42, 2
	s_add_u32 s23, s23, 0x100
	s_addc_u32 s33, s33, 0
	s_add_u32 s6, s6, 0x100
	s_addc_u32 s7, s7, 0
	s_cmp_gt_u32 s42, 13
	s_cbranch_scc0 .LBB0_417
	s_and_b64 vcc, exec, s[18:19]
	s_cbranch_vccz .LBB0_420
	s_barrier

.LBB0_587:
	s_add_u32 s18, s34, s62
	s_addc_u32 s19, s35, s63
	s_add_u32 s18, s18, 0x100
	s_addc_u32 s19, s19, 0
	s_add_u32 s70, s8, s62
	s_addc_u32 s71, s9, s63
	s_add_i32 s26, 0, 0x10000
	s_cmpk_eq_i32 s62, 0x700
	s_cselect_b32 s77, s47, s19
	s_cselect_b32 s76, s59, s18
	s_cselect_b32 s71, s37, s71
	s_cselect_b32 s70, vcc_lo, s70
	s_add_i32 s27, 0, 0x14000
	v_add_u32_e32 v158, s26, v144
	v_add_u32_e32 v176, s27, v144
	ds_read_b128 v[146:149], v158
	ds_read_b128 v[150:153], v158 offset:1024
	ds_read_b128 v[154:157], v158 offset:2048
	ds_read_b128 v[158:161], v158 offset:3072
	ds_read_b128 v[162:165], v176
	ds_read_b128 v[168:171], v176 offset:1024
	ds_read_b128 v[172:175], v176 offset:2048
	ds_read_b128 v[176:179], v176 offset:3072
	v_lshl_add_u64 v[208:209], v[142:143], 0, s[62:63]
	s_add_i32 m0, s4, 0xc000
	ds_read_b128 v[180:183], v145
	ds_read_b128 v[184:187], v145 offset:1024
	ds_read_b128 v[188:191], v145 offset:2048
	ds_read_b128 v[192:195], v145 offset:3072
	ds_read_b128 v[196:199], v145 offset:4096
	ds_read_b128 v[200:203], v145 offset:5120
	ds_read_b128 v[204:207], v145 offset:6144
	ds_read_b128 v[216:219], v145 offset:7168
	global_load_lds_dwordx4 v[208:209], off
	s_add_i32 m0, s4, 0xe000
	v_lshl_add_u64 v[208:209], v[140:141], 0, s[62:63]
	global_load_lds_dwordx4 v[208:209], off
	s_waitcnt vmcnt(8)
	s_waitcnt lgkmcnt(0)
	s_barrier
	s_setprio 1
	s_waitcnt lgkmcnt(0)
	v_mfma_f32_16x16x32_bf16 v[134:137], v[146:149], v[180:183], v[134:137]
	v_mfma_f32_16x16x32_bf16 v[130:133], v[154:157], v[180:183], v[130:133]
	v_mfma_f32_16x16x32_bf16 v[110:113], v[146:149], v[188:191], v[110:113]
	v_mfma_f32_16x16x32_bf16 v[106:109], v[154:157], v[188:191], v[106:109]
	v_mfma_f32_16x16x32_bf16 v[94:97], v[146:149], v[196:199], v[94:97]
	v_mfma_f32_16x16x32_bf16 v[90:93], v[154:157], v[196:199], v[90:93]
	v_mfma_f32_16x16x32_bf16 v[78:81], v[146:149], v[204:207], v[78:81]
	v_mfma_f32_16x16x32_bf16 v[74:77], v[154:157], v[204:207], v[74:77]
	v_mfma_f32_16x16x32_bf16 v[134:137], v[150:153], v[184:187], v[134:137]
	v_mfma_f32_16x16x32_bf16 v[130:133], v[158:161], v[184:187], v[130:133]
	v_mfma_f32_16x16x32_bf16 v[110:113], v[150:153], v[192:195], v[110:113]
	v_mfma_f32_16x16x32_bf16 v[106:109], v[158:161], v[192:195], v[106:109]
	v_mfma_f32_16x16x32_bf16 v[94:97], v[150:153], v[200:203], v[94:97]
	v_mfma_f32_16x16x32_bf16 v[90:93], v[158:161], v[200:203], v[90:93]
	v_mfma_f32_16x16x32_bf16 v[78:81], v[150:153], v[216:219], v[78:81]
	v_mfma_f32_16x16x32_bf16 v[74:77], v[158:161], v[216:219], v[74:77]
	s_setprio 0
	s_setprio 1
	v_mfma_f32_16x16x32_bf16 v[122:125], v[162:165], v[180:183], v[122:125]
	v_mfma_f32_16x16x32_bf16 v[114:117], v[172:175], v[180:183], v[114:117]
	v_mfma_f32_16x16x32_bf16 v[102:105], v[162:165], v[188:191], v[102:105]
	v_mfma_f32_16x16x32_bf16 v[98:101], v[172:175], v[188:191], v[98:101]
	v_mfma_f32_16x16x32_bf16 v[86:89], v[162:165], v[196:199], v[86:89]
	v_mfma_f32_16x16x32_bf16 v[82:85], v[172:175], v[196:199], v[82:85]
	v_mfma_f32_16x16x32_bf16 v[70:73], v[162:165], v[204:207], v[70:73]
	v_mfma_f32_16x16x32_bf16 v[66:69], v[172:175], v[204:207], v[66:69]
	v_mfma_f32_16x16x32_bf16 v[122:125], v[168:171], v[184:187], v[122:125]
	v_mfma_f32_16x16x32_bf16 v[114:117], v[176:179], v[184:187], v[114:117]
	v_mfma_f32_16x16x32_bf16 v[102:105], v[168:171], v[192:195], v[102:105]
	v_mfma_f32_16x16x32_bf16 v[98:101], v[176:179], v[192:195], v[98:101]
	v_mfma_f32_16x16x32_bf16 v[86:89], v[168:171], v[200:203], v[86:89]
	v_mfma_f32_16x16x32_bf16 v[82:85], v[176:179], v[200:203], v[82:85]
	v_mfma_f32_16x16x32_bf16 v[70:73], v[168:171], v[216:219], v[70:73]
	v_mfma_f32_16x16x32_bf16 v[66:69], v[176:179], v[216:219], v[66:69]
	s_setprio 0
	s_barrier
	s_add_i32 s18, s26, s84
	v_lshl_add_u64 v[208:209], s[70:71], 0, v[0:1]
	s_mov_b32 m0, s18
	ds_read_b128 v[180:183], v145 offset:16384
	ds_read_b128 v[184:187], v145 offset:17408
	ds_read_b128 v[188:191], v145 offset:18432
	ds_read_b128 v[192:195], v145 offset:19456
	ds_read_b128 v[196:199], v145 offset:20480
	ds_read_b128 v[200:203], v145 offset:21504
	ds_read_b128 v[204:207], v145 offset:22528
	ds_read_b128 v[216:219], v145 offset:23552
	global_load_lds_dwordx4 v[208:209], off
	s_add_i32 m0, s18, 0x2000
	s_add_u32 s18, s70, 0x40000
	v_lshl_add_u64 v[220:221], s[70:71], 0, v[118:119]
	s_addc_u32 s19, s71, 0
	s_add_i32 s26, s27, s84
	global_load_lds_dwordx4 v[220:221], off
	v_lshl_add_u64 v[222:223], s[18:19], 0, v[0:1]
	s_mov_b32 m0, s26
	v_lshl_add_u64 v[224:225], s[76:77], 0, v[120:121]
	global_load_lds_dwordx4 v[222:223], off
	s_add_i32 m0, s26, 0x2000
	v_lshl_add_u64 v[222:223], s[18:19], 0, v[118:119]
	global_load_lds_dwordx4 v[222:223], off
	s_mov_b32 m0, s4
	v_lshl_add_u64 v[222:223], s[76:77], 0, v[126:127]
	global_load_lds_dwordx4 v[222:223], off
	s_mov_b32 m0, s5
	s_nop 0
	global_load_lds_dwordx4 v[224:225], off
	s_waitcnt vmcnt(8)
	s_waitcnt lgkmcnt(0)
	s_barrier
	s_setprio 1
	s_waitcnt lgkmcnt(0)
	v_mfma_f32_16x16x32_bf16 v[62:65], v[146:149], v[180:183], v[62:65]
	v_mfma_f32_16x16x32_bf16 v[58:61], v[154:157], v[180:183], v[58:61]
	v_mfma_f32_16x16x32_bf16 v[46:49], v[146:149], v[188:191], v[46:49]
	v_mfma_f32_16x16x32_bf16 v[42:45], v[154:157], v[188:191], v[42:45]
	v_mfma_f32_16x16x32_bf16 v[30:33], v[146:149], v[196:199], v[30:33]
	v_mfma_f32_16x16x32_bf16 v[26:29], v[154:157], v[196:199], v[26:29]
	v_mfma_f32_16x16x32_bf16 v[14:17], v[146:149], v[204:207], v[14:17]
	v_mfma_f32_16x16x32_bf16 v[10:13], v[154:157], v[204:207], v[10:13]
	v_mfma_f32_16x16x32_bf16 v[62:65], v[150:153], v[184:187], v[62:65]
	v_mfma_f32_16x16x32_bf16 v[58:61], v[158:161], v[184:187], v[58:61]
	v_mfma_f32_16x16x32_bf16 v[46:49], v[150:153], v[192:195], v[46:49]
	v_mfma_f32_16x16x32_bf16 v[42:45], v[158:161], v[192:195], v[42:45]
	v_mfma_f32_16x16x32_bf16 v[30:33], v[150:153], v[200:203], v[30:33]
	v_mfma_f32_16x16x32_bf16 v[26:29], v[158:161], v[200:203], v[26:29]
	v_mfma_f32_16x16x32_bf16 v[14:17], v[150:153], v[216:219], v[14:17]
	v_mfma_f32_16x16x32_bf16 v[10:13], v[158:161], v[216:219], v[10:13]
	s_setprio 0
	s_setprio 1
	v_mfma_f32_16x16x32_bf16 v[54:57], v[162:165], v[180:183], v[54:57]
	v_mfma_f32_16x16x32_bf16 v[50:53], v[172:175], v[180:183], v[50:53]
	v_mfma_f32_16x16x32_bf16 v[38:41], v[162:165], v[188:191], v[38:41]
	v_mfma_f32_16x16x32_bf16 v[34:37], v[172:175], v[188:191], v[34:37]
	v_mfma_f32_16x16x32_bf16 v[22:25], v[162:165], v[196:199], v[22:25]
	v_mfma_f32_16x16x32_bf16 v[18:21], v[172:175], v[196:199], v[18:21]
	v_mfma_f32_16x16x32_bf16 v[6:9], v[162:165], v[204:207], v[6:9]
	v_mfma_f32_16x16x32_bf16 v[2:5], v[172:175], v[204:207], v[2:5]
	v_mfma_f32_16x16x32_bf16 v[54:57], v[168:171], v[184:187], v[54:57]
	v_mfma_f32_16x16x32_bf16 v[50:53], v[176:179], v[184:187], v[50:53]
	v_mfma_f32_16x16x32_bf16 v[38:41], v[168:171], v[192:195], v[38:41]
	v_mfma_f32_16x16x32_bf16 v[34:37], v[176:179], v[192:195], v[34:37]
	v_mfma_f32_16x16x32_bf16 v[22:25], v[168:171], v[200:203], v[22:25]
	v_mfma_f32_16x16x32_bf16 v[18:21], v[176:179], v[200:203], v[18:21]
	v_mfma_f32_16x16x32_bf16 v[6:9], v[168:171], v[216:219], v[6:9]
	v_mfma_f32_16x16x32_bf16 v[2:5], v[176:179], v[216:219], v[2:5]
	s_setprio 0
	s_barrier
	s_add_i32 s26, 0, 0x18000
	s_add_i32 s27, 0, 0x1c000
	v_add_u32_e32 v158, s26, v144
	v_add_u32_e32 v176, s27, v144
	ds_read_b128 v[146:149], v158
	ds_read_b128 v[150:153], v158 offset:1024
	ds_read_b128 v[154:157], v158 offset:2048
	ds_read_b128 v[158:161], v158 offset:3072
	ds_read_b128 v[162:165], v176
	ds_read_b128 v[168:171], v176 offset:1024
	ds_read_b128 v[172:175], v176 offset:2048
	ds_read_b128 v[176:179], v176 offset:3072
	s_add_u32 s18, s76, 0x40000
	s_addc_u32 s19, s77, 0
	s_mov_b32 m0, s33
	v_lshl_add_u64 v[242:243], s[18:19], 0, v[126:127]
	ds_read_b128 v[180:183], v145 offset:32768
	ds_read_b128 v[184:187], v145 offset:33792
	ds_read_b128 v[188:191], v145 offset:34816
	ds_read_b128 v[192:195], v145 offset:35840
	ds_read_b128 v[196:199], v145 offset:36864
	ds_read_b128 v[200:203], v145 offset:37888
	ds_read_b128 v[204:207], v145 offset:38912
	ds_read_b128 v[216:219], v145 offset:39936
	global_load_lds_dwordx4 v[242:243], off
	s_mov_b32 m0, s92
	v_lshl_add_u64 v[242:243], s[18:19], 0, v[120:121]
	global_load_lds_dwordx4 v[242:243], off
	s_waitcnt vmcnt(8)
	s_waitcnt lgkmcnt(0)
	s_barrier
	s_setprio 1
	s_waitcnt lgkmcnt(0)
	v_mfma_f32_16x16x32_bf16 v[134:137], v[146:149], v[180:183], v[134:137]
	v_mfma_f32_16x16x32_bf16 v[130:133], v[154:157], v[180:183], v[130:133]
	v_mfma_f32_16x16x32_bf16 v[110:113], v[146:149], v[188:191], v[110:113]
	v_mfma_f32_16x16x32_bf16 v[106:109], v[154:157], v[188:191], v[106:109]
	v_mfma_f32_16x16x32_bf16 v[94:97], v[146:149], v[196:199], v[94:97]
	v_mfma_f32_16x16x32_bf16 v[90:93], v[154:157], v[196:199], v[90:93]
	v_mfma_f32_16x16x32_bf16 v[78:81], v[146:149], v[204:207], v[78:81]
	v_mfma_f32_16x16x32_bf16 v[74:77], v[154:157], v[204:207], v[74:77]
	v_mfma_f32_16x16x32_bf16 v[134:137], v[150:153], v[184:187], v[134:137]
	v_mfma_f32_16x16x32_bf16 v[130:133], v[158:161], v[184:187], v[130:133]
	v_mfma_f32_16x16x32_bf16 v[110:113], v[150:153], v[192:195], v[110:113]
	v_mfma_f32_16x16x32_bf16 v[106:109], v[158:161], v[192:195], v[106:109]
	v_mfma_f32_16x16x32_bf16 v[94:97], v[150:153], v[200:203], v[94:97]
	v_mfma_f32_16x16x32_bf16 v[90:93], v[158:161], v[200:203], v[90:93]
	v_mfma_f32_16x16x32_bf16 v[78:81], v[150:153], v[216:219], v[78:81]
	v_mfma_f32_16x16x32_bf16 v[74:77], v[158:161], v[216:219], v[74:77]
	s_setprio 0
	s_setprio 1
	v_mfma_f32_16x16x32_bf16 v[122:125], v[162:165], v[180:183], v[122:125]
	v_mfma_f32_16x16x32_bf16 v[114:117], v[172:175], v[180:183], v[114:117]
	v_mfma_f32_16x16x32_bf16 v[102:105], v[162:165], v[188:191], v[102:105]
	v_mfma_f32_16x16x32_bf16 v[98:101], v[172:175], v[188:191], v[98:101]
	v_mfma_f32_16x16x32_bf16 v[86:89], v[162:165], v[196:199], v[86:89]
	v_mfma_f32_16x16x32_bf16 v[82:85], v[172:175], v[196:199], v[82:85]
	v_mfma_f32_16x16x32_bf16 v[70:73], v[162:165], v[204:207], v[70:73]
	v_mfma_f32_16x16x32_bf16 v[66:69], v[172:175], v[204:207], v[66:69]
	v_mfma_f32_16x16x32_bf16 v[122:125], v[168:171], v[184:187], v[122:125]
	v_mfma_f32_16x16x32_bf16 v[114:117], v[176:179], v[184:187], v[114:117]
	v_mfma_f32_16x16x32_bf16 v[102:105], v[168:171], v[192:195], v[102:105]
	v_mfma_f32_16x16x32_bf16 v[98:101], v[176:179], v[192:195], v[98:101]
	v_mfma_f32_16x16x32_bf16 v[86:89], v[168:171], v[200:203], v[86:89]
	v_mfma_f32_16x16x32_bf16 v[82:85], v[176:179], v[200:203], v[82:85]
	v_mfma_f32_16x16x32_bf16 v[70:73], v[168:171], v[216:219], v[70:73]
	v_mfma_f32_16x16x32_bf16 v[66:69], v[176:179], v[216:219], v[66:69]
	s_setprio 0
	s_barrier
	s_add_i32 s18, s26, s84
	v_lshl_add_u64 v[208:209], v[208:209], 0, s[56:57]
	s_mov_b32 m0, s18
	ds_read_b128 v[180:183], v145 offset:49152
	ds_read_b128 v[184:187], v145 offset:50176
	ds_read_b128 v[188:191], v145 offset:51200
	ds_read_b128 v[192:195], v145 offset:52224
	ds_read_b128 v[196:199], v145 offset:53248
	ds_read_b128 v[200:203], v145 offset:54272
	ds_read_b128 v[204:207], v145 offset:55296
	ds_read_b128 v[216:219], v145 offset:56320
	global_load_lds_dwordx4 v[208:209], off
	s_add_i32 m0, s18, 0x2000
	s_add_u32 s18, s70, 0x40080
	v_lshl_add_u64 v[208:209], v[220:221], 0, s[56:57]
	s_addc_u32 s19, s71, 0
	s_add_i32 s26, s27, s84
	global_load_lds_dwordx4 v[208:209], off
	s_mov_b32 m0, s26
	v_lshl_add_u64 v[208:209], s[18:19], 0, v[0:1]
	global_load_lds_dwordx4 v[208:209], off
	s_add_i32 m0, s26, 0x2000
	v_lshl_add_u64 v[208:209], s[18:19], 0, v[118:119]
	global_load_lds_dwordx4 v[208:209], off
	s_mov_b32 m0, s90
	v_lshl_add_u64 v[208:209], v[222:223], 0, s[56:57]
	global_load_lds_dwordx4 v[208:209], off
	s_mov_b32 m0, s96
	v_lshl_add_u64 v[208:209], v[224:225], 0, s[56:57]
	global_load_lds_dwordx4 v[208:209], off
	s_waitcnt vmcnt(8)
	s_waitcnt lgkmcnt(0)
	s_barrier
	s_setprio 1
	s_waitcnt lgkmcnt(0)
	v_mfma_f32_16x16x32_bf16 v[62:65], v[146:149], v[180:183], v[62:65]
	v_mfma_f32_16x16x32_bf16 v[58:61], v[154:157], v[180:183], v[58:61]
	v_mfma_f32_16x16x32_bf16 v[46:49], v[146:149], v[188:191], v[46:49]
	v_mfma_f32_16x16x32_bf16 v[42:45], v[154:157], v[188:191], v[42:45]
	v_mfma_f32_16x16x32_bf16 v[30:33], v[146:149], v[196:199], v[30:33]
	v_mfma_f32_16x16x32_bf16 v[26:29], v[154:157], v[196:199], v[26:29]
	v_mfma_f32_16x16x32_bf16 v[14:17], v[146:149], v[204:207], v[14:17]
	v_mfma_f32_16x16x32_bf16 v[10:13], v[154:157], v[204:207], v[10:13]
	v_mfma_f32_16x16x32_bf16 v[62:65], v[150:153], v[184:187], v[62:65]
	v_mfma_f32_16x16x32_bf16 v[58:61], v[158:161], v[184:187], v[58:61]
	v_mfma_f32_16x16x32_bf16 v[46:49], v[150:153], v[192:195], v[46:49]
	v_mfma_f32_16x16x32_bf16 v[42:45], v[158:161], v[192:195], v[42:45]
	v_mfma_f32_16x16x32_bf16 v[30:33], v[150:153], v[200:203], v[30:33]
	v_mfma_f32_16x16x32_bf16 v[26:29], v[158:161], v[200:203], v[26:29]
	v_mfma_f32_16x16x32_bf16 v[14:17], v[150:153], v[216:219], v[14:17]
	v_mfma_f32_16x16x32_bf16 v[10:13], v[158:161], v[216:219], v[10:13]
	s_setprio 0
	s_setprio 1
	v_mfma_f32_16x16x32_bf16 v[54:57], v[162:165], v[180:183], v[54:57]
	v_mfma_f32_16x16x32_bf16 v[50:53], v[172:175], v[180:183], v[50:53]
	v_mfma_f32_16x16x32_bf16 v[38:41], v[162:165], v[188:191], v[38:41]
	v_mfma_f32_16x16x32_bf16 v[34:37], v[172:175], v[188:191], v[34:37]
	v_mfma_f32_16x16x32_bf16 v[22:25], v[162:165], v[196:199], v[22:25]
	v_mfma_f32_16x16x32_bf16 v[18:21], v[172:175], v[196:199], v[18:21]
	v_mfma_f32_16x16x32_bf16 v[6:9], v[162:165], v[204:207], v[6:9]
	v_mfma_f32_16x16x32_bf16 v[2:5], v[172:175], v[204:207], v[2:5]
	v_mfma_f32_16x16x32_bf16 v[54:57], v[168:171], v[184:187], v[54:57]
	v_mfma_f32_16x16x32_bf16 v[50:53], v[176:179], v[184:187], v[50:53]
	v_mfma_f32_16x16x32_bf16 v[38:41], v[168:171], v[192:195], v[38:41]
	v_mfma_f32_16x16x32_bf16 v[34:37], v[176:179], v[192:195], v[34:37]
	v_mfma_f32_16x16x32_bf16 v[22:25], v[168:171], v[200:203], v[22:25]
	v_mfma_f32_16x16x32_bf16 v[18:21], v[176:179], v[200:203], v[18:21]
	v_mfma_f32_16x16x32_bf16 v[6:9], v[168:171], v[216:219], v[6:9]
	v_mfma_f32_16x16x32_bf16 v[2:5], v[176:179], v[216:219], v[2:5]
	s_setprio 0
	s_barrier
	s_add_i32 vcc_hi, vcc_hi, 2
	s_add_u32 s62, s62, 0x100
	s_addc_u32 s63, s63, 0
	s_cmp_gt_u32 vcc_hi, 13
	s_cbranch_scc0 .LBB0_587
	s_add_u32 s62, s8, 0xffffff00
	s_addc_u32 s63, s9, -1
	s_andn2_b64 vcc, exec, s[44:45]
	s_cbranch_vccnz .LBB0_590
	v_mov_b32_e32 v2, 0
	s_mov_b32 s20, s36
	s_mov_b32 s83, s46
	s_mov_b64 s[34:35], s[52:53]
	s_mov_b32 s68, s58
	v_mov_b32_e32 v3, v2
	v_mov_b32_e32 v4, v2
	v_mov_b32_e32 v5, v2
	v_mov_b32_e32 v6, v2
	v_mov_b32_e32 v7, v2
	v_mov_b32_e32 v8, v2
	v_mov_b32_e32 v9, v2
	v_mov_b32_e32 v18, v2
	v_mov_b32_e32 v19, v2
	v_mov_b32_e32 v20, v2
	v_mov_b32_e32 v21, v2
	v_mov_b32_e32 v22, v2
	v_mov_b32_e32 v23, v2
	v_mov_b32_e32 v24, v2
	v_mov_b32_e32 v25, v2
	v_mov_b32_e32 v34, v2
	v_mov_b32_e32 v35, v2
	v_mov_b32_e32 v36, v2
	v_mov_b32_e32 v37, v2
	v_mov_b32_e32 v38, v2
	v_mov_b32_e32 v39, v2
	v_mov_b32_e32 v40, v2
	v_mov_b32_e32 v41, v2
	v_mov_b32_e32 v50, v2
	v_mov_b32_e32 v51, v2
	v_mov_b32_e32 v52, v2
	v_mov_b32_e32 v53, v2
	v_mov_b32_e32 v54, v2
	v_mov_b32_e32 v55, v2
	v_mov_b32_e32 v56, v2
	v_mov_b32_e32 v57, v2
	v_mov_b32_e32 v10, v2
	v_mov_b32_e32 v11, v2
	v_mov_b32_e32 v12, v2
	v_mov_b32_e32 v13, v2
	v_mov_b32_e32 v14, v2
	v_mov_b32_e32 v15, v2
	v_mov_b32_e32 v16, v2
	v_mov_b32_e32 v17, v2
	v_mov_b32_e32 v26, v2
	v_mov_b32_e32 v27, v2
	v_mov_b32_e32 v28, v2
	v_mov_b32_e32 v29, v2
	v_mov_b32_e32 v30, v2
	v_mov_b32_e32 v31, v2
	v_mov_b32_e32 v32, v2
	v_mov_b32_e32 v33, v2
	v_mov_b32_e32 v42, v2
	v_mov_b32_e32 v43, v2
	v_mov_b32_e32 v44, v2
	v_mov_b32_e32 v45, v2
	v_mov_b32_e32 v46, v2
	v_mov_b32_e32 v47, v2
	v_mov_b32_e32 v48, v2
	v_mov_b32_e32 v49, v2
	v_mov_b32_e32 v58, v2
	v_mov_b32_e32 v59, v2
	v_mov_b32_e32 v60, v2
	v_mov_b32_e32 v61, v2
	v_mov_b32_e32 v62, v2
	v_mov_b32_e32 v63, v2
	v_mov_b32_e32 v64, v2
	v_mov_b32_e32 v65, v2
	v_mov_b32_e32 v66, v2
	v_mov_b32_e32 v67, v2
	v_mov_b32_e32 v68, v2
	v_mov_b32_e32 v69, v2
	v_mov_b32_e32 v70, v2
	v_mov_b32_e32 v71, v2
	v_mov_b32_e32 v72, v2
	v_mov_b32_e32 v73, v2
	v_mov_b32_e32 v82, v2
	v_mov_b32_e32 v83, v2
	v_mov_b32_e32 v84, v2
	v_mov_b32_e32 v85, v2
	v_mov_b32_e32 v86, v2
	v_mov_b32_e32 v87, v2
	v_mov_b32_e32 v88, v2
	v_mov_b32_e32 v89, v2
	v_mov_b32_e32 v98, v2
	v_mov_b32_e32 v99, v2
	v_mov_b32_e32 v100, v2
	v_mov_b32_e32 v101, v2
	v_mov_b32_e32 v102, v2
	v_mov_b32_e32 v103, v2
	v_mov_b32_e32 v104, v2
	v_mov_b32_e32 v105, v2
	v_mov_b32_e32 v114, v2
	v_mov_b32_e32 v115, v2
	v_mov_b32_e32 v116, v2
	v_mov_b32_e32 v117, v2
	v_mov_b32_e32 v122, v2
	v_mov_b32_e32 v123, v2
	v_mov_b32_e32 v124, v2
	v_mov_b32_e32 v125, v2
	v_mov_b32_e32 v74, v2
	v_mov_b32_e32 v75, v2
	v_mov_b32_e32 v76, v2
	v_mov_b32_e32 v77, v2
	v_mov_b32_e32 v78, v2
	v_mov_b32_e32 v79, v2
	v_mov_b32_e32 v80, v2
	v_mov_b32_e32 v81, v2
	v_mov_b32_e32 v90, v2
	v_mov_b32_e32 v91, v2
	v_mov_b32_e32 v92, v2
	v_mov_b32_e32 v93, v2
	v_mov_b32_e32 v94, v2
	v_mov_b32_e32 v95, v2
	v_mov_b32_e32 v96, v2
	v_mov_b32_e32 v97, v2
	v_mov_b32_e32 v106, v2
	v_mov_b32_e32 v107, v2
	v_mov_b32_e32 v108, v2
	v_mov_b32_e32 v109, v2
	v_mov_b32_e32 v110, v2
	v_mov_b32_e32 v111, v2
	v_mov_b32_e32 v112, v2
	v_mov_b32_e32 v113, v2
	v_mov_b32_e32 v130, v2
	v_mov_b32_e32 v131, v2
	v_mov_b32_e32 v132, v2
	v_mov_b32_e32 v133, v2
	v_mov_b32_e32 v134, v2
	v_mov_b32_e32 v135, v2
	v_mov_b32_e32 v136, v2
	v_mov_b32_e32 v137, v2
	s_andn2_b64 vcc, exec, s[42:43]
	s_cbranch_vccnz .LBB0_591
	s_branch .LBB0_592

.LBB0_684:
	s_add_u32 s52, s30, s48
	s_addc_u32 s53, s31, s49
	s_add_u32 s52, s52, 0x100
	s_addc_u32 s53, s53, 0
	s_add_u32 s95, s8, s48
	s_addc_u32 s96, s9, s49
	s_add_i32 vcc_lo, 0, 0x10000
	s_cmpk_eq_i32 s48, 0x700
	s_cselect_b32 s63, s37, s53
	s_cselect_b32 s62, s59, s52
	s_cselect_b32 s53, s35, s96
	s_cselect_b32 s52, s93, s95
	s_add_i32 s95, 0, 0x14000
	v_add_u32_e32 v158, vcc_lo, v144
	v_add_u32_e32 v167, s95, v144
	ds_read_b128 v[146:149], v158
	ds_read_b128 v[150:153], v158 offset:1024
	ds_read_b128 v[154:157], v158 offset:2048
	ds_read_b128 v[158:161], v158 offset:3072
	ds_read_b128 v[162:165], v167
	ds_read_b128 v[168:171], v167 offset:1024
	ds_read_b128 v[172:175], v167 offset:2048
	ds_read_b128 v[176:179], v167 offset:3072
	v_lshl_add_u64 v[208:209], v[142:143], 0, s[48:49]
	s_add_i32 m0, s4, 0xc000
	ds_read_b128 v[180:183], v145
	ds_read_b128 v[184:187], v145 offset:1024
	ds_read_b128 v[188:191], v145 offset:2048
	ds_read_b128 v[192:195], v145 offset:3072
	ds_read_b128 v[196:199], v145 offset:4096
	ds_read_b128 v[200:203], v145 offset:5120
	ds_read_b128 v[204:207], v145 offset:6144
	ds_read_b128 v[216:219], v145 offset:7168
	global_load_lds_dwordx4 v[208:209], off
	s_add_i32 m0, s4, 0xe000
	v_lshl_add_u64 v[208:209], v[140:141], 0, s[48:49]
	global_load_lds_dwordx4 v[208:209], off
	s_waitcnt vmcnt(8)
	s_waitcnt lgkmcnt(0)
	s_barrier
	s_setprio 1
	s_waitcnt lgkmcnt(0)
	v_mfma_f32_16x16x32_bf16 v[134:137], v[146:149], v[180:183], v[134:137]
	v_mfma_f32_16x16x32_bf16 v[130:133], v[154:157], v[180:183], v[130:133]
	v_mfma_f32_16x16x32_bf16 v[110:113], v[146:149], v[188:191], v[110:113]
	v_mfma_f32_16x16x32_bf16 v[106:109], v[154:157], v[188:191], v[106:109]
	v_mfma_f32_16x16x32_bf16 v[94:97], v[146:149], v[196:199], v[94:97]
	v_mfma_f32_16x16x32_bf16 v[90:93], v[154:157], v[196:199], v[90:93]
	v_mfma_f32_16x16x32_bf16 v[78:81], v[146:149], v[204:207], v[78:81]
	v_mfma_f32_16x16x32_bf16 v[74:77], v[154:157], v[204:207], v[74:77]
	v_mfma_f32_16x16x32_bf16 v[134:137], v[150:153], v[184:187], v[134:137]
	v_mfma_f32_16x16x32_bf16 v[130:133], v[158:161], v[184:187], v[130:133]
	v_mfma_f32_16x16x32_bf16 v[110:113], v[150:153], v[192:195], v[110:113]
	v_mfma_f32_16x16x32_bf16 v[106:109], v[158:161], v[192:195], v[106:109]
	v_mfma_f32_16x16x32_bf16 v[94:97], v[150:153], v[200:203], v[94:97]
	v_mfma_f32_16x16x32_bf16 v[90:93], v[158:161], v[200:203], v[90:93]
	v_mfma_f32_16x16x32_bf16 v[78:81], v[150:153], v[216:219], v[78:81]
	v_mfma_f32_16x16x32_bf16 v[74:77], v[158:161], v[216:219], v[74:77]
	s_setprio 0
	s_setprio 1
	v_mfma_f32_16x16x32_bf16 v[122:125], v[162:165], v[180:183], v[122:125]
	v_mfma_f32_16x16x32_bf16 v[114:117], v[172:175], v[180:183], v[114:117]
	v_mfma_f32_16x16x32_bf16 v[102:105], v[162:165], v[188:191], v[102:105]
	v_mfma_f32_16x16x32_bf16 v[98:101], v[172:175], v[188:191], v[98:101]
	v_mfma_f32_16x16x32_bf16 v[86:89], v[162:165], v[196:199], v[86:89]
	v_mfma_f32_16x16x32_bf16 v[82:85], v[172:175], v[196:199], v[82:85]
	v_mfma_f32_16x16x32_bf16 v[70:73], v[162:165], v[204:207], v[70:73]
	v_mfma_f32_16x16x32_bf16 v[66:69], v[172:175], v[204:207], v[66:69]
	v_mfma_f32_16x16x32_bf16 v[122:125], v[168:171], v[184:187], v[122:125]
	v_mfma_f32_16x16x32_bf16 v[114:117], v[176:179], v[184:187], v[114:117]
	v_mfma_f32_16x16x32_bf16 v[102:105], v[168:171], v[192:195], v[102:105]
	v_mfma_f32_16x16x32_bf16 v[98:101], v[176:179], v[192:195], v[98:101]
	v_mfma_f32_16x16x32_bf16 v[86:89], v[168:171], v[200:203], v[86:89]
	v_mfma_f32_16x16x32_bf16 v[82:85], v[176:179], v[200:203], v[82:85]
	v_mfma_f32_16x16x32_bf16 v[70:73], v[168:171], v[216:219], v[70:73]
	v_mfma_f32_16x16x32_bf16 v[66:69], v[176:179], v[216:219], v[66:69]
	s_setprio 0
	s_barrier
	s_add_i32 s96, vcc_lo, s77
	v_lshl_add_u64 v[208:209], s[52:53], 0, v[0:1]
	s_mov_b32 m0, s96
	ds_read_b128 v[180:183], v145 offset:16384
	ds_read_b128 v[184:187], v145 offset:17408
	ds_read_b128 v[188:191], v145 offset:18432
	ds_read_b128 v[192:195], v145 offset:19456
	ds_read_b128 v[196:199], v145 offset:20480
	ds_read_b128 v[200:203], v145 offset:21504
	ds_read_b128 v[204:207], v145 offset:22528
	ds_read_b128 v[216:219], v145 offset:23552
	global_load_lds_dwordx4 v[208:209], off
	s_add_i32 m0, s96, 0x2000
	s_add_u32 vcc_lo, s52, 0x40000
	v_lshl_add_u64 v[220:221], s[52:53], 0, v[118:119]
	s_addc_u32 vcc_hi, s53, 0
	s_add_i32 s95, s95, s77
	global_load_lds_dwordx4 v[220:221], off
	v_lshl_add_u64 v[222:223], vcc, 0, v[0:1]
	s_mov_b32 m0, s95
	v_lshl_add_u64 v[224:225], s[62:63], 0, v[120:121]
	global_load_lds_dwordx4 v[222:223], off
	s_add_i32 m0, s95, 0x2000
	v_lshl_add_u64 v[222:223], vcc, 0, v[118:119]
	global_load_lds_dwordx4 v[222:223], off
	s_mov_b32 m0, s4
	v_lshl_add_u64 v[222:223], s[62:63], 0, v[126:127]
	global_load_lds_dwordx4 v[222:223], off
	s_mov_b32 m0, s5
	s_nop 0
	global_load_lds_dwordx4 v[224:225], off
	s_waitcnt vmcnt(8)
	s_waitcnt lgkmcnt(0)
	s_barrier
	s_setprio 1
	s_waitcnt lgkmcnt(0)
	v_mfma_f32_16x16x32_bf16 v[62:65], v[146:149], v[180:183], v[62:65]
	v_mfma_f32_16x16x32_bf16 v[58:61], v[154:157], v[180:183], v[58:61]
	v_mfma_f32_16x16x32_bf16 v[46:49], v[146:149], v[188:191], v[46:49]
	v_mfma_f32_16x16x32_bf16 v[42:45], v[154:157], v[188:191], v[42:45]
	v_mfma_f32_16x16x32_bf16 v[30:33], v[146:149], v[196:199], v[30:33]
	v_mfma_f32_16x16x32_bf16 v[26:29], v[154:157], v[196:199], v[26:29]
	v_mfma_f32_16x16x32_bf16 v[14:17], v[146:149], v[204:207], v[14:17]
	v_mfma_f32_16x16x32_bf16 v[10:13], v[154:157], v[204:207], v[10:13]
	v_mfma_f32_16x16x32_bf16 v[62:65], v[150:153], v[184:187], v[62:65]
	v_mfma_f32_16x16x32_bf16 v[58:61], v[158:161], v[184:187], v[58:61]
	v_mfma_f32_16x16x32_bf16 v[46:49], v[150:153], v[192:195], v[46:49]
	v_mfma_f32_16x16x32_bf16 v[42:45], v[158:161], v[192:195], v[42:45]
	v_mfma_f32_16x16x32_bf16 v[30:33], v[150:153], v[200:203], v[30:33]
	v_mfma_f32_16x16x32_bf16 v[26:29], v[158:161], v[200:203], v[26:29]
	v_mfma_f32_16x16x32_bf16 v[14:17], v[150:153], v[216:219], v[14:17]
	v_mfma_f32_16x16x32_bf16 v[10:13], v[158:161], v[216:219], v[10:13]
	s_setprio 0
	s_setprio 1
	v_mfma_f32_16x16x32_bf16 v[54:57], v[162:165], v[180:183], v[54:57]
	v_mfma_f32_16x16x32_bf16 v[50:53], v[172:175], v[180:183], v[50:53]
	v_mfma_f32_16x16x32_bf16 v[38:41], v[162:165], v[188:191], v[38:41]
	v_mfma_f32_16x16x32_bf16 v[34:37], v[172:175], v[188:191], v[34:37]
	v_mfma_f32_16x16x32_bf16 v[22:25], v[162:165], v[196:199], v[22:25]
	v_mfma_f32_16x16x32_bf16 v[18:21], v[172:175], v[196:199], v[18:21]
	v_mfma_f32_16x16x32_bf16 v[6:9], v[162:165], v[204:207], v[6:9]
	v_mfma_f32_16x16x32_bf16 v[2:5], v[172:175], v[204:207], v[2:5]
	v_mfma_f32_16x16x32_bf16 v[54:57], v[168:171], v[184:187], v[54:57]
	v_mfma_f32_16x16x32_bf16 v[50:53], v[176:179], v[184:187], v[50:53]
	v_mfma_f32_16x16x32_bf16 v[38:41], v[168:171], v[192:195], v[38:41]
	v_mfma_f32_16x16x32_bf16 v[34:37], v[176:179], v[192:195], v[34:37]
	v_mfma_f32_16x16x32_bf16 v[22:25], v[168:171], v[200:203], v[22:25]
	v_mfma_f32_16x16x32_bf16 v[18:21], v[176:179], v[200:203], v[18:21]
	v_mfma_f32_16x16x32_bf16 v[6:9], v[168:171], v[216:219], v[6:9]
	v_mfma_f32_16x16x32_bf16 v[2:5], v[176:179], v[216:219], v[2:5]
	s_setprio 0
	s_barrier
	s_add_i32 s95, 0, 0x18000
	s_add_i32 s96, 0, 0x1c000
	v_add_u32_e32 v158, s95, v144
	v_add_u32_e32 v167, s96, v144
	ds_read_b128 v[146:149], v158
	ds_read_b128 v[150:153], v158 offset:1024
	ds_read_b128 v[154:157], v158 offset:2048
	ds_read_b128 v[158:161], v158 offset:3072
	ds_read_b128 v[162:165], v167
	ds_read_b128 v[168:171], v167 offset:1024
	ds_read_b128 v[172:175], v167 offset:2048
	ds_read_b128 v[176:179], v167 offset:3072
	s_add_u32 s62, s62, 0x40000
	s_addc_u32 s63, s63, 0
	s_mov_b32 m0, s33
	v_lshl_add_u64 v[242:243], s[62:63], 0, v[126:127]
	ds_read_b128 v[180:183], v145 offset:32768
	ds_read_b128 v[184:187], v145 offset:33792
	ds_read_b128 v[188:191], v145 offset:34816
	ds_read_b128 v[192:195], v145 offset:35840
	ds_read_b128 v[196:199], v145 offset:36864
	ds_read_b128 v[200:203], v145 offset:37888
	ds_read_b128 v[204:207], v145 offset:38912
	ds_read_b128 v[216:219], v145 offset:39936
	global_load_lds_dwordx4 v[242:243], off
	s_mov_b32 m0, s84
	v_lshl_add_u64 v[242:243], s[62:63], 0, v[120:121]
	global_load_lds_dwordx4 v[242:243], off
	s_waitcnt vmcnt(8)
	s_waitcnt lgkmcnt(0)
	s_barrier
	s_setprio 1
	s_waitcnt lgkmcnt(0)
	v_mfma_f32_16x16x32_bf16 v[134:137], v[146:149], v[180:183], v[134:137]
	v_mfma_f32_16x16x32_bf16 v[130:133], v[154:157], v[180:183], v[130:133]
	v_mfma_f32_16x16x32_bf16 v[110:113], v[146:149], v[188:191], v[110:113]
	v_mfma_f32_16x16x32_bf16 v[106:109], v[154:157], v[188:191], v[106:109]
	v_mfma_f32_16x16x32_bf16 v[94:97], v[146:149], v[196:199], v[94:97]
	v_mfma_f32_16x16x32_bf16 v[90:93], v[154:157], v[196:199], v[90:93]
	v_mfma_f32_16x16x32_bf16 v[78:81], v[146:149], v[204:207], v[78:81]
	v_mfma_f32_16x16x32_bf16 v[74:77], v[154:157], v[204:207], v[74:77]
	v_mfma_f32_16x16x32_bf16 v[134:137], v[150:153], v[184:187], v[134:137]
	v_mfma_f32_16x16x32_bf16 v[130:133], v[158:161], v[184:187], v[130:133]
	v_mfma_f32_16x16x32_bf16 v[110:113], v[150:153], v[192:195], v[110:113]
	v_mfma_f32_16x16x32_bf16 v[106:109], v[158:161], v[192:195], v[106:109]
	v_mfma_f32_16x16x32_bf16 v[94:97], v[150:153], v[200:203], v[94:97]
	v_mfma_f32_16x16x32_bf16 v[90:93], v[158:161], v[200:203], v[90:93]
	v_mfma_f32_16x16x32_bf16 v[78:81], v[150:153], v[216:219], v[78:81]
	v_mfma_f32_16x16x32_bf16 v[74:77], v[158:161], v[216:219], v[74:77]
	s_setprio 0
	s_setprio 1
	v_mfma_f32_16x16x32_bf16 v[122:125], v[162:165], v[180:183], v[122:125]
	v_mfma_f32_16x16x32_bf16 v[114:117], v[172:175], v[180:183], v[114:117]
	v_mfma_f32_16x16x32_bf16 v[102:105], v[162:165], v[188:191], v[102:105]
	v_mfma_f32_16x16x32_bf16 v[98:101], v[172:175], v[188:191], v[98:101]
	v_mfma_f32_16x16x32_bf16 v[86:89], v[162:165], v[196:199], v[86:89]
	v_mfma_f32_16x16x32_bf16 v[82:85], v[172:175], v[196:199], v[82:85]
	v_mfma_f32_16x16x32_bf16 v[70:73], v[162:165], v[204:207], v[70:73]
	v_mfma_f32_16x16x32_bf16 v[66:69], v[172:175], v[204:207], v[66:69]
	v_mfma_f32_16x16x32_bf16 v[122:125], v[168:171], v[184:187], v[122:125]
	v_mfma_f32_16x16x32_bf16 v[114:117], v[176:179], v[184:187], v[114:117]
	v_mfma_f32_16x16x32_bf16 v[102:105], v[168:171], v[192:195], v[102:105]
	v_mfma_f32_16x16x32_bf16 v[98:101], v[176:179], v[192:195], v[98:101]
	v_mfma_f32_16x16x32_bf16 v[86:89], v[168:171], v[200:203], v[86:89]
	v_mfma_f32_16x16x32_bf16 v[82:85], v[176:179], v[200:203], v[82:85]
	v_mfma_f32_16x16x32_bf16 v[70:73], v[168:171], v[216:219], v[70:73]
	v_mfma_f32_16x16x32_bf16 v[66:69], v[176:179], v[216:219], v[66:69]
	s_setprio 0
	s_barrier
	s_add_i32 s62, s95, s77
	v_lshl_add_u64 v[208:209], v[208:209], 0, s[56:57]
	s_mov_b32 m0, s62
	ds_read_b128 v[180:183], v145 offset:49152
	ds_read_b128 v[184:187], v145 offset:50176
	ds_read_b128 v[188:191], v145 offset:51200
	ds_read_b128 v[192:195], v145 offset:52224
	ds_read_b128 v[196:199], v145 offset:53248
	ds_read_b128 v[200:203], v145 offset:54272
	ds_read_b128 v[204:207], v145 offset:55296
	ds_read_b128 v[216:219], v145 offset:56320
	global_load_lds_dwordx4 v[208:209], off
	s_add_i32 m0, s62, 0x2000
	s_add_u32 s52, s52, 0x40080
	v_lshl_add_u64 v[208:209], v[220:221], 0, s[56:57]
	s_addc_u32 s53, s53, 0
	s_add_i32 s62, s96, s77
	global_load_lds_dwordx4 v[208:209], off
	s_mov_b32 m0, s62
	v_lshl_add_u64 v[208:209], s[52:53], 0, v[0:1]
	global_load_lds_dwordx4 v[208:209], off
	s_add_i32 m0, s62, 0x2000
	v_lshl_add_u64 v[208:209], s[52:53], 0, v[118:119]
	global_load_lds_dwordx4 v[208:209], off
	s_mov_b32 m0, s85
	v_lshl_add_u64 v[208:209], v[222:223], 0, s[56:57]
	global_load_lds_dwordx4 v[208:209], off
	s_mov_b32 m0, s90
	v_lshl_add_u64 v[208:209], v[224:225], 0, s[56:57]
	global_load_lds_dwordx4 v[208:209], off
	s_waitcnt vmcnt(8)
	s_waitcnt lgkmcnt(0)
	s_barrier
	s_setprio 1
	s_waitcnt lgkmcnt(0)
	v_mfma_f32_16x16x32_bf16 v[62:65], v[146:149], v[180:183], v[62:65]
	v_mfma_f32_16x16x32_bf16 v[58:61], v[154:157], v[180:183], v[58:61]
	v_mfma_f32_16x16x32_bf16 v[46:49], v[146:149], v[188:191], v[46:49]
	v_mfma_f32_16x16x32_bf16 v[42:45], v[154:157], v[188:191], v[42:45]
	v_mfma_f32_16x16x32_bf16 v[30:33], v[146:149], v[196:199], v[30:33]
	v_mfma_f32_16x16x32_bf16 v[26:29], v[154:157], v[196:199], v[26:29]
	v_mfma_f32_16x16x32_bf16 v[14:17], v[146:149], v[204:207], v[14:17]
	v_mfma_f32_16x16x32_bf16 v[10:13], v[154:157], v[204:207], v[10:13]
	v_mfma_f32_16x16x32_bf16 v[62:65], v[150:153], v[184:187], v[62:65]
	v_mfma_f32_16x16x32_bf16 v[58:61], v[158:161], v[184:187], v[58:61]
	v_mfma_f32_16x16x32_bf16 v[46:49], v[150:153], v[192:195], v[46:49]
	v_mfma_f32_16x16x32_bf16 v[42:45], v[158:161], v[192:195], v[42:45]
	v_mfma_f32_16x16x32_bf16 v[30:33], v[150:153], v[200:203], v[30:33]
	v_mfma_f32_16x16x32_bf16 v[26:29], v[158:161], v[200:203], v[26:29]
	v_mfma_f32_16x16x32_bf16 v[14:17], v[150:153], v[216:219], v[14:17]
	v_mfma_f32_16x16x32_bf16 v[10:13], v[158:161], v[216:219], v[10:13]
	s_setprio 0
	s_setprio 1
	v_mfma_f32_16x16x32_bf16 v[54:57], v[162:165], v[180:183], v[54:57]
	v_mfma_f32_16x16x32_bf16 v[50:53], v[172:175], v[180:183], v[50:53]
	v_mfma_f32_16x16x32_bf16 v[38:41], v[162:165], v[188:191], v[38:41]
	v_mfma_f32_16x16x32_bf16 v[34:37], v[172:175], v[188:191], v[34:37]
	v_mfma_f32_16x16x32_bf16 v[22:25], v[162:165], v[196:199], v[22:25]
	v_mfma_f32_16x16x32_bf16 v[18:21], v[172:175], v[196:199], v[18:21]
	v_mfma_f32_16x16x32_bf16 v[6:9], v[162:165], v[204:207], v[6:9]
	v_mfma_f32_16x16x32_bf16 v[2:5], v[172:175], v[204:207], v[2:5]
	v_mfma_f32_16x16x32_bf16 v[54:57], v[168:171], v[184:187], v[54:57]
	v_mfma_f32_16x16x32_bf16 v[50:53], v[176:179], v[184:187], v[50:53]
	v_mfma_f32_16x16x32_bf16 v[38:41], v[168:171], v[192:195], v[38:41]
	v_mfma_f32_16x16x32_bf16 v[34:37], v[176:179], v[192:195], v[34:37]
	v_mfma_f32_16x16x32_bf16 v[22:25], v[168:171], v[200:203], v[22:25]
	v_mfma_f32_16x16x32_bf16 v[18:21], v[176:179], v[200:203], v[18:21]
	v_mfma_f32_16x16x32_bf16 v[6:9], v[168:171], v[216:219], v[6:9]
	v_mfma_f32_16x16x32_bf16 v[2:5], v[176:179], v[216:219], v[2:5]
	s_setprio 0
	s_barrier
	s_add_i32 s94, s94, 2
	s_add_u32 s48, s48, 0x100
	s_addc_u32 s49, s49, 0
	s_cmp_gt_u32 s94, 13
	s_cbranch_scc0 .LBB0_684
	s_add_u32 s48, s8, 0xffffff00
	s_addc_u32 s49, s9, -1
	s_andn2_b64 vcc, exec, s[42:43]
	s_cbranch_vccnz .LBB0_687
	v_mov_b32_e32 v2, 0
	s_mov_b32 s18, s34
	s_mov_b32 s92, s36
	s_mov_b64 s[30:31], s[46:47]
	s_mov_b32 s68, s58
	v_mov_b32_e32 v3, v2
	v_mov_b32_e32 v4, v2
	v_mov_b32_e32 v5, v2
	v_mov_b32_e32 v6, v2
	v_mov_b32_e32 v7, v2
	v_mov_b32_e32 v8, v2
	v_mov_b32_e32 v9, v2
	v_mov_b32_e32 v18, v2
	v_mov_b32_e32 v19, v2
	v_mov_b32_e32 v20, v2
	v_mov_b32_e32 v21, v2
	v_mov_b32_e32 v22, v2
	v_mov_b32_e32 v23, v2
	v_mov_b32_e32 v24, v2
	v_mov_b32_e32 v25, v2
	v_mov_b32_e32 v34, v2
	v_mov_b32_e32 v35, v2
	v_mov_b32_e32 v36, v2
	v_mov_b32_e32 v37, v2
	v_mov_b32_e32 v38, v2
	v_mov_b32_e32 v39, v2
	v_mov_b32_e32 v40, v2
	v_mov_b32_e32 v41, v2
	v_mov_b32_e32 v50, v2
	v_mov_b32_e32 v51, v2
	v_mov_b32_e32 v52, v2
	v_mov_b32_e32 v53, v2
	v_mov_b32_e32 v54, v2
	v_mov_b32_e32 v55, v2
	v_mov_b32_e32 v56, v2
	v_mov_b32_e32 v57, v2
	v_mov_b32_e32 v10, v2
	v_mov_b32_e32 v11, v2
	v_mov_b32_e32 v12, v2
	v_mov_b32_e32 v13, v2
	v_mov_b32_e32 v14, v2
	v_mov_b32_e32 v15, v2
	v_mov_b32_e32 v16, v2
	v_mov_b32_e32 v17, v2
	v_mov_b32_e32 v26, v2
	v_mov_b32_e32 v27, v2
	v_mov_b32_e32 v28, v2
	v_mov_b32_e32 v29, v2
	v_mov_b32_e32 v30, v2
	v_mov_b32_e32 v31, v2
	v_mov_b32_e32 v32, v2
	v_mov_b32_e32 v33, v2
	v_mov_b32_e32 v42, v2
	v_mov_b32_e32 v43, v2
	v_mov_b32_e32 v44, v2
	v_mov_b32_e32 v45, v2
	v_mov_b32_e32 v46, v2
	v_mov_b32_e32 v47, v2
	v_mov_b32_e32 v48, v2
	v_mov_b32_e32 v49, v2
	v_mov_b32_e32 v58, v2
	v_mov_b32_e32 v59, v2
	v_mov_b32_e32 v60, v2
	v_mov_b32_e32 v61, v2
	v_mov_b32_e32 v62, v2
	v_mov_b32_e32 v63, v2
	v_mov_b32_e32 v64, v2
	v_mov_b32_e32 v65, v2
	v_mov_b32_e32 v66, v2
	v_mov_b32_e32 v67, v2
	v_mov_b32_e32 v68, v2
	v_mov_b32_e32 v69, v2
	v_mov_b32_e32 v70, v2
	v_mov_b32_e32 v71, v2
	v_mov_b32_e32 v72, v2
	v_mov_b32_e32 v73, v2
	v_mov_b32_e32 v82, v2
	v_mov_b32_e32 v83, v2
	v_mov_b32_e32 v84, v2
	v_mov_b32_e32 v85, v2
	v_mov_b32_e32 v86, v2
	v_mov_b32_e32 v87, v2
	v_mov_b32_e32 v88, v2
	v_mov_b32_e32 v89, v2
	v_mov_b32_e32 v98, v2
	v_mov_b32_e32 v99, v2
	v_mov_b32_e32 v100, v2
	v_mov_b32_e32 v101, v2
	v_mov_b32_e32 v102, v2
	v_mov_b32_e32 v103, v2
	v_mov_b32_e32 v104, v2
	v_mov_b32_e32 v105, v2
	v_mov_b32_e32 v114, v2
	v_mov_b32_e32 v115, v2
	v_mov_b32_e32 v116, v2
	v_mov_b32_e32 v117, v2
	v_mov_b32_e32 v122, v2
	v_mov_b32_e32 v123, v2
	v_mov_b32_e32 v124, v2
	v_mov_b32_e32 v125, v2
	v_mov_b32_e32 v74, v2
	v_mov_b32_e32 v75, v2
	v_mov_b32_e32 v76, v2
	v_mov_b32_e32 v77, v2
	v_mov_b32_e32 v78, v2
	v_mov_b32_e32 v79, v2
	v_mov_b32_e32 v80, v2
	v_mov_b32_e32 v81, v2
	v_mov_b32_e32 v90, v2
	v_mov_b32_e32 v91, v2
	v_mov_b32_e32 v92, v2
	v_mov_b32_e32 v93, v2
	v_mov_b32_e32 v94, v2
	v_mov_b32_e32 v95, v2
	v_mov_b32_e32 v96, v2
	v_mov_b32_e32 v97, v2
	v_mov_b32_e32 v106, v2
	v_mov_b32_e32 v107, v2
	v_mov_b32_e32 v108, v2
	v_mov_b32_e32 v109, v2
	v_mov_b32_e32 v110, v2
	v_mov_b32_e32 v111, v2
	v_mov_b32_e32 v112, v2
	v_mov_b32_e32 v113, v2
	v_mov_b32_e32 v130, v2
	v_mov_b32_e32 v131, v2
	v_mov_b32_e32 v132, v2
	v_mov_b32_e32 v133, v2
	v_mov_b32_e32 v134, v2
	v_mov_b32_e32 v135, v2
	v_mov_b32_e32 v136, v2
	v_mov_b32_e32 v137, v2
	s_branch .LBB0_688

.Lnobar_e1e:
.LBB0_836:
	s_add_u32 s28, s6, 0xfffc0080
	s_addc_u32 s29, s7, -1
	s_add_i32 s41, 0, 0x10000
	s_cmp_eq_u32 s40, 12
	s_cselect_b32 s31, s5, s29
	s_cselect_b32 s30, s8, s28
	s_cselect_b32 s29, s9, s33
	s_cselect_b32 s28, s21, s23
	s_add_i32 s53, 0, 0x14000
	v_add_u32_e32 v142, s41, v186
	v_add_u32_e32 v168, s53, v186
	ds_read_b128 v[130:133], v142
	ds_read_b128 v[134:137], v142 offset:1024
	ds_read_b128 v[138:141], v142 offset:2048
	ds_read_b128 v[142:145], v142 offset:3072
	ds_read_b128 v[146:149], v168
	ds_read_b128 v[150:153], v168 offset:1024
	ds_read_b128 v[154:157], v168 offset:2048
	ds_read_b128 v[168:171], v168 offset:3072
	v_lshl_add_u64 v[216:217], s[6:7], 0, v[166:167]
	s_add_i32 m0, s43, 0xc000
	ds_read_b128 v[172:175], v188
	ds_read_b128 v[176:179], v188 offset:1024
	ds_read_b128 v[180:183], v188 offset:2048
	ds_read_b128 v[190:193], v188 offset:3072
	ds_read_b128 v[194:197], v188 offset:4096
	ds_read_b128 v[198:201], v188 offset:5120
	ds_read_b128 v[202:205], v188 offset:6144
	ds_read_b128 v[206:209], v188 offset:7168
	global_load_lds_dwordx4 v[216:217], off
	s_add_i32 m0, s43, 0xe000
	v_lshl_add_u64 v[216:217], s[6:7], 0, v[164:165]
	global_load_lds_dwordx4 v[216:217], off
	s_waitcnt vmcnt(8)
	s_waitcnt lgkmcnt(0)
	s_barrier
	s_setprio 1
	s_waitcnt lgkmcnt(0)
	v_mfma_f32_16x16x32_bf16 v[126:129], v[130:133], v[172:175], v[126:129]
	v_mfma_f32_16x16x32_bf16 v[122:125], v[138:141], v[172:175], v[122:125]
	v_mfma_f32_16x16x32_bf16 v[114:117], v[130:133], v[180:183], v[114:117]
	v_mfma_f32_16x16x32_bf16 v[106:109], v[138:141], v[180:183], v[106:109]
	v_mfma_f32_16x16x32_bf16 v[98:101], v[130:133], v[194:197], v[98:101]
	v_mfma_f32_16x16x32_bf16 v[90:93], v[138:141], v[194:197], v[90:93]
	v_mfma_f32_16x16x32_bf16 v[82:85], v[130:133], v[202:205], v[82:85]
	v_mfma_f32_16x16x32_bf16 v[74:77], v[138:141], v[202:205], v[74:77]
	v_mfma_f32_16x16x32_bf16 v[126:129], v[134:137], v[176:179], v[126:129]
	v_mfma_f32_16x16x32_bf16 v[122:125], v[142:145], v[176:179], v[122:125]
	v_mfma_f32_16x16x32_bf16 v[114:117], v[134:137], v[190:193], v[114:117]
	v_mfma_f32_16x16x32_bf16 v[106:109], v[142:145], v[190:193], v[106:109]
	v_mfma_f32_16x16x32_bf16 v[98:101], v[134:137], v[198:201], v[98:101]
	v_mfma_f32_16x16x32_bf16 v[90:93], v[142:145], v[198:201], v[90:93]
	v_mfma_f32_16x16x32_bf16 v[82:85], v[134:137], v[206:209], v[82:85]
	v_mfma_f32_16x16x32_bf16 v[74:77], v[142:145], v[206:209], v[74:77]
	s_setprio 0
	s_setprio 1
	v_mfma_f32_16x16x32_bf16 v[118:121], v[146:149], v[172:175], v[118:121]
	v_mfma_f32_16x16x32_bf16 v[110:113], v[154:157], v[172:175], v[110:113]
	v_mfma_f32_16x16x32_bf16 v[102:105], v[146:149], v[180:183], v[102:105]
	v_mfma_f32_16x16x32_bf16 v[94:97], v[154:157], v[180:183], v[94:97]
	v_mfma_f32_16x16x32_bf16 v[86:89], v[146:149], v[194:197], v[86:89]
	v_mfma_f32_16x16x32_bf16 v[78:81], v[154:157], v[194:197], v[78:81]
	v_mfma_f32_16x16x32_bf16 v[70:73], v[146:149], v[202:205], v[70:73]
	v_mfma_f32_16x16x32_bf16 v[66:69], v[154:157], v[202:205], v[66:69]
	v_mfma_f32_16x16x32_bf16 v[118:121], v[150:153], v[176:179], v[118:121]
	v_mfma_f32_16x16x32_bf16 v[110:113], v[168:171], v[176:179], v[110:113]
	v_mfma_f32_16x16x32_bf16 v[102:105], v[150:153], v[190:193], v[102:105]
	v_mfma_f32_16x16x32_bf16 v[94:97], v[168:171], v[190:193], v[94:97]
	v_mfma_f32_16x16x32_bf16 v[86:89], v[150:153], v[198:201], v[86:89]
	v_mfma_f32_16x16x32_bf16 v[78:81], v[168:171], v[198:201], v[78:81]
	v_mfma_f32_16x16x32_bf16 v[70:73], v[150:153], v[206:209], v[70:73]
	v_mfma_f32_16x16x32_bf16 v[66:69], v[168:171], v[206:209], v[66:69]
	s_setprio 0
	s_barrier
	s_add_i32 s41, s41, s42
	v_lshl_add_u64 v[216:217], s[28:29], 0, v[0:1]
	s_mov_b32 m0, s41
	ds_read_b128 v[172:175], v188 offset:16384
	ds_read_b128 v[176:179], v188 offset:17408
	ds_read_b128 v[180:183], v188 offset:18432
	ds_read_b128 v[190:193], v188 offset:19456
	ds_read_b128 v[194:197], v188 offset:20480
	ds_read_b128 v[198:201], v188 offset:21504
	ds_read_b128 v[202:205], v188 offset:22528
	ds_read_b128 v[206:209], v188 offset:23552
	global_load_lds_dwordx4 v[216:217], off
	s_add_i32 m0, s41, 0x2000
	s_add_u32 s58, s28, 0x40000
	v_lshl_add_u64 v[218:219], s[28:29], 0, v[158:159]
	s_addc_u32 s59, s29, 0
	s_add_i32 s41, s53, s42
	global_load_lds_dwordx4 v[218:219], off
	v_lshl_add_u64 v[220:221], s[58:59], 0, v[0:1]
	s_mov_b32 m0, s41
	v_lshl_add_u64 v[222:223], s[30:31], 0, v[160:161]
	global_load_lds_dwordx4 v[220:221], off
	s_add_i32 m0, s41, 0x2000
	v_lshl_add_u64 v[220:221], s[58:59], 0, v[158:159]
	global_load_lds_dwordx4 v[220:221], off
	s_mov_b32 m0, s43
	v_lshl_add_u64 v[220:221], s[30:31], 0, v[162:163]
	global_load_lds_dwordx4 v[220:221], off
	s_mov_b32 m0, s44
	s_nop 0
	global_load_lds_dwordx4 v[222:223], off
	s_waitcnt vmcnt(8)
	s_waitcnt lgkmcnt(0)
	s_barrier
	s_setprio 1
	s_waitcnt lgkmcnt(0)
	v_mfma_f32_16x16x32_bf16 v[62:65], v[130:133], v[172:175], v[62:65]
	v_mfma_f32_16x16x32_bf16 v[58:61], v[138:141], v[172:175], v[58:61]
	v_mfma_f32_16x16x32_bf16 v[50:53], v[130:133], v[180:183], v[50:53]
	v_mfma_f32_16x16x32_bf16 v[42:45], v[138:141], v[180:183], v[42:45]
	v_mfma_f32_16x16x32_bf16 v[34:37], v[130:133], v[194:197], v[34:37]
	v_mfma_f32_16x16x32_bf16 v[26:29], v[138:141], v[194:197], v[26:29]
	v_mfma_f32_16x16x32_bf16 v[18:21], v[130:133], v[202:205], v[18:21]
	v_mfma_f32_16x16x32_bf16 v[10:13], v[138:141], v[202:205], v[10:13]
	v_mfma_f32_16x16x32_bf16 v[62:65], v[134:137], v[176:179], v[62:65]
	v_mfma_f32_16x16x32_bf16 v[58:61], v[142:145], v[176:179], v[58:61]
	v_mfma_f32_16x16x32_bf16 v[50:53], v[134:137], v[190:193], v[50:53]
	v_mfma_f32_16x16x32_bf16 v[42:45], v[142:145], v[190:193], v[42:45]
	v_mfma_f32_16x16x32_bf16 v[34:37], v[134:137], v[198:201], v[34:37]
	v_mfma_f32_16x16x32_bf16 v[26:29], v[142:145], v[198:201], v[26:29]
	v_mfma_f32_16x16x32_bf16 v[18:21], v[134:137], v[206:209], v[18:21]
	v_mfma_f32_16x16x32_bf16 v[10:13], v[142:145], v[206:209], v[10:13]
	s_setprio 0
	s_setprio 1
	v_mfma_f32_16x16x32_bf16 v[54:57], v[146:149], v[172:175], v[54:57]
	v_mfma_f32_16x16x32_bf16 v[46:49], v[154:157], v[172:175], v[46:49]
	v_mfma_f32_16x16x32_bf16 v[38:41], v[146:149], v[180:183], v[38:41]
	v_mfma_f32_16x16x32_bf16 v[30:33], v[154:157], v[180:183], v[30:33]
	v_mfma_f32_16x16x32_bf16 v[22:25], v[146:149], v[194:197], v[22:25]
	v_mfma_f32_16x16x32_bf16 v[14:17], v[154:157], v[194:197], v[14:17]
	v_mfma_f32_16x16x32_bf16 v[6:9], v[146:149], v[202:205], v[6:9]
	v_mfma_f32_16x16x32_bf16 v[2:5], v[154:157], v[202:205], v[2:5]
	v_mfma_f32_16x16x32_bf16 v[54:57], v[150:153], v[176:179], v[54:57]
	v_mfma_f32_16x16x32_bf16 v[46:49], v[168:171], v[176:179], v[46:49]
	v_mfma_f32_16x16x32_bf16 v[38:41], v[150:153], v[190:193], v[38:41]
	v_mfma_f32_16x16x32_bf16 v[30:33], v[168:171], v[190:193], v[30:33]
	v_mfma_f32_16x16x32_bf16 v[22:25], v[150:153], v[198:201], v[22:25]
	v_mfma_f32_16x16x32_bf16 v[14:17], v[168:171], v[198:201], v[14:17]
	v_mfma_f32_16x16x32_bf16 v[6:9], v[150:153], v[206:209], v[6:9]
	v_mfma_f32_16x16x32_bf16 v[2:5], v[168:171], v[206:209], v[2:5]
	s_setprio 0
	s_barrier
	s_add_i32 s41, 0, 0x18000
	s_add_i32 s53, 0, 0x1c000
	v_add_u32_e32 v142, s41, v186
	v_add_u32_e32 v168, s53, v186
	ds_read_b128 v[130:133], v142
	ds_read_b128 v[134:137], v142 offset:1024
	ds_read_b128 v[138:141], v142 offset:2048
	ds_read_b128 v[142:145], v142 offset:3072
	ds_read_b128 v[146:149], v168
	ds_read_b128 v[150:153], v168 offset:1024
	ds_read_b128 v[154:157], v168 offset:2048
	ds_read_b128 v[168:171], v168 offset:3072
	s_add_u32 s30, s30, 0x40000
	s_addc_u32 s31, s31, 0
	s_mov_b32 m0, s45
	v_lshl_add_u64 v[224:225], s[30:31], 0, v[162:163]
	ds_read_b128 v[172:175], v188 offset:32768
	ds_read_b128 v[176:179], v188 offset:33792
	ds_read_b128 v[180:183], v188 offset:34816
	ds_read_b128 v[190:193], v188 offset:35840
	ds_read_b128 v[194:197], v188 offset:36864
	ds_read_b128 v[198:201], v188 offset:37888
	ds_read_b128 v[202:205], v188 offset:38912
	ds_read_b128 v[206:209], v188 offset:39936
	global_load_lds_dwordx4 v[224:225], off
	s_mov_b32 m0, s46
	v_lshl_add_u64 v[224:225], s[30:31], 0, v[160:161]
	global_load_lds_dwordx4 v[224:225], off
	s_waitcnt vmcnt(8)
	s_waitcnt lgkmcnt(0)
	s_barrier
	s_setprio 1
	s_waitcnt lgkmcnt(0)
	v_mfma_f32_16x16x32_bf16 v[126:129], v[130:133], v[172:175], v[126:129]
	v_mfma_f32_16x16x32_bf16 v[122:125], v[138:141], v[172:175], v[122:125]
	v_mfma_f32_16x16x32_bf16 v[114:117], v[130:133], v[180:183], v[114:117]
	v_mfma_f32_16x16x32_bf16 v[106:109], v[138:141], v[180:183], v[106:109]
	v_mfma_f32_16x16x32_bf16 v[98:101], v[130:133], v[194:197], v[98:101]
	v_mfma_f32_16x16x32_bf16 v[90:93], v[138:141], v[194:197], v[90:93]
	v_mfma_f32_16x16x32_bf16 v[82:85], v[130:133], v[202:205], v[82:85]
	v_mfma_f32_16x16x32_bf16 v[74:77], v[138:141], v[202:205], v[74:77]
	v_mfma_f32_16x16x32_bf16 v[126:129], v[134:137], v[176:179], v[126:129]
	v_mfma_f32_16x16x32_bf16 v[122:125], v[142:145], v[176:179], v[122:125]
	v_mfma_f32_16x16x32_bf16 v[114:117], v[134:137], v[190:193], v[114:117]
	v_mfma_f32_16x16x32_bf16 v[106:109], v[142:145], v[190:193], v[106:109]
	v_mfma_f32_16x16x32_bf16 v[98:101], v[134:137], v[198:201], v[98:101]
	v_mfma_f32_16x16x32_bf16 v[90:93], v[142:145], v[198:201], v[90:93]
	v_mfma_f32_16x16x32_bf16 v[82:85], v[134:137], v[206:209], v[82:85]
	v_mfma_f32_16x16x32_bf16 v[74:77], v[142:145], v[206:209], v[74:77]
	s_setprio 0
	s_setprio 1
	v_mfma_f32_16x16x32_bf16 v[118:121], v[146:149], v[172:175], v[118:121]
	v_mfma_f32_16x16x32_bf16 v[110:113], v[154:157], v[172:175], v[110:113]
	v_mfma_f32_16x16x32_bf16 v[102:105], v[146:149], v[180:183], v[102:105]
	v_mfma_f32_16x16x32_bf16 v[94:97], v[154:157], v[180:183], v[94:97]
	v_mfma_f32_16x16x32_bf16 v[86:89], v[146:149], v[194:197], v[86:89]
	v_mfma_f32_16x16x32_bf16 v[78:81], v[154:157], v[194:197], v[78:81]
	v_mfma_f32_16x16x32_bf16 v[70:73], v[146:149], v[202:205], v[70:73]
	v_mfma_f32_16x16x32_bf16 v[66:69], v[154:157], v[202:205], v[66:69]
	v_mfma_f32_16x16x32_bf16 v[118:121], v[150:153], v[176:179], v[118:121]
	v_mfma_f32_16x16x32_bf16 v[110:113], v[168:171], v[176:179], v[110:113]
	v_mfma_f32_16x16x32_bf16 v[102:105], v[150:153], v[190:193], v[102:105]
	v_mfma_f32_16x16x32_bf16 v[94:97], v[168:171], v[190:193], v[94:97]
	v_mfma_f32_16x16x32_bf16 v[86:89], v[150:153], v[198:201], v[86:89]
	v_mfma_f32_16x16x32_bf16 v[78:81], v[168:171], v[198:201], v[78:81]
	v_mfma_f32_16x16x32_bf16 v[70:73], v[150:153], v[206:209], v[70:73]
	v_mfma_f32_16x16x32_bf16 v[66:69], v[168:171], v[206:209], v[66:69]
	s_setprio 0
	s_barrier
	s_add_i32 s30, s41, s42
	v_lshl_add_u64 v[216:217], v[216:217], 0, s[56:57]
	s_mov_b32 m0, s30
	ds_read_b128 v[172:175], v188 offset:49152
	ds_read_b128 v[176:179], v188 offset:50176
	ds_read_b128 v[180:183], v188 offset:51200
	ds_read_b128 v[190:193], v188 offset:52224
	ds_read_b128 v[194:197], v188 offset:53248
	ds_read_b128 v[198:201], v188 offset:54272
	ds_read_b128 v[202:205], v188 offset:55296
	ds_read_b128 v[206:209], v188 offset:56320
	global_load_lds_dwordx4 v[216:217], off
	s_add_i32 m0, s30, 0x2000
	s_add_u32 s28, s28, 0x40080
	v_lshl_add_u64 v[216:217], v[218:219], 0, s[56:57]
	s_addc_u32 s29, s29, 0
	s_add_i32 s30, s53, s42
	global_load_lds_dwordx4 v[216:217], off
	s_mov_b32 m0, s30
	v_lshl_add_u64 v[216:217], s[28:29], 0, v[0:1]
	global_load_lds_dwordx4 v[216:217], off
	s_add_i32 m0, s30, 0x2000
	v_lshl_add_u64 v[216:217], s[28:29], 0, v[158:159]
	global_load_lds_dwordx4 v[216:217], off
	s_mov_b32 m0, s47
	v_lshl_add_u64 v[216:217], v[220:221], 0, s[56:57]
	global_load_lds_dwordx4 v[216:217], off
	s_mov_b32 m0, s48
	v_lshl_add_u64 v[216:217], v[222:223], 0, s[56:57]
	global_load_lds_dwordx4 v[216:217], off
	s_waitcnt vmcnt(8)
	s_waitcnt lgkmcnt(0)
	s_barrier
	s_setprio 1
	s_waitcnt lgkmcnt(0)
	v_mfma_f32_16x16x32_bf16 v[62:65], v[130:133], v[172:175], v[62:65]
	v_mfma_f32_16x16x32_bf16 v[58:61], v[138:141], v[172:175], v[58:61]
	v_mfma_f32_16x16x32_bf16 v[50:53], v[130:133], v[180:183], v[50:53]
	v_mfma_f32_16x16x32_bf16 v[42:45], v[138:141], v[180:183], v[42:45]
	v_mfma_f32_16x16x32_bf16 v[34:37], v[130:133], v[194:197], v[34:37]
	v_mfma_f32_16x16x32_bf16 v[26:29], v[138:141], v[194:197], v[26:29]
	v_mfma_f32_16x16x32_bf16 v[18:21], v[130:133], v[202:205], v[18:21]
	v_mfma_f32_16x16x32_bf16 v[10:13], v[138:141], v[202:205], v[10:13]
	v_mfma_f32_16x16x32_bf16 v[62:65], v[134:137], v[176:179], v[62:65]
	v_mfma_f32_16x16x32_bf16 v[58:61], v[142:145], v[176:179], v[58:61]
	v_mfma_f32_16x16x32_bf16 v[50:53], v[134:137], v[190:193], v[50:53]
	v_mfma_f32_16x16x32_bf16 v[42:45], v[142:145], v[190:193], v[42:45]
	v_mfma_f32_16x16x32_bf16 v[34:37], v[134:137], v[198:201], v[34:37]
	v_mfma_f32_16x16x32_bf16 v[26:29], v[142:145], v[198:201], v[26:29]
	v_mfma_f32_16x16x32_bf16 v[18:21], v[134:137], v[206:209], v[18:21]
	v_mfma_f32_16x16x32_bf16 v[10:13], v[142:145], v[206:209], v[10:13]
	s_setprio 0
	s_setprio 1
	v_mfma_f32_16x16x32_bf16 v[54:57], v[146:149], v[172:175], v[54:57]
	v_mfma_f32_16x16x32_bf16 v[46:49], v[154:157], v[172:175], v[46:49]
	v_mfma_f32_16x16x32_bf16 v[38:41], v[146:149], v[180:183], v[38:41]
	v_mfma_f32_16x16x32_bf16 v[30:33], v[154:157], v[180:183], v[30:33]
	v_mfma_f32_16x16x32_bf16 v[22:25], v[146:149], v[194:197], v[22:25]
	v_mfma_f32_16x16x32_bf16 v[14:17], v[154:157], v[194:197], v[14:17]
	v_mfma_f32_16x16x32_bf16 v[6:9], v[146:149], v[202:205], v[6:9]
	v_mfma_f32_16x16x32_bf16 v[2:5], v[154:157], v[202:205], v[2:5]
	v_mfma_f32_16x16x32_bf16 v[54:57], v[150:153], v[176:179], v[54:57]
	v_mfma_f32_16x16x32_bf16 v[46:49], v[168:171], v[176:179], v[46:49]
	v_mfma_f32_16x16x32_bf16 v[38:41], v[150:153], v[190:193], v[38:41]
	v_mfma_f32_16x16x32_bf16 v[30:33], v[168:171], v[190:193], v[30:33]
	v_mfma_f32_16x16x32_bf16 v[22:25], v[150:153], v[198:201], v[22:25]
	v_mfma_f32_16x16x32_bf16 v[14:17], v[168:171], v[198:201], v[14:17]
	v_mfma_f32_16x16x32_bf16 v[6:9], v[150:153], v[206:209], v[6:9]
	v_mfma_f32_16x16x32_bf16 v[2:5], v[168:171], v[206:209], v[2:5]
	s_setprio 0
	s_barrier
	s_add_i32 s40, s40, 2
	s_add_u32 s23, s23, 0x100
	s_addc_u32 s33, s33, 0
	s_add_u32 s6, s6, 0x100
	s_addc_u32 s7, s7, 0
	s_cmp_gt_u32 s40, 13
	s_cbranch_scc0 .LBB0_836
	s_and_b64 vcc, exec, s[18:19]
	s_cbranch_vccz .LBB0_839
	s_barrier

.LBB0_1525:
	s_add_u32 s36, s26, s34
	s_addc_u32 s37, s27, s35
	s_add_u32 s36, s36, 0x100
	s_addc_u32 s37, s37, 0
	s_add_u32 s82, s8, s34
	s_addc_u32 s83, s9, s35
	s_add_i32 s84, 0, 0x10000
	s_cmpk_eq_i32 s34, 0xb00
	s_cselect_b32 s45, s31, s37
	s_cselect_b32 s44, s30, s36
	s_cselect_b32 s37, s29, s83
	s_cselect_b32 s36, s28, s82
	s_add_i32 s85, 0, 0x14000
	v_add_u32_e32 v158, s84, v144
	v_add_u32_e32 v176, s85, v144
	ds_read_b128 v[146:149], v158
	ds_read_b128 v[150:153], v158 offset:1024
	ds_read_b128 v[154:157], v158 offset:2048
	ds_read_b128 v[158:161], v158 offset:3072
	ds_read_b128 v[162:165], v176
	ds_read_b128 v[168:171], v176 offset:1024
	ds_read_b128 v[172:175], v176 offset:2048
	ds_read_b128 v[176:179], v176 offset:3072
	v_lshl_add_u64 v[208:209], v[142:143], 0, s[34:35]
	s_add_i32 m0, s4, 0xc000
	ds_read_b128 v[180:183], v145
	ds_read_b128 v[184:187], v145 offset:1024
	ds_read_b128 v[188:191], v145 offset:2048
	ds_read_b128 v[192:195], v145 offset:3072
	ds_read_b128 v[196:199], v145 offset:4096
	ds_read_b128 v[200:203], v145 offset:5120
	ds_read_b128 v[204:207], v145 offset:6144
	ds_read_b128 v[216:219], v145 offset:7168
	global_load_lds_dwordx4 v[208:209], off
	s_add_i32 m0, s4, 0xe000
	v_lshl_add_u64 v[208:209], v[140:141], 0, s[34:35]
	global_load_lds_dwordx4 v[208:209], off
	s_waitcnt vmcnt(8)
	s_waitcnt lgkmcnt(0)
	s_barrier
	s_setprio 1
	s_waitcnt lgkmcnt(0)
	v_mfma_f32_16x16x32_bf16 v[134:137], v[146:149], v[180:183], v[134:137]
	v_mfma_f32_16x16x32_bf16 v[130:133], v[154:157], v[180:183], v[130:133]
	v_mfma_f32_16x16x32_bf16 v[110:113], v[146:149], v[188:191], v[110:113]
	v_mfma_f32_16x16x32_bf16 v[106:109], v[154:157], v[188:191], v[106:109]
	v_mfma_f32_16x16x32_bf16 v[94:97], v[146:149], v[196:199], v[94:97]
	v_mfma_f32_16x16x32_bf16 v[90:93], v[154:157], v[196:199], v[90:93]
	v_mfma_f32_16x16x32_bf16 v[78:81], v[146:149], v[204:207], v[78:81]
	v_mfma_f32_16x16x32_bf16 v[74:77], v[154:157], v[204:207], v[74:77]
	v_mfma_f32_16x16x32_bf16 v[134:137], v[150:153], v[184:187], v[134:137]
	v_mfma_f32_16x16x32_bf16 v[130:133], v[158:161], v[184:187], v[130:133]
	v_mfma_f32_16x16x32_bf16 v[110:113], v[150:153], v[192:195], v[110:113]
	v_mfma_f32_16x16x32_bf16 v[106:109], v[158:161], v[192:195], v[106:109]
	v_mfma_f32_16x16x32_bf16 v[94:97], v[150:153], v[200:203], v[94:97]
	v_mfma_f32_16x16x32_bf16 v[90:93], v[158:161], v[200:203], v[90:93]
	v_mfma_f32_16x16x32_bf16 v[78:81], v[150:153], v[216:219], v[78:81]
	v_mfma_f32_16x16x32_bf16 v[74:77], v[158:161], v[216:219], v[74:77]
	s_setprio 0
	s_setprio 1
	v_mfma_f32_16x16x32_bf16 v[122:125], v[162:165], v[180:183], v[122:125]
	v_mfma_f32_16x16x32_bf16 v[114:117], v[172:175], v[180:183], v[114:117]
	v_mfma_f32_16x16x32_bf16 v[102:105], v[162:165], v[188:191], v[102:105]
	v_mfma_f32_16x16x32_bf16 v[98:101], v[172:175], v[188:191], v[98:101]
	v_mfma_f32_16x16x32_bf16 v[86:89], v[162:165], v[196:199], v[86:89]
	v_mfma_f32_16x16x32_bf16 v[82:85], v[172:175], v[196:199], v[82:85]
	v_mfma_f32_16x16x32_bf16 v[70:73], v[162:165], v[204:207], v[70:73]
	v_mfma_f32_16x16x32_bf16 v[66:69], v[172:175], v[204:207], v[66:69]
	v_mfma_f32_16x16x32_bf16 v[122:125], v[168:171], v[184:187], v[122:125]
	v_mfma_f32_16x16x32_bf16 v[114:117], v[176:179], v[184:187], v[114:117]
	v_mfma_f32_16x16x32_bf16 v[102:105], v[168:171], v[192:195], v[102:105]
	v_mfma_f32_16x16x32_bf16 v[98:101], v[176:179], v[192:195], v[98:101]
	v_mfma_f32_16x16x32_bf16 v[86:89], v[168:171], v[200:203], v[86:89]
	v_mfma_f32_16x16x32_bf16 v[82:85], v[176:179], v[200:203], v[82:85]
	v_mfma_f32_16x16x32_bf16 v[70:73], v[168:171], v[216:219], v[70:73]
	v_mfma_f32_16x16x32_bf16 v[66:69], v[176:179], v[216:219], v[66:69]
	s_setprio 0
	s_barrier
	s_add_i32 s82, s84, s70
	v_lshl_add_u64 v[208:209], s[36:37], 0, v[0:1]
	s_mov_b32 m0, s82
	ds_read_b128 v[180:183], v145 offset:16384
	ds_read_b128 v[184:187], v145 offset:17408
	ds_read_b128 v[188:191], v145 offset:18432
	ds_read_b128 v[192:195], v145 offset:19456
	ds_read_b128 v[196:199], v145 offset:20480
	ds_read_b128 v[200:203], v145 offset:21504
	ds_read_b128 v[204:207], v145 offset:22528
	ds_read_b128 v[216:219], v145 offset:23552
	global_load_lds_dwordx4 v[208:209], off
	s_add_i32 m0, s82, 0x2000
	s_add_u32 s82, s36, 0x60000
	v_lshl_add_u64 v[220:221], s[36:37], 0, v[118:119]
	s_addc_u32 s83, s37, 0
	s_add_i32 s84, s85, s70
	global_load_lds_dwordx4 v[220:221], off
	v_lshl_add_u64 v[222:223], s[82:83], 0, v[0:1]
	s_mov_b32 m0, s84
	v_lshl_add_u64 v[224:225], s[44:45], 0, v[120:121]
	global_load_lds_dwordx4 v[222:223], off
	s_add_i32 m0, s84, 0x2000
	v_lshl_add_u64 v[222:223], s[82:83], 0, v[118:119]
	global_load_lds_dwordx4 v[222:223], off
	s_mov_b32 m0, s4
	v_lshl_add_u64 v[222:223], s[44:45], 0, v[126:127]
	global_load_lds_dwordx4 v[222:223], off
	s_mov_b32 m0, s33
	s_nop 0
	global_load_lds_dwordx4 v[224:225], off
	s_waitcnt vmcnt(8)
	s_waitcnt lgkmcnt(0)
	s_barrier
	s_setprio 1
	s_waitcnt lgkmcnt(0)
	v_mfma_f32_16x16x32_bf16 v[62:65], v[146:149], v[180:183], v[62:65]
	v_mfma_f32_16x16x32_bf16 v[58:61], v[154:157], v[180:183], v[58:61]
	v_mfma_f32_16x16x32_bf16 v[46:49], v[146:149], v[188:191], v[46:49]
	v_mfma_f32_16x16x32_bf16 v[42:45], v[154:157], v[188:191], v[42:45]
	v_mfma_f32_16x16x32_bf16 v[30:33], v[146:149], v[196:199], v[30:33]
	v_mfma_f32_16x16x32_bf16 v[26:29], v[154:157], v[196:199], v[26:29]
	v_mfma_f32_16x16x32_bf16 v[14:17], v[146:149], v[204:207], v[14:17]
	v_mfma_f32_16x16x32_bf16 v[10:13], v[154:157], v[204:207], v[10:13]
	v_mfma_f32_16x16x32_bf16 v[62:65], v[150:153], v[184:187], v[62:65]
	v_mfma_f32_16x16x32_bf16 v[58:61], v[158:161], v[184:187], v[58:61]
	v_mfma_f32_16x16x32_bf16 v[46:49], v[150:153], v[192:195], v[46:49]
	v_mfma_f32_16x16x32_bf16 v[42:45], v[158:161], v[192:195], v[42:45]
	v_mfma_f32_16x16x32_bf16 v[30:33], v[150:153], v[200:203], v[30:33]
	v_mfma_f32_16x16x32_bf16 v[26:29], v[158:161], v[200:203], v[26:29]
	v_mfma_f32_16x16x32_bf16 v[14:17], v[150:153], v[216:219], v[14:17]
	v_mfma_f32_16x16x32_bf16 v[10:13], v[158:161], v[216:219], v[10:13]
	s_setprio 0
	s_setprio 1
	v_mfma_f32_16x16x32_bf16 v[54:57], v[162:165], v[180:183], v[54:57]
	v_mfma_f32_16x16x32_bf16 v[50:53], v[172:175], v[180:183], v[50:53]
	v_mfma_f32_16x16x32_bf16 v[38:41], v[162:165], v[188:191], v[38:41]
	v_mfma_f32_16x16x32_bf16 v[34:37], v[172:175], v[188:191], v[34:37]
	v_mfma_f32_16x16x32_bf16 v[22:25], v[162:165], v[196:199], v[22:25]
	v_mfma_f32_16x16x32_bf16 v[18:21], v[172:175], v[196:199], v[18:21]
	v_mfma_f32_16x16x32_bf16 v[6:9], v[162:165], v[204:207], v[6:9]
	v_mfma_f32_16x16x32_bf16 v[2:5], v[172:175], v[204:207], v[2:5]
	v_mfma_f32_16x16x32_bf16 v[54:57], v[168:171], v[184:187], v[54:57]
	v_mfma_f32_16x16x32_bf16 v[50:53], v[176:179], v[184:187], v[50:53]
	v_mfma_f32_16x16x32_bf16 v[38:41], v[168:171], v[192:195], v[38:41]
	v_mfma_f32_16x16x32_bf16 v[34:37], v[176:179], v[192:195], v[34:37]
	v_mfma_f32_16x16x32_bf16 v[22:25], v[168:171], v[200:203], v[22:25]
	v_mfma_f32_16x16x32_bf16 v[18:21], v[176:179], v[200:203], v[18:21]
	v_mfma_f32_16x16x32_bf16 v[6:9], v[168:171], v[216:219], v[6:9]
	v_mfma_f32_16x16x32_bf16 v[2:5], v[176:179], v[216:219], v[2:5]
	s_setprio 0
	s_barrier
	s_add_i32 s82, 0, 0x18000
	s_add_i32 s83, 0, 0x1c000
	v_add_u32_e32 v158, s82, v144
	v_add_u32_e32 v176, s83, v144
	ds_read_b128 v[146:149], v158
	ds_read_b128 v[150:153], v158 offset:1024
	ds_read_b128 v[154:157], v158 offset:2048
	ds_read_b128 v[158:161], v158 offset:3072
	ds_read_b128 v[162:165], v176
	ds_read_b128 v[168:171], v176 offset:1024
	ds_read_b128 v[172:175], v176 offset:2048
	ds_read_b128 v[176:179], v176 offset:3072
	s_add_u32 s44, s44, 0x60000
	s_addc_u32 s45, s45, 0
	s_mov_b32 m0, s71
	v_lshl_add_u64 v[242:243], s[44:45], 0, v[126:127]
	ds_read_b128 v[180:183], v145 offset:32768
	ds_read_b128 v[184:187], v145 offset:33792
	ds_read_b128 v[188:191], v145 offset:34816
	ds_read_b128 v[192:195], v145 offset:35840
	ds_read_b128 v[196:199], v145 offset:36864
	ds_read_b128 v[200:203], v145 offset:37888
	ds_read_b128 v[204:207], v145 offset:38912
	ds_read_b128 v[216:219], v145 offset:39936
	global_load_lds_dwordx4 v[242:243], off
	s_mov_b32 m0, s76
	v_lshl_add_u64 v[242:243], s[44:45], 0, v[120:121]
	global_load_lds_dwordx4 v[242:243], off
	s_waitcnt vmcnt(8)
	s_waitcnt lgkmcnt(0)
	s_barrier
	s_setprio 1
	s_waitcnt lgkmcnt(0)
	v_mfma_f32_16x16x32_bf16 v[134:137], v[146:149], v[180:183], v[134:137]
	v_mfma_f32_16x16x32_bf16 v[130:133], v[154:157], v[180:183], v[130:133]
	v_mfma_f32_16x16x32_bf16 v[110:113], v[146:149], v[188:191], v[110:113]
	v_mfma_f32_16x16x32_bf16 v[106:109], v[154:157], v[188:191], v[106:109]
	v_mfma_f32_16x16x32_bf16 v[94:97], v[146:149], v[196:199], v[94:97]
	v_mfma_f32_16x16x32_bf16 v[90:93], v[154:157], v[196:199], v[90:93]
	v_mfma_f32_16x16x32_bf16 v[78:81], v[146:149], v[204:207], v[78:81]
	v_mfma_f32_16x16x32_bf16 v[74:77], v[154:157], v[204:207], v[74:77]
	v_mfma_f32_16x16x32_bf16 v[134:137], v[150:153], v[184:187], v[134:137]
	v_mfma_f32_16x16x32_bf16 v[130:133], v[158:161], v[184:187], v[130:133]
	v_mfma_f32_16x16x32_bf16 v[110:113], v[150:153], v[192:195], v[110:113]
	v_mfma_f32_16x16x32_bf16 v[106:109], v[158:161], v[192:195], v[106:109]
	v_mfma_f32_16x16x32_bf16 v[94:97], v[150:153], v[200:203], v[94:97]
	v_mfma_f32_16x16x32_bf16 v[90:93], v[158:161], v[200:203], v[90:93]
	v_mfma_f32_16x16x32_bf16 v[78:81], v[150:153], v[216:219], v[78:81]
	v_mfma_f32_16x16x32_bf16 v[74:77], v[158:161], v[216:219], v[74:77]
	s_setprio 0
	s_setprio 1
	v_mfma_f32_16x16x32_bf16 v[122:125], v[162:165], v[180:183], v[122:125]
	v_mfma_f32_16x16x32_bf16 v[114:117], v[172:175], v[180:183], v[114:117]
	v_mfma_f32_16x16x32_bf16 v[102:105], v[162:165], v[188:191], v[102:105]
	v_mfma_f32_16x16x32_bf16 v[98:101], v[172:175], v[188:191], v[98:101]
	v_mfma_f32_16x16x32_bf16 v[86:89], v[162:165], v[196:199], v[86:89]
	v_mfma_f32_16x16x32_bf16 v[82:85], v[172:175], v[196:199], v[82:85]
	v_mfma_f32_16x16x32_bf16 v[70:73], v[162:165], v[204:207], v[70:73]
	v_mfma_f32_16x16x32_bf16 v[66:69], v[172:175], v[204:207], v[66:69]
	v_mfma_f32_16x16x32_bf16 v[122:125], v[168:171], v[184:187], v[122:125]
	v_mfma_f32_16x16x32_bf16 v[114:117], v[176:179], v[184:187], v[114:117]
	v_mfma_f32_16x16x32_bf16 v[102:105], v[168:171], v[192:195], v[102:105]
	v_mfma_f32_16x16x32_bf16 v[98:101], v[176:179], v[192:195], v[98:101]
	v_mfma_f32_16x16x32_bf16 v[86:89], v[168:171], v[200:203], v[86:89]
	v_mfma_f32_16x16x32_bf16 v[82:85], v[176:179], v[200:203], v[82:85]
	v_mfma_f32_16x16x32_bf16 v[70:73], v[168:171], v[216:219], v[70:73]
	v_mfma_f32_16x16x32_bf16 v[66:69], v[176:179], v[216:219], v[66:69]
	s_setprio 0
	s_barrier
	s_add_i32 s44, s82, s70
	v_lshl_add_u64 v[208:209], v[208:209], 0, s[56:57]
	s_mov_b32 m0, s44
	ds_read_b128 v[180:183], v145 offset:49152
	ds_read_b128 v[184:187], v145 offset:50176
	ds_read_b128 v[188:191], v145 offset:51200
	ds_read_b128 v[192:195], v145 offset:52224
	ds_read_b128 v[196:199], v145 offset:53248
	ds_read_b128 v[200:203], v145 offset:54272
	ds_read_b128 v[204:207], v145 offset:55296
	ds_read_b128 v[216:219], v145 offset:56320
	global_load_lds_dwordx4 v[208:209], off
	s_add_i32 m0, s44, 0x2000
	s_add_u32 s36, s36, 0x60080
	v_lshl_add_u64 v[208:209], v[220:221], 0, s[56:57]
	s_addc_u32 s37, s37, 0
	s_add_i32 s44, s83, s70
	global_load_lds_dwordx4 v[208:209], off
	s_mov_b32 m0, s44
	v_lshl_add_u64 v[208:209], s[36:37], 0, v[0:1]
	global_load_lds_dwordx4 v[208:209], off
	s_add_i32 m0, s44, 0x2000
	v_lshl_add_u64 v[208:209], s[36:37], 0, v[118:119]
	global_load_lds_dwordx4 v[208:209], off
	s_mov_b32 m0, s77
	v_lshl_add_u64 v[208:209], v[222:223], 0, s[56:57]
	global_load_lds_dwordx4 v[208:209], off
	s_mov_b32 m0, s79
	v_lshl_add_u64 v[208:209], v[224:225], 0, s[56:57]
	global_load_lds_dwordx4 v[208:209], off
	s_waitcnt vmcnt(8)
	s_waitcnt lgkmcnt(0)
	s_barrier
	s_setprio 1
	s_waitcnt lgkmcnt(0)
	v_mfma_f32_16x16x32_bf16 v[62:65], v[146:149], v[180:183], v[62:65]
	v_mfma_f32_16x16x32_bf16 v[58:61], v[154:157], v[180:183], v[58:61]
	v_mfma_f32_16x16x32_bf16 v[46:49], v[146:149], v[188:191], v[46:49]
	v_mfma_f32_16x16x32_bf16 v[42:45], v[154:157], v[188:191], v[42:45]
	v_mfma_f32_16x16x32_bf16 v[30:33], v[146:149], v[196:199], v[30:33]
	v_mfma_f32_16x16x32_bf16 v[26:29], v[154:157], v[196:199], v[26:29]
	v_mfma_f32_16x16x32_bf16 v[14:17], v[146:149], v[204:207], v[14:17]
	v_mfma_f32_16x16x32_bf16 v[10:13], v[154:157], v[204:207], v[10:13]
	v_mfma_f32_16x16x32_bf16 v[62:65], v[150:153], v[184:187], v[62:65]
	v_mfma_f32_16x16x32_bf16 v[58:61], v[158:161], v[184:187], v[58:61]
	v_mfma_f32_16x16x32_bf16 v[46:49], v[150:153], v[192:195], v[46:49]
	v_mfma_f32_16x16x32_bf16 v[42:45], v[158:161], v[192:195], v[42:45]
	v_mfma_f32_16x16x32_bf16 v[30:33], v[150:153], v[200:203], v[30:33]
	v_mfma_f32_16x16x32_bf16 v[26:29], v[158:161], v[200:203], v[26:29]
	v_mfma_f32_16x16x32_bf16 v[14:17], v[150:153], v[216:219], v[14:17]
	v_mfma_f32_16x16x32_bf16 v[10:13], v[158:161], v[216:219], v[10:13]
	s_setprio 0
	s_setprio 1
	v_mfma_f32_16x16x32_bf16 v[54:57], v[162:165], v[180:183], v[54:57]
	v_mfma_f32_16x16x32_bf16 v[50:53], v[172:175], v[180:183], v[50:53]
	v_mfma_f32_16x16x32_bf16 v[38:41], v[162:165], v[188:191], v[38:41]
	v_mfma_f32_16x16x32_bf16 v[34:37], v[172:175], v[188:191], v[34:37]
	v_mfma_f32_16x16x32_bf16 v[22:25], v[162:165], v[196:199], v[22:25]
	v_mfma_f32_16x16x32_bf16 v[18:21], v[172:175], v[196:199], v[18:21]
	v_mfma_f32_16x16x32_bf16 v[6:9], v[162:165], v[204:207], v[6:9]
	v_mfma_f32_16x16x32_bf16 v[2:5], v[172:175], v[204:207], v[2:5]
	v_mfma_f32_16x16x32_bf16 v[54:57], v[168:171], v[184:187], v[54:57]
	v_mfma_f32_16x16x32_bf16 v[50:53], v[176:179], v[184:187], v[50:53]
	v_mfma_f32_16x16x32_bf16 v[38:41], v[168:171], v[192:195], v[38:41]
	v_mfma_f32_16x16x32_bf16 v[34:37], v[176:179], v[192:195], v[34:37]
	v_mfma_f32_16x16x32_bf16 v[22:25], v[168:171], v[200:203], v[22:25]
	v_mfma_f32_16x16x32_bf16 v[18:21], v[176:179], v[200:203], v[18:21]
	v_mfma_f32_16x16x32_bf16 v[6:9], v[168:171], v[216:219], v[6:9]
	v_mfma_f32_16x16x32_bf16 v[2:5], v[176:179], v[216:219], v[2:5]
	s_setprio 0
	s_barrier
	s_add_i32 s59, s59, 2
	s_add_u32 s34, s34, 0x100
	s_addc_u32 s35, s35, 0
	s_cmp_gt_u32 s59, 21
	s_cbranch_scc0 .LBB0_1525
	s_add_u32 s34, s8, 0xffffff00
	s_addc_u32 s35, s9, -1
	s_and_b64 vcc, exec, s[42:43]
	s_cbranch_vccnz .LBB0_1528
	v_mov_b32_e32 v2, 0
	s_mov_b32 s16, s80
	s_mov_b32 s47, s81
	s_mov_b64 s[26:27], s[30:31]
	s_mov_b32 s68, s58
	v_mov_b32_e32 v3, v2
	v_mov_b32_e32 v4, v2
	v_mov_b32_e32 v5, v2
	v_mov_b32_e32 v6, v2
	v_mov_b32_e32 v7, v2
	v_mov_b32_e32 v8, v2
	v_mov_b32_e32 v9, v2
	v_mov_b32_e32 v18, v2
	v_mov_b32_e32 v19, v2
	v_mov_b32_e32 v20, v2
	v_mov_b32_e32 v21, v2
	v_mov_b32_e32 v22, v2
	v_mov_b32_e32 v23, v2
	v_mov_b32_e32 v24, v2
	v_mov_b32_e32 v25, v2
	v_mov_b32_e32 v34, v2
	v_mov_b32_e32 v35, v2
	v_mov_b32_e32 v36, v2
	v_mov_b32_e32 v37, v2
	v_mov_b32_e32 v38, v2
	v_mov_b32_e32 v39, v2
	v_mov_b32_e32 v40, v2
	v_mov_b32_e32 v41, v2
	v_mov_b32_e32 v50, v2
	v_mov_b32_e32 v51, v2
	v_mov_b32_e32 v52, v2
	v_mov_b32_e32 v53, v2
	v_mov_b32_e32 v54, v2
	v_mov_b32_e32 v55, v2
	v_mov_b32_e32 v56, v2
	v_mov_b32_e32 v57, v2
	v_mov_b32_e32 v10, v2
	v_mov_b32_e32 v11, v2
	v_mov_b32_e32 v12, v2
	v_mov_b32_e32 v13, v2
	v_mov_b32_e32 v14, v2
	v_mov_b32_e32 v15, v2
	v_mov_b32_e32 v16, v2
	v_mov_b32_e32 v17, v2
	v_mov_b32_e32 v26, v2
	v_mov_b32_e32 v27, v2
	v_mov_b32_e32 v28, v2
	v_mov_b32_e32 v29, v2
	v_mov_b32_e32 v30, v2
	v_mov_b32_e32 v31, v2
	v_mov_b32_e32 v32, v2
	v_mov_b32_e32 v33, v2
	v_mov_b32_e32 v42, v2
	v_mov_b32_e32 v43, v2
	v_mov_b32_e32 v44, v2
	v_mov_b32_e32 v45, v2
	v_mov_b32_e32 v46, v2
	v_mov_b32_e32 v47, v2
	v_mov_b32_e32 v48, v2
	v_mov_b32_e32 v49, v2
	v_mov_b32_e32 v58, v2
	v_mov_b32_e32 v59, v2
	v_mov_b32_e32 v60, v2
	v_mov_b32_e32 v61, v2
	v_mov_b32_e32 v62, v2
	v_mov_b32_e32 v63, v2
	v_mov_b32_e32 v64, v2
	v_mov_b32_e32 v65, v2
	v_mov_b32_e32 v66, v2
	v_mov_b32_e32 v67, v2
	v_mov_b32_e32 v68, v2
	v_mov_b32_e32 v69, v2
	v_mov_b32_e32 v70, v2
	v_mov_b32_e32 v71, v2
	v_mov_b32_e32 v72, v2
	v_mov_b32_e32 v73, v2
	v_mov_b32_e32 v82, v2
	v_mov_b32_e32 v83, v2
	v_mov_b32_e32 v84, v2
	v_mov_b32_e32 v85, v2
	v_mov_b32_e32 v86, v2
	v_mov_b32_e32 v87, v2
	v_mov_b32_e32 v88, v2
	v_mov_b32_e32 v89, v2
	v_mov_b32_e32 v98, v2
	v_mov_b32_e32 v99, v2
	v_mov_b32_e32 v100, v2
	v_mov_b32_e32 v101, v2
	v_mov_b32_e32 v102, v2
	v_mov_b32_e32 v103, v2
	v_mov_b32_e32 v104, v2
	v_mov_b32_e32 v105, v2
	v_mov_b32_e32 v114, v2
	v_mov_b32_e32 v115, v2
	v_mov_b32_e32 v116, v2
	v_mov_b32_e32 v117, v2
	v_mov_b32_e32 v122, v2
	v_mov_b32_e32 v123, v2
	v_mov_b32_e32 v124, v2
	v_mov_b32_e32 v125, v2
	v_mov_b32_e32 v74, v2
	v_mov_b32_e32 v75, v2
	v_mov_b32_e32 v76, v2
	v_mov_b32_e32 v77, v2
	v_mov_b32_e32 v78, v2
	v_mov_b32_e32 v79, v2
	v_mov_b32_e32 v80, v2
	v_mov_b32_e32 v81, v2
	v_mov_b32_e32 v90, v2
	v_mov_b32_e32 v91, v2
	v_mov_b32_e32 v92, v2
	v_mov_b32_e32 v93, v2
	v_mov_b32_e32 v94, v2
	v_mov_b32_e32 v95, v2
	v_mov_b32_e32 v96, v2
	v_mov_b32_e32 v97, v2
	v_mov_b32_e32 v106, v2
	v_mov_b32_e32 v107, v2
	v_mov_b32_e32 v108, v2
	v_mov_b32_e32 v109, v2
	v_mov_b32_e32 v110, v2
	v_mov_b32_e32 v111, v2
	v_mov_b32_e32 v112, v2
	v_mov_b32_e32 v113, v2
	v_mov_b32_e32 v130, v2
	v_mov_b32_e32 v131, v2
	v_mov_b32_e32 v132, v2
	v_mov_b32_e32 v133, v2
	v_mov_b32_e32 v134, v2
	v_mov_b32_e32 v135, v2
	v_mov_b32_e32 v136, v2
	v_mov_b32_e32 v137, v2
	s_andn2_b64 vcc, exec, s[40:41]
	s_cbranch_vccnz .LBB0_1529
	s_branch .LBB0_1531

.LBB0_1623:
	s_add_u32 s36, s26, s34
	s_addc_u32 s37, s27, s35
	s_add_u32 s36, s36, 0x100
	s_addc_u32 s37, s37, 0
	s_add_u32 s80, s8, s34
	s_addc_u32 s81, s9, s35
	s_add_i32 s82, 0, 0x10000
	s_cmpk_eq_i32 s34, 0xb00
	s_cselect_b32 s43, s31, s37
	s_cselect_b32 s42, s30, s36
	s_cselect_b32 s37, s29, s81
	s_cselect_b32 s36, s28, s80
	s_add_i32 s83, 0, 0x14000
	v_add_u32_e32 v158, s82, v144
	v_add_u32_e32 v167, s83, v144
	ds_read_b128 v[146:149], v158
	ds_read_b128 v[150:153], v158 offset:1024
	ds_read_b128 v[154:157], v158 offset:2048
	ds_read_b128 v[158:161], v158 offset:3072
	ds_read_b128 v[162:165], v167
	ds_read_b128 v[168:171], v167 offset:1024
	ds_read_b128 v[172:175], v167 offset:2048
	ds_read_b128 v[176:179], v167 offset:3072
	v_lshl_add_u64 v[208:209], v[142:143], 0, s[34:35]
	s_add_i32 m0, s4, 0xc000
	ds_read_b128 v[180:183], v145
	ds_read_b128 v[184:187], v145 offset:1024
	ds_read_b128 v[188:191], v145 offset:2048
	ds_read_b128 v[192:195], v145 offset:3072
	ds_read_b128 v[196:199], v145 offset:4096
	ds_read_b128 v[200:203], v145 offset:5120
	ds_read_b128 v[204:207], v145 offset:6144
	ds_read_b128 v[216:219], v145 offset:7168
	global_load_lds_dwordx4 v[208:209], off
	s_add_i32 m0, s4, 0xe000
	v_lshl_add_u64 v[208:209], v[140:141], 0, s[34:35]
	global_load_lds_dwordx4 v[208:209], off
	s_waitcnt vmcnt(8)
	s_waitcnt lgkmcnt(0)
	s_barrier
	s_setprio 1
	s_waitcnt lgkmcnt(0)
	v_mfma_f32_16x16x32_bf16 v[134:137], v[146:149], v[180:183], v[134:137]
	v_mfma_f32_16x16x32_bf16 v[130:133], v[154:157], v[180:183], v[130:133]
	v_mfma_f32_16x16x32_bf16 v[110:113], v[146:149], v[188:191], v[110:113]
	v_mfma_f32_16x16x32_bf16 v[106:109], v[154:157], v[188:191], v[106:109]
	v_mfma_f32_16x16x32_bf16 v[94:97], v[146:149], v[196:199], v[94:97]
	v_mfma_f32_16x16x32_bf16 v[90:93], v[154:157], v[196:199], v[90:93]
	v_mfma_f32_16x16x32_bf16 v[78:81], v[146:149], v[204:207], v[78:81]
	v_mfma_f32_16x16x32_bf16 v[74:77], v[154:157], v[204:207], v[74:77]
	v_mfma_f32_16x16x32_bf16 v[134:137], v[150:153], v[184:187], v[134:137]
	v_mfma_f32_16x16x32_bf16 v[130:133], v[158:161], v[184:187], v[130:133]
	v_mfma_f32_16x16x32_bf16 v[110:113], v[150:153], v[192:195], v[110:113]
	v_mfma_f32_16x16x32_bf16 v[106:109], v[158:161], v[192:195], v[106:109]
	v_mfma_f32_16x16x32_bf16 v[94:97], v[150:153], v[200:203], v[94:97]
	v_mfma_f32_16x16x32_bf16 v[90:93], v[158:161], v[200:203], v[90:93]
	v_mfma_f32_16x16x32_bf16 v[78:81], v[150:153], v[216:219], v[78:81]
	v_mfma_f32_16x16x32_bf16 v[74:77], v[158:161], v[216:219], v[74:77]
	s_setprio 0
	s_setprio 1
	v_mfma_f32_16x16x32_bf16 v[122:125], v[162:165], v[180:183], v[122:125]
	v_mfma_f32_16x16x32_bf16 v[114:117], v[172:175], v[180:183], v[114:117]
	v_mfma_f32_16x16x32_bf16 v[102:105], v[162:165], v[188:191], v[102:105]
	v_mfma_f32_16x16x32_bf16 v[98:101], v[172:175], v[188:191], v[98:101]
	v_mfma_f32_16x16x32_bf16 v[86:89], v[162:165], v[196:199], v[86:89]
	v_mfma_f32_16x16x32_bf16 v[82:85], v[172:175], v[196:199], v[82:85]
	v_mfma_f32_16x16x32_bf16 v[70:73], v[162:165], v[204:207], v[70:73]
	v_mfma_f32_16x16x32_bf16 v[66:69], v[172:175], v[204:207], v[66:69]
	v_mfma_f32_16x16x32_bf16 v[122:125], v[168:171], v[184:187], v[122:125]
	v_mfma_f32_16x16x32_bf16 v[114:117], v[176:179], v[184:187], v[114:117]
	v_mfma_f32_16x16x32_bf16 v[102:105], v[168:171], v[192:195], v[102:105]
	v_mfma_f32_16x16x32_bf16 v[98:101], v[176:179], v[192:195], v[98:101]
	v_mfma_f32_16x16x32_bf16 v[86:89], v[168:171], v[200:203], v[86:89]
	v_mfma_f32_16x16x32_bf16 v[82:85], v[176:179], v[200:203], v[82:85]
	v_mfma_f32_16x16x32_bf16 v[70:73], v[168:171], v[216:219], v[70:73]
	v_mfma_f32_16x16x32_bf16 v[66:69], v[176:179], v[216:219], v[66:69]
	s_setprio 0
	s_barrier
	s_add_i32 s80, s82, s53
	v_lshl_add_u64 v[208:209], s[36:37], 0, v[0:1]
	s_mov_b32 m0, s80
	ds_read_b128 v[180:183], v145 offset:16384
	ds_read_b128 v[184:187], v145 offset:17408
	ds_read_b128 v[188:191], v145 offset:18432
	ds_read_b128 v[192:195], v145 offset:19456
	ds_read_b128 v[196:199], v145 offset:20480
	ds_read_b128 v[200:203], v145 offset:21504
	ds_read_b128 v[204:207], v145 offset:22528
	ds_read_b128 v[216:219], v145 offset:23552
	global_load_lds_dwordx4 v[208:209], off
	s_add_i32 m0, s80, 0x2000
	s_add_u32 s80, s36, 0x60000
	v_lshl_add_u64 v[220:221], s[36:37], 0, v[118:119]
	s_addc_u32 s81, s37, 0
	s_add_i32 s82, s83, s53
	global_load_lds_dwordx4 v[220:221], off
	v_lshl_add_u64 v[222:223], s[80:81], 0, v[0:1]
	s_mov_b32 m0, s82
	v_lshl_add_u64 v[224:225], s[42:43], 0, v[120:121]
	global_load_lds_dwordx4 v[222:223], off
	s_add_i32 m0, s82, 0x2000
	v_lshl_add_u64 v[222:223], s[80:81], 0, v[118:119]
	global_load_lds_dwordx4 v[222:223], off
	s_mov_b32 m0, s4
	v_lshl_add_u64 v[222:223], s[42:43], 0, v[126:127]
	global_load_lds_dwordx4 v[222:223], off
	s_mov_b32 m0, s33
	s_nop 0
	global_load_lds_dwordx4 v[224:225], off
	s_waitcnt vmcnt(8)
	s_waitcnt lgkmcnt(0)
	s_barrier
	s_setprio 1
	s_waitcnt lgkmcnt(0)
	v_mfma_f32_16x16x32_bf16 v[62:65], v[146:149], v[180:183], v[62:65]
	v_mfma_f32_16x16x32_bf16 v[58:61], v[154:157], v[180:183], v[58:61]
	v_mfma_f32_16x16x32_bf16 v[46:49], v[146:149], v[188:191], v[46:49]
	v_mfma_f32_16x16x32_bf16 v[42:45], v[154:157], v[188:191], v[42:45]
	v_mfma_f32_16x16x32_bf16 v[30:33], v[146:149], v[196:199], v[30:33]
	v_mfma_f32_16x16x32_bf16 v[26:29], v[154:157], v[196:199], v[26:29]
	v_mfma_f32_16x16x32_bf16 v[14:17], v[146:149], v[204:207], v[14:17]
	v_mfma_f32_16x16x32_bf16 v[10:13], v[154:157], v[204:207], v[10:13]
	v_mfma_f32_16x16x32_bf16 v[62:65], v[150:153], v[184:187], v[62:65]
	v_mfma_f32_16x16x32_bf16 v[58:61], v[158:161], v[184:187], v[58:61]
	v_mfma_f32_16x16x32_bf16 v[46:49], v[150:153], v[192:195], v[46:49]
	v_mfma_f32_16x16x32_bf16 v[42:45], v[158:161], v[192:195], v[42:45]
	v_mfma_f32_16x16x32_bf16 v[30:33], v[150:153], v[200:203], v[30:33]
	v_mfma_f32_16x16x32_bf16 v[26:29], v[158:161], v[200:203], v[26:29]
	v_mfma_f32_16x16x32_bf16 v[14:17], v[150:153], v[216:219], v[14:17]
	v_mfma_f32_16x16x32_bf16 v[10:13], v[158:161], v[216:219], v[10:13]
	s_setprio 0
	s_setprio 1
	v_mfma_f32_16x16x32_bf16 v[54:57], v[162:165], v[180:183], v[54:57]
	v_mfma_f32_16x16x32_bf16 v[50:53], v[172:175], v[180:183], v[50:53]
	v_mfma_f32_16x16x32_bf16 v[38:41], v[162:165], v[188:191], v[38:41]
	v_mfma_f32_16x16x32_bf16 v[34:37], v[172:175], v[188:191], v[34:37]
	v_mfma_f32_16x16x32_bf16 v[22:25], v[162:165], v[196:199], v[22:25]
	v_mfma_f32_16x16x32_bf16 v[18:21], v[172:175], v[196:199], v[18:21]
	v_mfma_f32_16x16x32_bf16 v[6:9], v[162:165], v[204:207], v[6:9]
	v_mfma_f32_16x16x32_bf16 v[2:5], v[172:175], v[204:207], v[2:5]
	v_mfma_f32_16x16x32_bf16 v[54:57], v[168:171], v[184:187], v[54:57]
	v_mfma_f32_16x16x32_bf16 v[50:53], v[176:179], v[184:187], v[50:53]
	v_mfma_f32_16x16x32_bf16 v[38:41], v[168:171], v[192:195], v[38:41]
	v_mfma_f32_16x16x32_bf16 v[34:37], v[176:179], v[192:195], v[34:37]
	v_mfma_f32_16x16x32_bf16 v[22:25], v[168:171], v[200:203], v[22:25]
	v_mfma_f32_16x16x32_bf16 v[18:21], v[176:179], v[200:203], v[18:21]
	v_mfma_f32_16x16x32_bf16 v[6:9], v[168:171], v[216:219], v[6:9]
	v_mfma_f32_16x16x32_bf16 v[2:5], v[176:179], v[216:219], v[2:5]
	s_setprio 0
	s_barrier
	s_add_i32 s80, 0, 0x18000
	s_add_i32 s81, 0, 0x1c000
	v_add_u32_e32 v158, s80, v144
	v_add_u32_e32 v167, s81, v144
	ds_read_b128 v[146:149], v158
	ds_read_b128 v[150:153], v158 offset:1024
	ds_read_b128 v[154:157], v158 offset:2048
	ds_read_b128 v[158:161], v158 offset:3072
	ds_read_b128 v[162:165], v167
	ds_read_b128 v[168:171], v167 offset:1024
	ds_read_b128 v[172:175], v167 offset:2048
	ds_read_b128 v[176:179], v167 offset:3072
	s_add_u32 s42, s42, 0x60000
	s_addc_u32 s43, s43, 0
	s_mov_b32 m0, s62
	v_lshl_add_u64 v[242:243], s[42:43], 0, v[126:127]
	ds_read_b128 v[180:183], v145 offset:32768
	ds_read_b128 v[184:187], v145 offset:33792
	ds_read_b128 v[188:191], v145 offset:34816
	ds_read_b128 v[192:195], v145 offset:35840
	ds_read_b128 v[196:199], v145 offset:36864
	ds_read_b128 v[200:203], v145 offset:37888
	ds_read_b128 v[204:207], v145 offset:38912
	ds_read_b128 v[216:219], v145 offset:39936
	global_load_lds_dwordx4 v[242:243], off
	s_mov_b32 m0, s63
	v_lshl_add_u64 v[242:243], s[42:43], 0, v[120:121]
	global_load_lds_dwordx4 v[242:243], off
	s_waitcnt vmcnt(8)
	s_waitcnt lgkmcnt(0)
	s_barrier
	s_setprio 1
	s_waitcnt lgkmcnt(0)
	v_mfma_f32_16x16x32_bf16 v[134:137], v[146:149], v[180:183], v[134:137]
	v_mfma_f32_16x16x32_bf16 v[130:133], v[154:157], v[180:183], v[130:133]
	v_mfma_f32_16x16x32_bf16 v[110:113], v[146:149], v[188:191], v[110:113]
	v_mfma_f32_16x16x32_bf16 v[106:109], v[154:157], v[188:191], v[106:109]
	v_mfma_f32_16x16x32_bf16 v[94:97], v[146:149], v[196:199], v[94:97]
	v_mfma_f32_16x16x32_bf16 v[90:93], v[154:157], v[196:199], v[90:93]
	v_mfma_f32_16x16x32_bf16 v[78:81], v[146:149], v[204:207], v[78:81]
	v_mfma_f32_16x16x32_bf16 v[74:77], v[154:157], v[204:207], v[74:77]
	v_mfma_f32_16x16x32_bf16 v[134:137], v[150:153], v[184:187], v[134:137]
	v_mfma_f32_16x16x32_bf16 v[130:133], v[158:161], v[184:187], v[130:133]
	v_mfma_f32_16x16x32_bf16 v[110:113], v[150:153], v[192:195], v[110:113]
	v_mfma_f32_16x16x32_bf16 v[106:109], v[158:161], v[192:195], v[106:109]
	v_mfma_f32_16x16x32_bf16 v[94:97], v[150:153], v[200:203], v[94:97]
	v_mfma_f32_16x16x32_bf16 v[90:93], v[158:161], v[200:203], v[90:93]
	v_mfma_f32_16x16x32_bf16 v[78:81], v[150:153], v[216:219], v[78:81]
	v_mfma_f32_16x16x32_bf16 v[74:77], v[158:161], v[216:219], v[74:77]
	s_setprio 0
	s_setprio 1
	v_mfma_f32_16x16x32_bf16 v[122:125], v[162:165], v[180:183], v[122:125]
	v_mfma_f32_16x16x32_bf16 v[114:117], v[172:175], v[180:183], v[114:117]
	v_mfma_f32_16x16x32_bf16 v[102:105], v[162:165], v[188:191], v[102:105]
	v_mfma_f32_16x16x32_bf16 v[98:101], v[172:175], v[188:191], v[98:101]
	v_mfma_f32_16x16x32_bf16 v[86:89], v[162:165], v[196:199], v[86:89]
	v_mfma_f32_16x16x32_bf16 v[82:85], v[172:175], v[196:199], v[82:85]
	v_mfma_f32_16x16x32_bf16 v[70:73], v[162:165], v[204:207], v[70:73]
	v_mfma_f32_16x16x32_bf16 v[66:69], v[172:175], v[204:207], v[66:69]
	v_mfma_f32_16x16x32_bf16 v[122:125], v[168:171], v[184:187], v[122:125]
	v_mfma_f32_16x16x32_bf16 v[114:117], v[176:179], v[184:187], v[114:117]
	v_mfma_f32_16x16x32_bf16 v[102:105], v[168:171], v[192:195], v[102:105]
	v_mfma_f32_16x16x32_bf16 v[98:101], v[176:179], v[192:195], v[98:101]
	v_mfma_f32_16x16x32_bf16 v[86:89], v[168:171], v[200:203], v[86:89]
	v_mfma_f32_16x16x32_bf16 v[82:85], v[176:179], v[200:203], v[82:85]
	v_mfma_f32_16x16x32_bf16 v[70:73], v[168:171], v[216:219], v[70:73]
	v_mfma_f32_16x16x32_bf16 v[66:69], v[176:179], v[216:219], v[66:69]
	s_setprio 0
	s_barrier
	s_add_i32 s42, s80, s53
	v_lshl_add_u64 v[208:209], v[208:209], 0, s[56:57]
	s_mov_b32 m0, s42
	ds_read_b128 v[180:183], v145 offset:49152
	ds_read_b128 v[184:187], v145 offset:50176
	ds_read_b128 v[188:191], v145 offset:51200
	ds_read_b128 v[192:195], v145 offset:52224
	ds_read_b128 v[196:199], v145 offset:53248
	ds_read_b128 v[200:203], v145 offset:54272
	ds_read_b128 v[204:207], v145 offset:55296
	ds_read_b128 v[216:219], v145 offset:56320
	global_load_lds_dwordx4 v[208:209], off
	s_add_i32 m0, s42, 0x2000
	s_add_u32 s36, s36, 0x60080
	v_lshl_add_u64 v[208:209], v[220:221], 0, s[56:57]
	s_addc_u32 s37, s37, 0
	s_add_i32 s42, s81, s53
	global_load_lds_dwordx4 v[208:209], off
	s_mov_b32 m0, s42
	v_lshl_add_u64 v[208:209], s[36:37], 0, v[0:1]
	global_load_lds_dwordx4 v[208:209], off
	s_add_i32 m0, s42, 0x2000
	v_lshl_add_u64 v[208:209], s[36:37], 0, v[118:119]
	global_load_lds_dwordx4 v[208:209], off
	s_mov_b32 m0, s70
	v_lshl_add_u64 v[208:209], v[222:223], 0, s[56:57]
	global_load_lds_dwordx4 v[208:209], off
	s_mov_b32 m0, s71
	v_lshl_add_u64 v[208:209], v[224:225], 0, s[56:57]
	global_load_lds_dwordx4 v[208:209], off
	s_waitcnt vmcnt(8)
	s_waitcnt lgkmcnt(0)
	s_barrier
	s_setprio 1
	s_waitcnt lgkmcnt(0)
	v_mfma_f32_16x16x32_bf16 v[62:65], v[146:149], v[180:183], v[62:65]
	v_mfma_f32_16x16x32_bf16 v[58:61], v[154:157], v[180:183], v[58:61]
	v_mfma_f32_16x16x32_bf16 v[46:49], v[146:149], v[188:191], v[46:49]
	v_mfma_f32_16x16x32_bf16 v[42:45], v[154:157], v[188:191], v[42:45]
	v_mfma_f32_16x16x32_bf16 v[30:33], v[146:149], v[196:199], v[30:33]
	v_mfma_f32_16x16x32_bf16 v[26:29], v[154:157], v[196:199], v[26:29]
	v_mfma_f32_16x16x32_bf16 v[14:17], v[146:149], v[204:207], v[14:17]
	v_mfma_f32_16x16x32_bf16 v[10:13], v[154:157], v[204:207], v[10:13]
	v_mfma_f32_16x16x32_bf16 v[62:65], v[150:153], v[184:187], v[62:65]
	v_mfma_f32_16x16x32_bf16 v[58:61], v[158:161], v[184:187], v[58:61]
	v_mfma_f32_16x16x32_bf16 v[46:49], v[150:153], v[192:195], v[46:49]
	v_mfma_f32_16x16x32_bf16 v[42:45], v[158:161], v[192:195], v[42:45]
	v_mfma_f32_16x16x32_bf16 v[30:33], v[150:153], v[200:203], v[30:33]
	v_mfma_f32_16x16x32_bf16 v[26:29], v[158:161], v[200:203], v[26:29]
	v_mfma_f32_16x16x32_bf16 v[14:17], v[150:153], v[216:219], v[14:17]
	v_mfma_f32_16x16x32_bf16 v[10:13], v[158:161], v[216:219], v[10:13]
	s_setprio 0
	s_setprio 1
	v_mfma_f32_16x16x32_bf16 v[54:57], v[162:165], v[180:183], v[54:57]
	v_mfma_f32_16x16x32_bf16 v[50:53], v[172:175], v[180:183], v[50:53]
	v_mfma_f32_16x16x32_bf16 v[38:41], v[162:165], v[188:191], v[38:41]
	v_mfma_f32_16x16x32_bf16 v[34:37], v[172:175], v[188:191], v[34:37]
	v_mfma_f32_16x16x32_bf16 v[22:25], v[162:165], v[196:199], v[22:25]
	v_mfma_f32_16x16x32_bf16 v[18:21], v[172:175], v[196:199], v[18:21]
	v_mfma_f32_16x16x32_bf16 v[6:9], v[162:165], v[204:207], v[6:9]
	v_mfma_f32_16x16x32_bf16 v[2:5], v[172:175], v[204:207], v[2:5]
	v_mfma_f32_16x16x32_bf16 v[54:57], v[168:171], v[184:187], v[54:57]
	v_mfma_f32_16x16x32_bf16 v[50:53], v[176:179], v[184:187], v[50:53]
	v_mfma_f32_16x16x32_bf16 v[38:41], v[168:171], v[192:195], v[38:41]
	v_mfma_f32_16x16x32_bf16 v[34:37], v[176:179], v[192:195], v[34:37]
	v_mfma_f32_16x16x32_bf16 v[22:25], v[168:171], v[200:203], v[22:25]
	v_mfma_f32_16x16x32_bf16 v[18:21], v[176:179], v[200:203], v[18:21]
	v_mfma_f32_16x16x32_bf16 v[6:9], v[168:171], v[216:219], v[6:9]
	v_mfma_f32_16x16x32_bf16 v[2:5], v[176:179], v[216:219], v[2:5]
	s_setprio 0
	s_barrier
	s_add_i32 s59, s59, 2
	s_add_u32 s34, s34, 0x100
	s_addc_u32 s35, s35, 0
	s_cmp_gt_u32 s59, 21
	s_cbranch_scc0 .LBB0_1623
	s_add_u32 s34, s8, 0xffffff00
	s_addc_u32 s35, s9, -1
	s_and_b64 vcc, exec, s[40:41]
	s_cbranch_vccnz .LBB0_1626
	v_mov_b32_e32 v2, 0
	s_mov_b32 s16, s77
	s_mov_b32 s76, s79
	s_mov_b64 s[26:27], s[30:31]
	s_mov_b32 s68, s58
	v_mov_b32_e32 v3, v2
	v_mov_b32_e32 v4, v2
	v_mov_b32_e32 v5, v2
	v_mov_b32_e32 v6, v2
	v_mov_b32_e32 v7, v2
	v_mov_b32_e32 v8, v2
	v_mov_b32_e32 v9, v2
	v_mov_b32_e32 v18, v2
	v_mov_b32_e32 v19, v2
	v_mov_b32_e32 v20, v2
	v_mov_b32_e32 v21, v2
	v_mov_b32_e32 v22, v2
	v_mov_b32_e32 v23, v2
	v_mov_b32_e32 v24, v2
	v_mov_b32_e32 v25, v2
	v_mov_b32_e32 v34, v2
	v_mov_b32_e32 v35, v2
	v_mov_b32_e32 v36, v2
	v_mov_b32_e32 v37, v2
	v_mov_b32_e32 v38, v2
	v_mov_b32_e32 v39, v2
	v_mov_b32_e32 v40, v2
	v_mov_b32_e32 v41, v2
	v_mov_b32_e32 v50, v2
	v_mov_b32_e32 v51, v2
	v_mov_b32_e32 v52, v2
	v_mov_b32_e32 v53, v2
	v_mov_b32_e32 v54, v2
	v_mov_b32_e32 v55, v2
	v_mov_b32_e32 v56, v2
	v_mov_b32_e32 v57, v2
	v_mov_b32_e32 v10, v2
	v_mov_b32_e32 v11, v2
	v_mov_b32_e32 v12, v2
	v_mov_b32_e32 v13, v2
	v_mov_b32_e32 v14, v2
	v_mov_b32_e32 v15, v2
	v_mov_b32_e32 v16, v2
	v_mov_b32_e32 v17, v2
	v_mov_b32_e32 v26, v2
	v_mov_b32_e32 v27, v2
	v_mov_b32_e32 v28, v2
	v_mov_b32_e32 v29, v2
	v_mov_b32_e32 v30, v2
	v_mov_b32_e32 v31, v2
	v_mov_b32_e32 v32, v2
	v_mov_b32_e32 v33, v2
	v_mov_b32_e32 v42, v2
	v_mov_b32_e32 v43, v2
	v_mov_b32_e32 v44, v2
	v_mov_b32_e32 v45, v2
	v_mov_b32_e32 v46, v2
	v_mov_b32_e32 v47, v2
	v_mov_b32_e32 v48, v2
	v_mov_b32_e32 v49, v2
	v_mov_b32_e32 v58, v2
	v_mov_b32_e32 v59, v2
	v_mov_b32_e32 v60, v2
	v_mov_b32_e32 v61, v2
	v_mov_b32_e32 v62, v2
	v_mov_b32_e32 v63, v2
	v_mov_b32_e32 v64, v2
	v_mov_b32_e32 v65, v2
	v_mov_b32_e32 v66, v2
	v_mov_b32_e32 v67, v2
	v_mov_b32_e32 v68, v2
	v_mov_b32_e32 v69, v2
	v_mov_b32_e32 v70, v2
	v_mov_b32_e32 v71, v2
	v_mov_b32_e32 v72, v2
	v_mov_b32_e32 v73, v2
	v_mov_b32_e32 v82, v2
	v_mov_b32_e32 v83, v2
	v_mov_b32_e32 v84, v2
	v_mov_b32_e32 v85, v2
	v_mov_b32_e32 v86, v2
	v_mov_b32_e32 v87, v2
	v_mov_b32_e32 v88, v2
	v_mov_b32_e32 v89, v2
	v_mov_b32_e32 v98, v2
	v_mov_b32_e32 v99, v2
	v_mov_b32_e32 v100, v2
	v_mov_b32_e32 v101, v2
	v_mov_b32_e32 v102, v2
	v_mov_b32_e32 v103, v2
	v_mov_b32_e32 v104, v2
	v_mov_b32_e32 v105, v2
	v_mov_b32_e32 v114, v2
	v_mov_b32_e32 v115, v2
	v_mov_b32_e32 v116, v2
	v_mov_b32_e32 v117, v2
	v_mov_b32_e32 v122, v2
	v_mov_b32_e32 v123, v2
	v_mov_b32_e32 v124, v2
	v_mov_b32_e32 v125, v2
	v_mov_b32_e32 v74, v2
	v_mov_b32_e32 v75, v2
	v_mov_b32_e32 v76, v2
	v_mov_b32_e32 v77, v2
	v_mov_b32_e32 v78, v2
	v_mov_b32_e32 v79, v2
	v_mov_b32_e32 v80, v2
	v_mov_b32_e32 v81, v2
	v_mov_b32_e32 v90, v2
	v_mov_b32_e32 v91, v2
	v_mov_b32_e32 v92, v2
	v_mov_b32_e32 v93, v2
	v_mov_b32_e32 v94, v2
	v_mov_b32_e32 v95, v2
	v_mov_b32_e32 v96, v2
	v_mov_b32_e32 v97, v2
	v_mov_b32_e32 v106, v2
	v_mov_b32_e32 v107, v2
	v_mov_b32_e32 v108, v2
	v_mov_b32_e32 v109, v2
	v_mov_b32_e32 v110, v2
	v_mov_b32_e32 v111, v2
	v_mov_b32_e32 v112, v2
	v_mov_b32_e32 v113, v2
	v_mov_b32_e32 v130, v2
	v_mov_b32_e32 v131, v2
	v_mov_b32_e32 v132, v2
	v_mov_b32_e32 v133, v2
	v_mov_b32_e32 v134, v2
	v_mov_b32_e32 v135, v2
	v_mov_b32_e32 v136, v2
	v_mov_b32_e32 v137, v2
	s_andn2_b64 vcc, exec, s[38:39]
	s_cbranch_vccnz .LBB0_1627
	s_branch .LBB0_1628

.LBB0_1783:
	s_add_u32 s28, s6, 0xfffc0080
	s_addc_u32 s29, s7, -1
	s_add_i32 s53, 0, 0x10000
	s_cmp_eq_u32 s41, 12
	s_cselect_b32 s31, s8, s29
	s_cselect_b32 s30, s9, s28
	s_cselect_b32 s29, s21, s40
	s_cselect_b32 s28, s23, s33
	s_add_i32 s62, 0, 0x14000
	v_add_u32_e32 v142, s53, v181
	v_add_u32_e32 v168, s62, v181
	ds_read_b128 v[130:133], v142
	ds_read_b128 v[134:137], v142 offset:1024
	ds_read_b128 v[138:141], v142 offset:2048
	ds_read_b128 v[142:145], v142 offset:3072
	ds_read_b128 v[146:149], v168
	ds_read_b128 v[150:153], v168 offset:1024
	ds_read_b128 v[154:157], v168 offset:2048
	ds_read_b128 v[168:171], v168 offset:3072
	v_lshl_add_u64 v[176:177], s[6:7], 0, v[166:167]
	s_add_i32 m0, s37, 0xc000
	ds_read_b128 v[172:175], v183
	ds_read_b128 v[184:187], v183 offset:1024
	ds_read_b128 v[188:191], v183 offset:2048
	ds_read_b128 v[192:195], v183 offset:3072
	ds_read_b128 v[196:199], v183 offset:4096
	ds_read_b128 v[200:203], v183 offset:5120
	ds_read_b128 v[204:207], v183 offset:6144
	ds_read_b128 v[216:219], v183 offset:7168
	global_load_lds_dwordx4 v[176:177], off
	s_add_i32 m0, s37, 0xe000
	v_lshl_add_u64 v[176:177], s[6:7], 0, v[164:165]
	global_load_lds_dwordx4 v[176:177], off
	s_waitcnt vmcnt(8)
	s_waitcnt lgkmcnt(0)
	s_barrier
	s_setprio 1
	s_waitcnt lgkmcnt(0)
	v_mfma_f32_16x16x32_bf16 v[126:129], v[130:133], v[172:175], v[126:129]
	v_mfma_f32_16x16x32_bf16 v[122:125], v[138:141], v[172:175], v[122:125]
	v_mfma_f32_16x16x32_bf16 v[114:117], v[130:133], v[188:191], v[114:117]
	v_mfma_f32_16x16x32_bf16 v[106:109], v[138:141], v[188:191], v[106:109]
	v_mfma_f32_16x16x32_bf16 v[98:101], v[130:133], v[196:199], v[98:101]
	v_mfma_f32_16x16x32_bf16 v[90:93], v[138:141], v[196:199], v[90:93]
	v_mfma_f32_16x16x32_bf16 v[82:85], v[130:133], v[204:207], v[82:85]
	v_mfma_f32_16x16x32_bf16 v[74:77], v[138:141], v[204:207], v[74:77]
	v_mfma_f32_16x16x32_bf16 v[126:129], v[134:137], v[184:187], v[126:129]
	v_mfma_f32_16x16x32_bf16 v[122:125], v[142:145], v[184:187], v[122:125]
	v_mfma_f32_16x16x32_bf16 v[114:117], v[134:137], v[192:195], v[114:117]
	v_mfma_f32_16x16x32_bf16 v[106:109], v[142:145], v[192:195], v[106:109]
	v_mfma_f32_16x16x32_bf16 v[98:101], v[134:137], v[200:203], v[98:101]
	v_mfma_f32_16x16x32_bf16 v[90:93], v[142:145], v[200:203], v[90:93]
	v_mfma_f32_16x16x32_bf16 v[82:85], v[134:137], v[216:219], v[82:85]
	v_mfma_f32_16x16x32_bf16 v[74:77], v[142:145], v[216:219], v[74:77]
	s_setprio 0
	s_setprio 1
	v_mfma_f32_16x16x32_bf16 v[118:121], v[146:149], v[172:175], v[118:121]
	v_mfma_f32_16x16x32_bf16 v[110:113], v[154:157], v[172:175], v[110:113]
	v_mfma_f32_16x16x32_bf16 v[102:105], v[146:149], v[188:191], v[102:105]
	v_mfma_f32_16x16x32_bf16 v[94:97], v[154:157], v[188:191], v[94:97]
	v_mfma_f32_16x16x32_bf16 v[86:89], v[146:149], v[196:199], v[86:89]
	v_mfma_f32_16x16x32_bf16 v[78:81], v[154:157], v[196:199], v[78:81]
	v_mfma_f32_16x16x32_bf16 v[70:73], v[146:149], v[204:207], v[70:73]
	v_mfma_f32_16x16x32_bf16 v[66:69], v[154:157], v[204:207], v[66:69]
	v_mfma_f32_16x16x32_bf16 v[118:121], v[150:153], v[184:187], v[118:121]
	v_mfma_f32_16x16x32_bf16 v[110:113], v[168:171], v[184:187], v[110:113]
	v_mfma_f32_16x16x32_bf16 v[102:105], v[150:153], v[192:195], v[102:105]
	v_mfma_f32_16x16x32_bf16 v[94:97], v[168:171], v[192:195], v[94:97]
	v_mfma_f32_16x16x32_bf16 v[86:89], v[150:153], v[200:203], v[86:89]
	v_mfma_f32_16x16x32_bf16 v[78:81], v[168:171], v[200:203], v[78:81]
	v_mfma_f32_16x16x32_bf16 v[70:73], v[150:153], v[216:219], v[70:73]
	v_mfma_f32_16x16x32_bf16 v[66:69], v[168:171], v[216:219], v[66:69]
	s_setprio 0
	s_barrier
	s_add_i32 s53, s53, s36
	v_lshl_add_u64 v[176:177], s[28:29], 0, v[162:163]
	s_mov_b32 m0, s53
	ds_read_b128 v[172:175], v183 offset:16384
	ds_read_b128 v[184:187], v183 offset:17408
	ds_read_b128 v[188:191], v183 offset:18432
	ds_read_b128 v[192:195], v183 offset:19456
	ds_read_b128 v[196:199], v183 offset:20480
	ds_read_b128 v[200:203], v183 offset:21504
	ds_read_b128 v[204:207], v183 offset:22528
	ds_read_b128 v[216:219], v183 offset:23552
	global_load_lds_dwordx4 v[176:177], off
	s_add_i32 m0, s53, 0x2000
	s_add_u32 s58, s28, 0x40000
	v_lshl_add_u64 v[208:209], s[28:29], 0, v[158:159]
	s_addc_u32 s59, s29, 0
	s_add_i32 s53, s62, s36
	global_load_lds_dwordx4 v[208:209], off
	v_lshl_add_u64 v[220:221], s[58:59], 0, v[162:163]
	s_mov_b32 m0, s53
	v_lshl_add_u64 v[222:223], s[30:31], 0, v[160:161]
	global_load_lds_dwordx4 v[220:221], off
	s_add_i32 m0, s53, 0x2000
	v_lshl_add_u64 v[220:221], s[58:59], 0, v[158:159]
	global_load_lds_dwordx4 v[220:221], off
	s_mov_b32 m0, s37
	v_lshl_add_u64 v[220:221], s[30:31], 0, v[0:1]
	global_load_lds_dwordx4 v[220:221], off
	s_mov_b32 m0, s44
	s_nop 0
	global_load_lds_dwordx4 v[222:223], off
	s_waitcnt vmcnt(8)
	s_waitcnt lgkmcnt(0)
	s_barrier
	s_setprio 1
	s_waitcnt lgkmcnt(0)
	v_mfma_f32_16x16x32_bf16 v[62:65], v[130:133], v[172:175], v[62:65]
	v_mfma_f32_16x16x32_bf16 v[58:61], v[138:141], v[172:175], v[58:61]
	v_mfma_f32_16x16x32_bf16 v[50:53], v[130:133], v[188:191], v[50:53]
	v_mfma_f32_16x16x32_bf16 v[42:45], v[138:141], v[188:191], v[42:45]
	v_mfma_f32_16x16x32_bf16 v[34:37], v[130:133], v[196:199], v[34:37]
	v_mfma_f32_16x16x32_bf16 v[26:29], v[138:141], v[196:199], v[26:29]
	v_mfma_f32_16x16x32_bf16 v[18:21], v[130:133], v[204:207], v[18:21]
	v_mfma_f32_16x16x32_bf16 v[10:13], v[138:141], v[204:207], v[10:13]
	v_mfma_f32_16x16x32_bf16 v[62:65], v[134:137], v[184:187], v[62:65]
	v_mfma_f32_16x16x32_bf16 v[58:61], v[142:145], v[184:187], v[58:61]
	v_mfma_f32_16x16x32_bf16 v[50:53], v[134:137], v[192:195], v[50:53]
	v_mfma_f32_16x16x32_bf16 v[42:45], v[142:145], v[192:195], v[42:45]
	v_mfma_f32_16x16x32_bf16 v[34:37], v[134:137], v[200:203], v[34:37]
	v_mfma_f32_16x16x32_bf16 v[26:29], v[142:145], v[200:203], v[26:29]
	v_mfma_f32_16x16x32_bf16 v[18:21], v[134:137], v[216:219], v[18:21]
	v_mfma_f32_16x16x32_bf16 v[10:13], v[142:145], v[216:219], v[10:13]
	s_setprio 0
	s_setprio 1
	v_mfma_f32_16x16x32_bf16 v[54:57], v[146:149], v[172:175], v[54:57]
	v_mfma_f32_16x16x32_bf16 v[46:49], v[154:157], v[172:175], v[46:49]
	v_mfma_f32_16x16x32_bf16 v[38:41], v[146:149], v[188:191], v[38:41]
	v_mfma_f32_16x16x32_bf16 v[30:33], v[154:157], v[188:191], v[30:33]
	v_mfma_f32_16x16x32_bf16 v[22:25], v[146:149], v[196:199], v[22:25]
	v_mfma_f32_16x16x32_bf16 v[14:17], v[154:157], v[196:199], v[14:17]
	v_mfma_f32_16x16x32_bf16 v[6:9], v[146:149], v[204:207], v[6:9]
	v_mfma_f32_16x16x32_bf16 v[2:5], v[154:157], v[204:207], v[2:5]
	v_mfma_f32_16x16x32_bf16 v[54:57], v[150:153], v[184:187], v[54:57]
	v_mfma_f32_16x16x32_bf16 v[46:49], v[168:171], v[184:187], v[46:49]
	v_mfma_f32_16x16x32_bf16 v[38:41], v[150:153], v[192:195], v[38:41]
	v_mfma_f32_16x16x32_bf16 v[30:33], v[168:171], v[192:195], v[30:33]
	v_mfma_f32_16x16x32_bf16 v[22:25], v[150:153], v[200:203], v[22:25]
	v_mfma_f32_16x16x32_bf16 v[14:17], v[168:171], v[200:203], v[14:17]
	v_mfma_f32_16x16x32_bf16 v[6:9], v[150:153], v[216:219], v[6:9]
	v_mfma_f32_16x16x32_bf16 v[2:5], v[168:171], v[216:219], v[2:5]
	s_setprio 0
	s_barrier
	s_add_i32 s53, 0, 0x18000
	s_add_i32 s58, 0, 0x1c000
	v_add_u32_e32 v142, s53, v181
	v_add_u32_e32 v168, s58, v181
	ds_read_b128 v[130:133], v142
	ds_read_b128 v[134:137], v142 offset:1024
	ds_read_b128 v[138:141], v142 offset:2048
	ds_read_b128 v[142:145], v142 offset:3072
	ds_read_b128 v[146:149], v168
	ds_read_b128 v[150:153], v168 offset:1024
	ds_read_b128 v[154:157], v168 offset:2048
	ds_read_b128 v[168:171], v168 offset:3072
	s_add_u32 s30, s30, 0x40000
	s_addc_u32 s31, s31, 0
	s_mov_b32 m0, s45
	v_lshl_add_u64 v[224:225], s[30:31], 0, v[0:1]
	ds_read_b128 v[172:175], v183 offset:32768
	ds_read_b128 v[184:187], v183 offset:33792
	ds_read_b128 v[188:191], v183 offset:34816
	ds_read_b128 v[192:195], v183 offset:35840
	ds_read_b128 v[196:199], v183 offset:36864
	ds_read_b128 v[200:203], v183 offset:37888
	ds_read_b128 v[204:207], v183 offset:38912
	ds_read_b128 v[216:219], v183 offset:39936
	global_load_lds_dwordx4 v[224:225], off
	s_mov_b32 m0, s46
	v_lshl_add_u64 v[224:225], s[30:31], 0, v[160:161]
	global_load_lds_dwordx4 v[224:225], off
	s_waitcnt vmcnt(8)
	s_waitcnt lgkmcnt(0)
	s_barrier
	s_setprio 1
	s_waitcnt lgkmcnt(0)
	v_mfma_f32_16x16x32_bf16 v[126:129], v[130:133], v[172:175], v[126:129]
	v_mfma_f32_16x16x32_bf16 v[122:125], v[138:141], v[172:175], v[122:125]
	v_mfma_f32_16x16x32_bf16 v[114:117], v[130:133], v[188:191], v[114:117]
	v_mfma_f32_16x16x32_bf16 v[106:109], v[138:141], v[188:191], v[106:109]
	v_mfma_f32_16x16x32_bf16 v[98:101], v[130:133], v[196:199], v[98:101]
	v_mfma_f32_16x16x32_bf16 v[90:93], v[138:141], v[196:199], v[90:93]
	v_mfma_f32_16x16x32_bf16 v[82:85], v[130:133], v[204:207], v[82:85]
	v_mfma_f32_16x16x32_bf16 v[74:77], v[138:141], v[204:207], v[74:77]
	v_mfma_f32_16x16x32_bf16 v[126:129], v[134:137], v[184:187], v[126:129]
	v_mfma_f32_16x16x32_bf16 v[122:125], v[142:145], v[184:187], v[122:125]
	v_mfma_f32_16x16x32_bf16 v[114:117], v[134:137], v[192:195], v[114:117]
	v_mfma_f32_16x16x32_bf16 v[106:109], v[142:145], v[192:195], v[106:109]
	v_mfma_f32_16x16x32_bf16 v[98:101], v[134:137], v[200:203], v[98:101]
	v_mfma_f32_16x16x32_bf16 v[90:93], v[142:145], v[200:203], v[90:93]
	v_mfma_f32_16x16x32_bf16 v[82:85], v[134:137], v[216:219], v[82:85]
	v_mfma_f32_16x16x32_bf16 v[74:77], v[142:145], v[216:219], v[74:77]
	s_setprio 0
	s_setprio 1
	v_mfma_f32_16x16x32_bf16 v[118:121], v[146:149], v[172:175], v[118:121]
	v_mfma_f32_16x16x32_bf16 v[110:113], v[154:157], v[172:175], v[110:113]
	v_mfma_f32_16x16x32_bf16 v[102:105], v[146:149], v[188:191], v[102:105]
	v_mfma_f32_16x16x32_bf16 v[94:97], v[154:157], v[188:191], v[94:97]
	v_mfma_f32_16x16x32_bf16 v[86:89], v[146:149], v[196:199], v[86:89]
	v_mfma_f32_16x16x32_bf16 v[78:81], v[154:157], v[196:199], v[78:81]
	v_mfma_f32_16x16x32_bf16 v[70:73], v[146:149], v[204:207], v[70:73]
	v_mfma_f32_16x16x32_bf16 v[66:69], v[154:157], v[204:207], v[66:69]
	v_mfma_f32_16x16x32_bf16 v[118:121], v[150:153], v[184:187], v[118:121]
	v_mfma_f32_16x16x32_bf16 v[110:113], v[168:171], v[184:187], v[110:113]
	v_mfma_f32_16x16x32_bf16 v[102:105], v[150:153], v[192:195], v[102:105]
	v_mfma_f32_16x16x32_bf16 v[94:97], v[168:171], v[192:195], v[94:97]
	v_mfma_f32_16x16x32_bf16 v[86:89], v[150:153], v[200:203], v[86:89]
	v_mfma_f32_16x16x32_bf16 v[78:81], v[168:171], v[200:203], v[78:81]
	v_mfma_f32_16x16x32_bf16 v[70:73], v[150:153], v[216:219], v[70:73]
	v_mfma_f32_16x16x32_bf16 v[66:69], v[168:171], v[216:219], v[66:69]
	s_setprio 0
	s_barrier
	s_add_i32 s30, s53, s36
	v_lshl_add_u64 v[176:177], v[176:177], 0, s[56:57]
	s_mov_b32 m0, s30
	ds_read_b128 v[172:175], v183 offset:49152
	ds_read_b128 v[184:187], v183 offset:50176
	ds_read_b128 v[188:191], v183 offset:51200
	ds_read_b128 v[192:195], v183 offset:52224
	ds_read_b128 v[196:199], v183 offset:53248
	ds_read_b128 v[200:203], v183 offset:54272
	ds_read_b128 v[204:207], v183 offset:55296
	ds_read_b128 v[216:219], v183 offset:56320
	global_load_lds_dwordx4 v[176:177], off
	s_add_i32 m0, s30, 0x2000
	s_add_u32 s28, s28, 0x40080
	v_lshl_add_u64 v[176:177], v[208:209], 0, s[56:57]
	s_addc_u32 s29, s29, 0
	s_add_i32 s30, s58, s36
	global_load_lds_dwordx4 v[176:177], off
	s_mov_b32 m0, s30
	v_lshl_add_u64 v[176:177], s[28:29], 0, v[162:163]
	global_load_lds_dwordx4 v[176:177], off
	s_add_i32 m0, s30, 0x2000
	v_lshl_add_u64 v[176:177], s[28:29], 0, v[158:159]
	global_load_lds_dwordx4 v[176:177], off
	s_mov_b32 m0, s47
	v_lshl_add_u64 v[176:177], v[220:221], 0, s[56:57]
	global_load_lds_dwordx4 v[176:177], off
	s_mov_b32 m0, s48
	v_lshl_add_u64 v[176:177], v[222:223], 0, s[56:57]
	global_load_lds_dwordx4 v[176:177], off
	s_waitcnt vmcnt(8)
	s_waitcnt lgkmcnt(0)
	s_barrier
	s_setprio 1
	s_waitcnt lgkmcnt(0)
	v_mfma_f32_16x16x32_bf16 v[62:65], v[130:133], v[172:175], v[62:65]
	v_mfma_f32_16x16x32_bf16 v[58:61], v[138:141], v[172:175], v[58:61]
	v_mfma_f32_16x16x32_bf16 v[50:53], v[130:133], v[188:191], v[50:53]
	v_mfma_f32_16x16x32_bf16 v[42:45], v[138:141], v[188:191], v[42:45]
	v_mfma_f32_16x16x32_bf16 v[34:37], v[130:133], v[196:199], v[34:37]
	v_mfma_f32_16x16x32_bf16 v[26:29], v[138:141], v[196:199], v[26:29]
	v_mfma_f32_16x16x32_bf16 v[18:21], v[130:133], v[204:207], v[18:21]
	v_mfma_f32_16x16x32_bf16 v[10:13], v[138:141], v[204:207], v[10:13]
	v_mfma_f32_16x16x32_bf16 v[62:65], v[134:137], v[184:187], v[62:65]
	v_mfma_f32_16x16x32_bf16 v[58:61], v[142:145], v[184:187], v[58:61]
	v_mfma_f32_16x16x32_bf16 v[50:53], v[134:137], v[192:195], v[50:53]
	v_mfma_f32_16x16x32_bf16 v[42:45], v[142:145], v[192:195], v[42:45]
	v_mfma_f32_16x16x32_bf16 v[34:37], v[134:137], v[200:203], v[34:37]
	v_mfma_f32_16x16x32_bf16 v[26:29], v[142:145], v[200:203], v[26:29]
	v_mfma_f32_16x16x32_bf16 v[18:21], v[134:137], v[216:219], v[18:21]
	v_mfma_f32_16x16x32_bf16 v[10:13], v[142:145], v[216:219], v[10:13]
	s_setprio 0
	s_setprio 1
	v_mfma_f32_16x16x32_bf16 v[54:57], v[146:149], v[172:175], v[54:57]
	v_mfma_f32_16x16x32_bf16 v[46:49], v[154:157], v[172:175], v[46:49]
	v_mfma_f32_16x16x32_bf16 v[38:41], v[146:149], v[188:191], v[38:41]
	v_mfma_f32_16x16x32_bf16 v[30:33], v[154:157], v[188:191], v[30:33]
	v_mfma_f32_16x16x32_bf16 v[22:25], v[146:149], v[196:199], v[22:25]
	v_mfma_f32_16x16x32_bf16 v[14:17], v[154:157], v[196:199], v[14:17]
	v_mfma_f32_16x16x32_bf16 v[6:9], v[146:149], v[204:207], v[6:9]
	v_mfma_f32_16x16x32_bf16 v[2:5], v[154:157], v[204:207], v[2:5]
	v_mfma_f32_16x16x32_bf16 v[54:57], v[150:153], v[184:187], v[54:57]
	v_mfma_f32_16x16x32_bf16 v[46:49], v[168:171], v[184:187], v[46:49]
	v_mfma_f32_16x16x32_bf16 v[38:41], v[150:153], v[192:195], v[38:41]
	v_mfma_f32_16x16x32_bf16 v[30:33], v[168:171], v[192:195], v[30:33]
	v_mfma_f32_16x16x32_bf16 v[22:25], v[150:153], v[200:203], v[22:25]
	v_mfma_f32_16x16x32_bf16 v[14:17], v[168:171], v[200:203], v[14:17]
	v_mfma_f32_16x16x32_bf16 v[6:9], v[150:153], v[216:219], v[6:9]
	v_mfma_f32_16x16x32_bf16 v[2:5], v[168:171], v[216:219], v[2:5]
	s_setprio 0
	s_barrier
	s_add_i32 s41, s41, 2
	s_add_u32 s33, s33, 0x100
	s_addc_u32 s40, s40, 0
	s_add_u32 s6, s6, 0x100
	s_addc_u32 s7, s7, 0
	s_cmp_gt_u32 s41, 13
	s_cbranch_scc0 .LBB0_1783
	s_and_b64 vcc, exec, s[18:19]
	s_cbranch_vccz .LBB0_1786
	s_barrier

.LBB0_1799:
	s_add_u32 s26, s24, 0xfffc0080
	s_addc_u32 s27, s25, -1
	s_add_i32 s48, 0, 0x10000
	s_cmp_eq_u32 s47, 12
	s_cselect_b32 s29, s8, s27
	s_cselect_b32 s28, s9, s26
	v_add_u32_e32 v142, s48, v144
	s_cselect_b32 s27, s15, s46
	s_cselect_b32 s26, s17, s45
	s_add_i32 s52, 0, 0x14000
	ds_read_b128 v[148:151], v142
	ds_read_b128 v[152:155], v142 offset:1024
	ds_read_b128 v[156:159], v142 offset:2048
	ds_read_b128 v[160:163], v142 offset:3072
	v_add_u32_e32 v142, s52, v144
	ds_read_b128 v[164:167], v142
	ds_read_b128 v[168:171], v142 offset:1024
	ds_read_b128 v[172:175], v142 offset:2048
	ds_read_b128 v[180:183], v142 offset:3072
	v_lshl_add_u64 v[142:143], s[24:25], 0, v[140:141]
	s_add_i32 m0, s36, 0xc000
	ds_read_b128 v[184:187], v146
	ds_read_b128 v[188:191], v146 offset:1024
	ds_read_b128 v[192:195], v146 offset:2048
	ds_read_b128 v[196:199], v146 offset:3072
	ds_read_b128 v[200:203], v146 offset:4096
	ds_read_b128 v[204:207], v146 offset:5120
	ds_read_b128 v[216:219], v146 offset:6144
	ds_read_b128 v[220:223], v146 offset:7168
	global_load_lds_dwordx4 v[142:143], off
	s_add_i32 m0, s36, 0xe000
	v_lshl_add_u64 v[142:143], s[24:25], 0, v[138:139]
	global_load_lds_dwordx4 v[142:143], off
	s_waitcnt vmcnt(8)
	s_waitcnt lgkmcnt(0)
	s_barrier
	s_setprio 1
	s_waitcnt lgkmcnt(0)
	v_mfma_f32_16x16x32_bf16 v[126:129], v[148:151], v[184:187], v[126:129]
	v_mfma_f32_16x16x32_bf16 v[122:125], v[156:159], v[184:187], v[122:125]
	v_mfma_f32_16x16x32_bf16 v[118:121], v[148:151], v[192:195], v[118:121]
	v_mfma_f32_16x16x32_bf16 v[110:113], v[156:159], v[192:195], v[110:113]
	v_mfma_f32_16x16x32_bf16 v[102:105], v[148:151], v[200:203], v[102:105]
	v_mfma_f32_16x16x32_bf16 v[94:97], v[156:159], v[200:203], v[94:97]
	v_mfma_f32_16x16x32_bf16 v[86:89], v[148:151], v[216:219], v[86:89]
	v_mfma_f32_16x16x32_bf16 v[78:81], v[156:159], v[216:219], v[78:81]
	v_mfma_f32_16x16x32_bf16 v[126:129], v[152:155], v[188:191], v[126:129]
	v_mfma_f32_16x16x32_bf16 v[122:125], v[160:163], v[188:191], v[122:125]
	v_mfma_f32_16x16x32_bf16 v[118:121], v[152:155], v[196:199], v[118:121]
	v_mfma_f32_16x16x32_bf16 v[110:113], v[160:163], v[196:199], v[110:113]
	v_mfma_f32_16x16x32_bf16 v[102:105], v[152:155], v[204:207], v[102:105]
	v_mfma_f32_16x16x32_bf16 v[94:97], v[160:163], v[204:207], v[94:97]
	v_mfma_f32_16x16x32_bf16 v[86:89], v[152:155], v[220:223], v[86:89]
	v_mfma_f32_16x16x32_bf16 v[78:81], v[160:163], v[220:223], v[78:81]
	s_setprio 0
	s_setprio 1
	v_mfma_f32_16x16x32_bf16 v[114:117], v[164:167], v[184:187], v[114:117]
	v_mfma_f32_16x16x32_bf16 v[106:109], v[172:175], v[184:187], v[106:109]
	v_mfma_f32_16x16x32_bf16 v[98:101], v[164:167], v[192:195], v[98:101]
	v_mfma_f32_16x16x32_bf16 v[90:93], v[172:175], v[192:195], v[90:93]
	v_mfma_f32_16x16x32_bf16 v[82:85], v[164:167], v[200:203], v[82:85]
	v_mfma_f32_16x16x32_bf16 v[74:77], v[172:175], v[200:203], v[74:77]
	v_mfma_f32_16x16x32_bf16 v[70:73], v[164:167], v[216:219], v[70:73]
	v_mfma_f32_16x16x32_bf16 v[66:69], v[172:175], v[216:219], v[66:69]
	v_mfma_f32_16x16x32_bf16 v[114:117], v[168:171], v[188:191], v[114:117]
	v_mfma_f32_16x16x32_bf16 v[106:109], v[180:183], v[188:191], v[106:109]
	v_mfma_f32_16x16x32_bf16 v[98:101], v[168:171], v[196:199], v[98:101]
	v_mfma_f32_16x16x32_bf16 v[90:93], v[180:183], v[196:199], v[90:93]
	v_mfma_f32_16x16x32_bf16 v[82:85], v[168:171], v[204:207], v[82:85]
	v_mfma_f32_16x16x32_bf16 v[74:77], v[180:183], v[204:207], v[74:77]
	v_mfma_f32_16x16x32_bf16 v[70:73], v[168:171], v[220:223], v[70:73]
	v_mfma_f32_16x16x32_bf16 v[66:69], v[180:183], v[220:223], v[66:69]
	s_setprio 0
	s_barrier
	s_add_i32 s48, s48, s35
	v_lshl_add_u64 v[142:143], s[26:27], 0, v[134:135]
	s_mov_b32 m0, s48
	ds_read_b128 v[184:187], v146 offset:16384
	ds_read_b128 v[188:191], v146 offset:17408
	ds_read_b128 v[192:195], v146 offset:18432
	ds_read_b128 v[196:199], v146 offset:19456
	ds_read_b128 v[200:203], v146 offset:20480
	ds_read_b128 v[204:207], v146 offset:21504
	ds_read_b128 v[216:219], v146 offset:22528
	ds_read_b128 v[220:223], v146 offset:23552
	global_load_lds_dwordx4 v[142:143], off
	s_add_i32 m0, s48, 0x2000
	s_add_u32 s48, s26, 0x40000
	v_lshl_add_u64 v[176:177], s[26:27], 0, v[130:131]
	s_addc_u32 s49, s27, 0
	s_add_i32 s52, s52, s35
	global_load_lds_dwordx4 v[176:177], off
	v_lshl_add_u64 v[208:209], s[48:49], 0, v[134:135]
	s_mov_b32 m0, s52
	v_lshl_add_u64 v[224:225], s[28:29], 0, v[132:133]
	global_load_lds_dwordx4 v[208:209], off
	s_add_i32 m0, s52, 0x2000
	v_lshl_add_u64 v[208:209], s[48:49], 0, v[130:131]
	global_load_lds_dwordx4 v[208:209], off
	s_mov_b32 m0, s36
	v_lshl_add_u64 v[208:209], s[28:29], 0, v[136:137]
	global_load_lds_dwordx4 v[208:209], off
	s_mov_b32 m0, s37
	s_nop 0
	global_load_lds_dwordx4 v[224:225], off
	s_waitcnt vmcnt(8)
	s_waitcnt lgkmcnt(0)
	s_barrier
	s_setprio 1
	s_waitcnt lgkmcnt(0)
	v_mfma_f32_16x16x32_bf16 v[62:65], v[148:151], v[184:187], v[62:65]
	v_mfma_f32_16x16x32_bf16 v[58:61], v[156:159], v[184:187], v[58:61]
	v_mfma_f32_16x16x32_bf16 v[54:57], v[148:151], v[192:195], v[54:57]
	v_mfma_f32_16x16x32_bf16 v[46:49], v[156:159], v[192:195], v[46:49]
	v_mfma_f32_16x16x32_bf16 v[38:41], v[148:151], v[200:203], v[38:41]
	v_mfma_f32_16x16x32_bf16 v[30:33], v[156:159], v[200:203], v[30:33]
	v_mfma_f32_16x16x32_bf16 v[22:25], v[148:151], v[216:219], v[22:25]
	v_mfma_f32_16x16x32_bf16 v[14:17], v[156:159], v[216:219], v[14:17]
	v_mfma_f32_16x16x32_bf16 v[62:65], v[152:155], v[188:191], v[62:65]
	v_mfma_f32_16x16x32_bf16 v[58:61], v[160:163], v[188:191], v[58:61]
	v_mfma_f32_16x16x32_bf16 v[54:57], v[152:155], v[196:199], v[54:57]
	v_mfma_f32_16x16x32_bf16 v[46:49], v[160:163], v[196:199], v[46:49]
	v_mfma_f32_16x16x32_bf16 v[38:41], v[152:155], v[204:207], v[38:41]
	v_mfma_f32_16x16x32_bf16 v[30:33], v[160:163], v[204:207], v[30:33]
	v_mfma_f32_16x16x32_bf16 v[22:25], v[152:155], v[220:223], v[22:25]
	v_mfma_f32_16x16x32_bf16 v[14:17], v[160:163], v[220:223], v[14:17]
	s_setprio 0
	s_setprio 1
	v_mfma_f32_16x16x32_bf16 v[50:53], v[164:167], v[184:187], v[50:53]
	v_mfma_f32_16x16x32_bf16 v[42:45], v[172:175], v[184:187], v[42:45]
	v_mfma_f32_16x16x32_bf16 v[34:37], v[164:167], v[192:195], v[34:37]
	v_mfma_f32_16x16x32_bf16 v[26:29], v[172:175], v[192:195], v[26:29]
	v_mfma_f32_16x16x32_bf16 v[18:21], v[164:167], v[200:203], v[18:21]
	v_mfma_f32_16x16x32_bf16 v[10:13], v[172:175], v[200:203], v[10:13]
	v_mfma_f32_16x16x32_bf16 v[6:9], v[164:167], v[216:219], v[6:9]
	v_mfma_f32_16x16x32_bf16 v[2:5], v[172:175], v[216:219], v[2:5]
	v_mfma_f32_16x16x32_bf16 v[50:53], v[168:171], v[188:191], v[50:53]
	v_mfma_f32_16x16x32_bf16 v[42:45], v[180:183], v[188:191], v[42:45]
	v_mfma_f32_16x16x32_bf16 v[34:37], v[168:171], v[196:199], v[34:37]
	v_mfma_f32_16x16x32_bf16 v[26:29], v[180:183], v[196:199], v[26:29]
	v_mfma_f32_16x16x32_bf16 v[18:21], v[168:171], v[204:207], v[18:21]
	v_mfma_f32_16x16x32_bf16 v[10:13], v[180:183], v[204:207], v[10:13]
	v_mfma_f32_16x16x32_bf16 v[6:9], v[168:171], v[220:223], v[6:9]
	v_mfma_f32_16x16x32_bf16 v[2:5], v[180:183], v[220:223], v[2:5]
	s_setprio 0
	s_barrier
	s_add_i32 s48, 0, 0x18000
	v_add_u32_e32 v147, s48, v144
	s_add_i32 s49, 0, 0x1c000
	ds_read_b128 v[148:151], v147
	ds_read_b128 v[152:155], v147 offset:1024
	ds_read_b128 v[156:159], v147 offset:2048
	ds_read_b128 v[160:163], v147 offset:3072
	v_add_u32_e32 v147, s49, v144
	ds_read_b128 v[164:167], v147
	ds_read_b128 v[168:171], v147 offset:1024
	ds_read_b128 v[172:175], v147 offset:2048
	ds_read_b128 v[180:183], v147 offset:3072
	s_add_u32 s28, s28, 0x40000
	s_addc_u32 s29, s29, 0
	s_mov_b32 m0, s4
	v_lshl_add_u64 v[240:241], s[28:29], 0, v[136:137]
	ds_read_b128 v[184:187], v146 offset:32768
	ds_read_b128 v[188:191], v146 offset:33792
	ds_read_b128 v[192:195], v146 offset:34816
	ds_read_b128 v[196:199], v146 offset:35840
	ds_read_b128 v[200:203], v146 offset:36864
	ds_read_b128 v[204:207], v146 offset:37888
	ds_read_b128 v[216:219], v146 offset:38912
	ds_read_b128 v[220:223], v146 offset:39936
	global_load_lds_dwordx4 v[240:241], off
	s_mov_b32 m0, s33
	v_lshl_add_u64 v[240:241], s[28:29], 0, v[132:133]
	global_load_lds_dwordx4 v[240:241], off
	s_waitcnt vmcnt(8)
	s_waitcnt lgkmcnt(0)
	s_barrier
	s_setprio 1
	s_waitcnt lgkmcnt(0)
	v_mfma_f32_16x16x32_bf16 v[126:129], v[148:151], v[184:187], v[126:129]
	v_mfma_f32_16x16x32_bf16 v[122:125], v[156:159], v[184:187], v[122:125]
	v_mfma_f32_16x16x32_bf16 v[118:121], v[148:151], v[192:195], v[118:121]
	v_mfma_f32_16x16x32_bf16 v[110:113], v[156:159], v[192:195], v[110:113]
	v_mfma_f32_16x16x32_bf16 v[102:105], v[148:151], v[200:203], v[102:105]
	v_mfma_f32_16x16x32_bf16 v[94:97], v[156:159], v[200:203], v[94:97]
	v_mfma_f32_16x16x32_bf16 v[86:89], v[148:151], v[216:219], v[86:89]
	v_mfma_f32_16x16x32_bf16 v[78:81], v[156:159], v[216:219], v[78:81]
	v_mfma_f32_16x16x32_bf16 v[126:129], v[152:155], v[188:191], v[126:129]
	v_mfma_f32_16x16x32_bf16 v[122:125], v[160:163], v[188:191], v[122:125]
	v_mfma_f32_16x16x32_bf16 v[118:121], v[152:155], v[196:199], v[118:121]
	v_mfma_f32_16x16x32_bf16 v[110:113], v[160:163], v[196:199], v[110:113]
	v_mfma_f32_16x16x32_bf16 v[102:105], v[152:155], v[204:207], v[102:105]
	v_mfma_f32_16x16x32_bf16 v[94:97], v[160:163], v[204:207], v[94:97]
	v_mfma_f32_16x16x32_bf16 v[86:89], v[152:155], v[220:223], v[86:89]
	v_mfma_f32_16x16x32_bf16 v[78:81], v[160:163], v[220:223], v[78:81]
	s_setprio 0
	s_setprio 1
	v_mfma_f32_16x16x32_bf16 v[114:117], v[164:167], v[184:187], v[114:117]
	v_mfma_f32_16x16x32_bf16 v[106:109], v[172:175], v[184:187], v[106:109]
	v_mfma_f32_16x16x32_bf16 v[98:101], v[164:167], v[192:195], v[98:101]
	v_mfma_f32_16x16x32_bf16 v[90:93], v[172:175], v[192:195], v[90:93]
	v_mfma_f32_16x16x32_bf16 v[82:85], v[164:167], v[200:203], v[82:85]
	v_mfma_f32_16x16x32_bf16 v[74:77], v[172:175], v[200:203], v[74:77]
	v_mfma_f32_16x16x32_bf16 v[70:73], v[164:167], v[216:219], v[70:73]
	v_mfma_f32_16x16x32_bf16 v[66:69], v[172:175], v[216:219], v[66:69]
	v_mfma_f32_16x16x32_bf16 v[114:117], v[168:171], v[188:191], v[114:117]
	v_mfma_f32_16x16x32_bf16 v[106:109], v[180:183], v[188:191], v[106:109]
	v_mfma_f32_16x16x32_bf16 v[98:101], v[168:171], v[196:199], v[98:101]
	v_mfma_f32_16x16x32_bf16 v[90:93], v[180:183], v[196:199], v[90:93]
	v_mfma_f32_16x16x32_bf16 v[82:85], v[168:171], v[204:207], v[82:85]
	v_mfma_f32_16x16x32_bf16 v[74:77], v[180:183], v[204:207], v[74:77]
	v_mfma_f32_16x16x32_bf16 v[70:73], v[168:171], v[220:223], v[70:73]
	v_mfma_f32_16x16x32_bf16 v[66:69], v[180:183], v[220:223], v[66:69]
	s_setprio 0
	s_barrier
	s_add_i32 s28, s48, s35
	v_lshl_add_u64 v[142:143], v[142:143], 0, s[56:57]
	s_mov_b32 m0, s28
	ds_read_b128 v[184:187], v146 offset:49152
	ds_read_b128 v[188:191], v146 offset:50176
	ds_read_b128 v[192:195], v146 offset:51200
	ds_read_b128 v[196:199], v146 offset:52224
	ds_read_b128 v[200:203], v146 offset:53248
	ds_read_b128 v[204:207], v146 offset:54272
	ds_read_b128 v[216:219], v146 offset:55296
	ds_read_b128 v[220:223], v146 offset:56320
	global_load_lds_dwordx4 v[142:143], off
	s_add_i32 m0, s28, 0x2000
	s_add_u32 s26, s26, 0x40080
	v_lshl_add_u64 v[142:143], v[176:177], 0, s[56:57]
	s_addc_u32 s27, s27, 0
	s_add_i32 s28, s49, s35
	global_load_lds_dwordx4 v[142:143], off
	s_mov_b32 m0, s28
	v_lshl_add_u64 v[142:143], s[26:27], 0, v[134:135]
	global_load_lds_dwordx4 v[142:143], off
	s_add_i32 m0, s28, 0x2000
	v_lshl_add_u64 v[142:143], s[26:27], 0, v[130:131]
	global_load_lds_dwordx4 v[142:143], off
	s_mov_b32 m0, s38
	v_lshl_add_u64 v[142:143], v[208:209], 0, s[56:57]
	global_load_lds_dwordx4 v[142:143], off
	s_mov_b32 m0, s39
	v_lshl_add_u64 v[142:143], v[224:225], 0, s[56:57]
	global_load_lds_dwordx4 v[142:143], off
	s_waitcnt vmcnt(8)
	s_waitcnt lgkmcnt(0)
	s_barrier
	s_setprio 1
	s_waitcnt lgkmcnt(0)
	v_mfma_f32_16x16x32_bf16 v[62:65], v[148:151], v[184:187], v[62:65]
	v_mfma_f32_16x16x32_bf16 v[58:61], v[156:159], v[184:187], v[58:61]
	v_mfma_f32_16x16x32_bf16 v[54:57], v[148:151], v[192:195], v[54:57]
	v_mfma_f32_16x16x32_bf16 v[46:49], v[156:159], v[192:195], v[46:49]
	v_mfma_f32_16x16x32_bf16 v[38:41], v[148:151], v[200:203], v[38:41]
	v_mfma_f32_16x16x32_bf16 v[30:33], v[156:159], v[200:203], v[30:33]
	v_mfma_f32_16x16x32_bf16 v[22:25], v[148:151], v[216:219], v[22:25]
	v_mfma_f32_16x16x32_bf16 v[14:17], v[156:159], v[216:219], v[14:17]
	v_mfma_f32_16x16x32_bf16 v[62:65], v[152:155], v[188:191], v[62:65]
	v_mfma_f32_16x16x32_bf16 v[58:61], v[160:163], v[188:191], v[58:61]
	v_mfma_f32_16x16x32_bf16 v[54:57], v[152:155], v[196:199], v[54:57]
	v_mfma_f32_16x16x32_bf16 v[46:49], v[160:163], v[196:199], v[46:49]
	v_mfma_f32_16x16x32_bf16 v[38:41], v[152:155], v[204:207], v[38:41]
	v_mfma_f32_16x16x32_bf16 v[30:33], v[160:163], v[204:207], v[30:33]
	v_mfma_f32_16x16x32_bf16 v[22:25], v[152:155], v[220:223], v[22:25]
	v_mfma_f32_16x16x32_bf16 v[14:17], v[160:163], v[220:223], v[14:17]
	s_setprio 0
	s_setprio 1
	v_mfma_f32_16x16x32_bf16 v[50:53], v[164:167], v[184:187], v[50:53]
	v_mfma_f32_16x16x32_bf16 v[42:45], v[172:175], v[184:187], v[42:45]
	v_mfma_f32_16x16x32_bf16 v[34:37], v[164:167], v[192:195], v[34:37]
	v_mfma_f32_16x16x32_bf16 v[26:29], v[172:175], v[192:195], v[26:29]
	v_mfma_f32_16x16x32_bf16 v[18:21], v[164:167], v[200:203], v[18:21]
	v_mfma_f32_16x16x32_bf16 v[10:13], v[172:175], v[200:203], v[10:13]
	v_mfma_f32_16x16x32_bf16 v[6:9], v[164:167], v[216:219], v[6:9]
	v_mfma_f32_16x16x32_bf16 v[2:5], v[172:175], v[216:219], v[2:5]
	v_mfma_f32_16x16x32_bf16 v[50:53], v[168:171], v[188:191], v[50:53]
	v_mfma_f32_16x16x32_bf16 v[42:45], v[180:183], v[188:191], v[42:45]
	v_mfma_f32_16x16x32_bf16 v[34:37], v[168:171], v[196:199], v[34:37]
	v_mfma_f32_16x16x32_bf16 v[26:29], v[180:183], v[196:199], v[26:29]
	v_mfma_f32_16x16x32_bf16 v[18:21], v[168:171], v[204:207], v[18:21]
	v_mfma_f32_16x16x32_bf16 v[10:13], v[180:183], v[204:207], v[10:13]
	v_mfma_f32_16x16x32_bf16 v[6:9], v[168:171], v[220:223], v[6:9]
	v_mfma_f32_16x16x32_bf16 v[2:5], v[180:183], v[220:223], v[2:5]
	s_setprio 0
	s_barrier
	s_add_i32 s47, s47, 2
	s_add_u32 s45, s45, 0x100
	s_addc_u32 s46, s46, 0
	s_add_u32 s24, s24, 0x100
	s_addc_u32 s25, s25, 0
	s_cmp_gt_u32 s47, 13
	s_cbranch_scc0 .LBB0_1799
	s_and_b64 vcc, exec, s[12:13]
	s_cbranch_vccz .LBB0_1802
	s_barrier

.LBB0_2367:
	s_add_u32 s10, s34, s38
	s_addc_u32 s11, s35, 0
	s_add_u32 s39, s10, 0x100
	s_addc_u32 s76, s11, 0
	s_and_b64 s[70:71], s[62:63], exec
	s_cselect_b32 s77, s45, s76
	s_cselect_b32 s76, s59, s39
	s_add_u32 s38, s30, s38
	s_addc_u32 s39, s31, 0
	s_add_u32 s70, s38, 0x100
	s_addc_u32 s71, s39, 0
	s_add_i32 s91, 0, 0x10000
	s_and_b64 s[38:39], s[62:63], exec
	s_cselect_b32 s79, s37, s71
	s_cselect_b32 s78, s82, s70
	s_add_i32 s38, 0, 0x14000
	s_add_u32 s10, s10, 0x10080
	s_addc_u32 s11, s11, 0
	s_add_i32 s8, s91, s95
	s_add_i32 m0, s65, 0xc000
	s_add_i32 s14, s65, 0xe000
	s_add_i32 s9, s8, 0x2000
	s_add_u32 s80, s78, 0x10000
	s_addc_u32 s81, s79, 0
	s_add_i32 s50, s38, s95
	v_add_u32_e32 v152, s91, v138
	v_add_u32_e32 v164, s38, v138
	s_add_i32 s74, s50, 0x2000
	s_add_i32 vcc_hi, 0, 0x18000
	s_add_i32 s39, 0, 0x1c000
	ds_read_b128 v[140:143], v152
	ds_read_b128 v[144:147], v152 offset:1024
	ds_read_b128 v[148:151], v152 offset:2048
	ds_read_b128 v[152:155], v152 offset:3072
	ds_read_b128 v[156:159], v164
	ds_read_b128 v[160:163], v164 offset:1024
	ds_read_b128 v[168:171], v164 offset:2048
	ds_read_b128 v[172:175], v164 offset:3072
	s_add_u32 s70, s76, 0x10000
	s_addc_u32 s71, s77, 0
	s_add_i32 vcc_lo, vcc_hi, s95
	s_add_i32 s64, vcc_lo, 0x2000
	s_add_u32 s62, s78, 0x10080
	s_addc_u32 s63, s79, 0
	s_add_i32 s91, s39, s95
	s_add_i32 s38, s91, 0x2000
	v_lshl_add_u64 v[164:165], s[10:11], 0, v[128:129]
	ds_read_b128 v[176:179], v139
	ds_read_b128 v[180:183], v139 offset:1024
	ds_read_b128 v[184:187], v139 offset:2048
	ds_read_b128 v[188:191], v139 offset:3072
	ds_read_b128 v[192:195], v139 offset:4096
	ds_read_b128 v[196:199], v139 offset:5120
	ds_read_b128 v[200:203], v139 offset:6144
	ds_read_b128 v[204:207], v139 offset:7168
	global_load_lds_dwordx4 v[164:165], off
	s_mov_b32 m0, s14
	v_lshl_add_u64 v[164:165], s[10:11], 0, v[124:125]
	global_load_lds_dwordx4 v[164:165], off
	s_waitcnt vmcnt(8)
	s_waitcnt lgkmcnt(0)
	s_barrier
	s_setprio 1
	s_waitcnt lgkmcnt(0)
	v_mfma_f32_16x16x32_bf16 v[134:137], v[140:143], v[176:179], v[134:137]
	v_mfma_f32_16x16x32_bf16 v[130:133], v[148:151], v[176:179], v[130:133]
	v_mfma_f32_16x16x32_bf16 v[110:113], v[140:143], v[184:187], v[110:113]
	v_mfma_f32_16x16x32_bf16 v[106:109], v[148:151], v[184:187], v[106:109]
	v_mfma_f32_16x16x32_bf16 v[94:97], v[140:143], v[192:195], v[94:97]
	v_mfma_f32_16x16x32_bf16 v[90:93], v[148:151], v[192:195], v[90:93]
	v_mfma_f32_16x16x32_bf16 v[78:81], v[140:143], v[200:203], v[78:81]
	v_mfma_f32_16x16x32_bf16 v[74:77], v[148:151], v[200:203], v[74:77]
	v_mfma_f32_16x16x32_bf16 v[134:137], v[144:147], v[180:183], v[134:137]
	v_mfma_f32_16x16x32_bf16 v[130:133], v[152:155], v[180:183], v[130:133]
	v_mfma_f32_16x16x32_bf16 v[110:113], v[144:147], v[188:191], v[110:113]
	v_mfma_f32_16x16x32_bf16 v[106:109], v[152:155], v[188:191], v[106:109]
	v_mfma_f32_16x16x32_bf16 v[94:97], v[144:147], v[196:199], v[94:97]
	v_mfma_f32_16x16x32_bf16 v[90:93], v[152:155], v[196:199], v[90:93]
	v_mfma_f32_16x16x32_bf16 v[78:81], v[144:147], v[204:207], v[78:81]
	v_mfma_f32_16x16x32_bf16 v[74:77], v[152:155], v[204:207], v[74:77]
	s_setprio 0
	s_setprio 1
	v_mfma_f32_16x16x32_bf16 v[118:121], v[156:159], v[176:179], v[118:121]
	v_mfma_f32_16x16x32_bf16 v[114:117], v[168:171], v[176:179], v[114:117]
	v_mfma_f32_16x16x32_bf16 v[102:105], v[156:159], v[184:187], v[102:105]
	v_mfma_f32_16x16x32_bf16 v[98:101], v[168:171], v[184:187], v[98:101]
	v_mfma_f32_16x16x32_bf16 v[86:89], v[156:159], v[192:195], v[86:89]
	v_mfma_f32_16x16x32_bf16 v[82:85], v[168:171], v[192:195], v[82:85]
	v_mfma_f32_16x16x32_bf16 v[70:73], v[156:159], v[200:203], v[70:73]
	v_mfma_f32_16x16x32_bf16 v[66:69], v[168:171], v[200:203], v[66:69]
	v_mfma_f32_16x16x32_bf16 v[118:121], v[160:163], v[180:183], v[118:121]
	v_mfma_f32_16x16x32_bf16 v[114:117], v[172:175], v[180:183], v[114:117]
	v_mfma_f32_16x16x32_bf16 v[102:105], v[160:163], v[188:191], v[102:105]
	v_mfma_f32_16x16x32_bf16 v[98:101], v[172:175], v[188:191], v[98:101]
	v_mfma_f32_16x16x32_bf16 v[86:89], v[160:163], v[196:199], v[86:89]
	v_mfma_f32_16x16x32_bf16 v[82:85], v[172:175], v[196:199], v[82:85]
	v_mfma_f32_16x16x32_bf16 v[70:73], v[160:163], v[204:207], v[70:73]
	v_mfma_f32_16x16x32_bf16 v[66:69], v[172:175], v[204:207], v[66:69]
	s_setprio 0
	s_barrier
	s_mov_b32 m0, s8
	v_lshl_add_u64 v[164:165], s[78:79], 0, v[126:127]
	ds_read_b128 v[176:179], v139 offset:16384
	ds_read_b128 v[180:183], v139 offset:17408
	ds_read_b128 v[184:187], v139 offset:18432
	ds_read_b128 v[188:191], v139 offset:19456
	ds_read_b128 v[192:195], v139 offset:20480
	ds_read_b128 v[196:199], v139 offset:21504
	ds_read_b128 v[200:203], v139 offset:22528
	ds_read_b128 v[204:207], v139 offset:23552
	global_load_lds_dwordx4 v[164:165], off
	v_lshl_add_u64 v[208:209], s[78:79], 0, v[122:123]
	s_mov_b32 m0, s9
	v_lshl_add_u64 v[216:217], s[80:81], 0, v[126:127]
	global_load_lds_dwordx4 v[208:209], off
	s_mov_b32 m0, s50
	v_lshl_add_u64 v[218:219], s[76:77], 0, v[124:125]
	global_load_lds_dwordx4 v[216:217], off
	s_mov_b32 m0, s74
	v_lshl_add_u64 v[216:217], s[80:81], 0, v[122:123]
	global_load_lds_dwordx4 v[216:217], off
	s_mov_b32 m0, s65
	v_lshl_add_u64 v[216:217], s[76:77], 0, v[128:129]
	global_load_lds_dwordx4 v[216:217], off
	s_mov_b32 m0, s15
	s_nop 0
	global_load_lds_dwordx4 v[218:219], off
	s_waitcnt vmcnt(8)
	s_waitcnt lgkmcnt(0)
	s_barrier
	s_setprio 1
	s_waitcnt lgkmcnt(0)
	v_mfma_f32_16x16x32_bf16 v[62:65], v[140:143], v[176:179], v[62:65]
	v_mfma_f32_16x16x32_bf16 v[58:61], v[148:151], v[176:179], v[58:61]
	v_mfma_f32_16x16x32_bf16 v[46:49], v[140:143], v[184:187], v[46:49]
	v_mfma_f32_16x16x32_bf16 v[42:45], v[148:151], v[184:187], v[42:45]
	v_mfma_f32_16x16x32_bf16 v[30:33], v[140:143], v[192:195], v[30:33]
	v_mfma_f32_16x16x32_bf16 v[26:29], v[148:151], v[192:195], v[26:29]
	v_mfma_f32_16x16x32_bf16 v[14:17], v[140:143], v[200:203], v[14:17]
	v_mfma_f32_16x16x32_bf16 v[10:13], v[148:151], v[200:203], v[10:13]
	v_mfma_f32_16x16x32_bf16 v[62:65], v[144:147], v[180:183], v[62:65]
	v_mfma_f32_16x16x32_bf16 v[58:61], v[152:155], v[180:183], v[58:61]
	v_mfma_f32_16x16x32_bf16 v[46:49], v[144:147], v[188:191], v[46:49]
	v_mfma_f32_16x16x32_bf16 v[42:45], v[152:155], v[188:191], v[42:45]
	v_mfma_f32_16x16x32_bf16 v[30:33], v[144:147], v[196:199], v[30:33]
	v_mfma_f32_16x16x32_bf16 v[26:29], v[152:155], v[196:199], v[26:29]
	v_mfma_f32_16x16x32_bf16 v[14:17], v[144:147], v[204:207], v[14:17]
	v_mfma_f32_16x16x32_bf16 v[10:13], v[152:155], v[204:207], v[10:13]
	s_setprio 0
	s_setprio 1
	v_mfma_f32_16x16x32_bf16 v[54:57], v[156:159], v[176:179], v[54:57]
	v_mfma_f32_16x16x32_bf16 v[50:53], v[168:171], v[176:179], v[50:53]
	v_mfma_f32_16x16x32_bf16 v[38:41], v[156:159], v[184:187], v[38:41]
	v_mfma_f32_16x16x32_bf16 v[34:37], v[168:171], v[184:187], v[34:37]
	v_mfma_f32_16x16x32_bf16 v[22:25], v[156:159], v[192:195], v[22:25]
	v_mfma_f32_16x16x32_bf16 v[18:21], v[168:171], v[192:195], v[18:21]
	v_mfma_f32_16x16x32_bf16 v[6:9], v[156:159], v[200:203], v[6:9]
	v_mfma_f32_16x16x32_bf16 v[2:5], v[168:171], v[200:203], v[2:5]
	v_mfma_f32_16x16x32_bf16 v[54:57], v[160:163], v[180:183], v[54:57]
	v_mfma_f32_16x16x32_bf16 v[50:53], v[172:175], v[180:183], v[50:53]
	v_mfma_f32_16x16x32_bf16 v[38:41], v[160:163], v[188:191], v[38:41]
	v_mfma_f32_16x16x32_bf16 v[34:37], v[172:175], v[188:191], v[34:37]
	v_mfma_f32_16x16x32_bf16 v[22:25], v[160:163], v[196:199], v[22:25]
	v_mfma_f32_16x16x32_bf16 v[18:21], v[172:175], v[196:199], v[18:21]
	v_mfma_f32_16x16x32_bf16 v[6:9], v[160:163], v[204:207], v[6:9]
	v_mfma_f32_16x16x32_bf16 v[2:5], v[172:175], v[204:207], v[2:5]
	s_setprio 0
	s_barrier
	v_add_u32_e32 v152, vcc_hi, v138
	v_add_u32_e32 v167, s39, v138
	ds_read_b128 v[140:143], v152
	ds_read_b128 v[144:147], v152 offset:1024
	ds_read_b128 v[148:151], v152 offset:2048
	ds_read_b128 v[152:155], v152 offset:3072
	ds_read_b128 v[156:159], v167
	ds_read_b128 v[160:163], v167 offset:1024
	ds_read_b128 v[168:171], v167 offset:2048
	ds_read_b128 v[172:175], v167 offset:3072
	s_mov_b32 m0, s84
	v_lshl_add_u64 v[220:221], s[70:71], 0, v[128:129]
	ds_read_b128 v[176:179], v139 offset:32768
	ds_read_b128 v[180:183], v139 offset:33792
	ds_read_b128 v[184:187], v139 offset:34816
	ds_read_b128 v[188:191], v139 offset:35840
	ds_read_b128 v[192:195], v139 offset:36864
	ds_read_b128 v[196:199], v139 offset:37888
	ds_read_b128 v[200:203], v139 offset:38912
	ds_read_b128 v[204:207], v139 offset:39936
	global_load_lds_dwordx4 v[220:221], off
	s_mov_b32 m0, s90
	v_lshl_add_u64 v[220:221], s[70:71], 0, v[124:125]
	global_load_lds_dwordx4 v[220:221], off
	s_waitcnt vmcnt(8)
	s_waitcnt lgkmcnt(0)
	s_barrier
	s_setprio 1
	s_waitcnt lgkmcnt(0)
	v_mfma_f32_16x16x32_bf16 v[134:137], v[140:143], v[176:179], v[134:137]
	v_mfma_f32_16x16x32_bf16 v[130:133], v[148:151], v[176:179], v[130:133]
	v_mfma_f32_16x16x32_bf16 v[110:113], v[140:143], v[184:187], v[110:113]
	v_mfma_f32_16x16x32_bf16 v[106:109], v[148:151], v[184:187], v[106:109]
	v_mfma_f32_16x16x32_bf16 v[94:97], v[140:143], v[192:195], v[94:97]
	v_mfma_f32_16x16x32_bf16 v[90:93], v[148:151], v[192:195], v[90:93]
	v_mfma_f32_16x16x32_bf16 v[78:81], v[140:143], v[200:203], v[78:81]
	v_mfma_f32_16x16x32_bf16 v[74:77], v[148:151], v[200:203], v[74:77]
	v_mfma_f32_16x16x32_bf16 v[134:137], v[144:147], v[180:183], v[134:137]
	v_mfma_f32_16x16x32_bf16 v[130:133], v[152:155], v[180:183], v[130:133]
	v_mfma_f32_16x16x32_bf16 v[110:113], v[144:147], v[188:191], v[110:113]
	v_mfma_f32_16x16x32_bf16 v[106:109], v[152:155], v[188:191], v[106:109]
	v_mfma_f32_16x16x32_bf16 v[94:97], v[144:147], v[196:199], v[94:97]
	v_mfma_f32_16x16x32_bf16 v[90:93], v[152:155], v[196:199], v[90:93]
	v_mfma_f32_16x16x32_bf16 v[78:81], v[144:147], v[204:207], v[78:81]
	v_mfma_f32_16x16x32_bf16 v[74:77], v[152:155], v[204:207], v[74:77]
	s_setprio 0
	s_setprio 1
	v_mfma_f32_16x16x32_bf16 v[118:121], v[156:159], v[176:179], v[118:121]
	v_mfma_f32_16x16x32_bf16 v[114:117], v[168:171], v[176:179], v[114:117]
	v_mfma_f32_16x16x32_bf16 v[102:105], v[156:159], v[184:187], v[102:105]
	v_mfma_f32_16x16x32_bf16 v[98:101], v[168:171], v[184:187], v[98:101]
	v_mfma_f32_16x16x32_bf16 v[86:89], v[156:159], v[192:195], v[86:89]
	v_mfma_f32_16x16x32_bf16 v[82:85], v[168:171], v[192:195], v[82:85]
	v_mfma_f32_16x16x32_bf16 v[70:73], v[156:159], v[200:203], v[70:73]
	v_mfma_f32_16x16x32_bf16 v[66:69], v[168:171], v[200:203], v[66:69]
	v_mfma_f32_16x16x32_bf16 v[118:121], v[160:163], v[180:183], v[118:121]
	v_mfma_f32_16x16x32_bf16 v[114:117], v[172:175], v[180:183], v[114:117]
	v_mfma_f32_16x16x32_bf16 v[102:105], v[160:163], v[188:191], v[102:105]
	v_mfma_f32_16x16x32_bf16 v[98:101], v[172:175], v[188:191], v[98:101]
	v_mfma_f32_16x16x32_bf16 v[86:89], v[160:163], v[196:199], v[86:89]
	v_mfma_f32_16x16x32_bf16 v[82:85], v[172:175], v[196:199], v[82:85]
	v_mfma_f32_16x16x32_bf16 v[70:73], v[160:163], v[204:207], v[70:73]
	v_mfma_f32_16x16x32_bf16 v[66:69], v[172:175], v[204:207], v[66:69]
	s_setprio 0
	s_barrier
	s_mov_b32 m0, vcc_lo
	v_lshl_add_u64 v[164:165], v[164:165], 0, s[56:57]
	ds_read_b128 v[176:179], v139 offset:49152
	ds_read_b128 v[180:183], v139 offset:50176
	ds_read_b128 v[184:187], v139 offset:51200
	ds_read_b128 v[188:191], v139 offset:52224
	ds_read_b128 v[192:195], v139 offset:53248
	ds_read_b128 v[196:199], v139 offset:54272
	ds_read_b128 v[200:203], v139 offset:55296
	ds_read_b128 v[204:207], v139 offset:56320
	global_load_lds_dwordx4 v[164:165], off
	s_mov_b32 m0, s64
	v_lshl_add_u64 v[164:165], v[208:209], 0, s[56:57]
	global_load_lds_dwordx4 v[164:165], off
	s_mov_b32 m0, s91
	v_lshl_add_u64 v[164:165], s[62:63], 0, v[126:127]
	global_load_lds_dwordx4 v[164:165], off
	s_mov_b32 m0, s38
	v_lshl_add_u64 v[164:165], s[62:63], 0, v[122:123]
	global_load_lds_dwordx4 v[164:165], off
	s_mov_b32 m0, s68
	v_lshl_add_u64 v[164:165], v[216:217], 0, s[56:57]
	global_load_lds_dwordx4 v[164:165], off
	s_mov_b32 m0, s22
	v_lshl_add_u64 v[164:165], v[218:219], 0, s[56:57]
	global_load_lds_dwordx4 v[164:165], off
	s_waitcnt vmcnt(8)
	s_waitcnt lgkmcnt(0)
	s_barrier
	s_setprio 1
	s_waitcnt lgkmcnt(0)
	v_mfma_f32_16x16x32_bf16 v[62:65], v[140:143], v[176:179], v[62:65]
	v_mfma_f32_16x16x32_bf16 v[58:61], v[148:151], v[176:179], v[58:61]
	v_mfma_f32_16x16x32_bf16 v[46:49], v[140:143], v[184:187], v[46:49]
	v_mfma_f32_16x16x32_bf16 v[42:45], v[148:151], v[184:187], v[42:45]
	v_mfma_f32_16x16x32_bf16 v[30:33], v[140:143], v[192:195], v[30:33]
	v_mfma_f32_16x16x32_bf16 v[26:29], v[148:151], v[192:195], v[26:29]
	v_mfma_f32_16x16x32_bf16 v[14:17], v[140:143], v[200:203], v[14:17]
	v_mfma_f32_16x16x32_bf16 v[10:13], v[148:151], v[200:203], v[10:13]
	v_mfma_f32_16x16x32_bf16 v[62:65], v[144:147], v[180:183], v[62:65]
	v_mfma_f32_16x16x32_bf16 v[58:61], v[152:155], v[180:183], v[58:61]
	v_mfma_f32_16x16x32_bf16 v[46:49], v[144:147], v[188:191], v[46:49]
	v_mfma_f32_16x16x32_bf16 v[42:45], v[152:155], v[188:191], v[42:45]
	v_mfma_f32_16x16x32_bf16 v[30:33], v[144:147], v[196:199], v[30:33]
	v_mfma_f32_16x16x32_bf16 v[26:29], v[152:155], v[196:199], v[26:29]
	v_mfma_f32_16x16x32_bf16 v[14:17], v[144:147], v[204:207], v[14:17]
	v_mfma_f32_16x16x32_bf16 v[10:13], v[152:155], v[204:207], v[10:13]
	s_setprio 0
	s_setprio 1
	v_mfma_f32_16x16x32_bf16 v[54:57], v[156:159], v[176:179], v[54:57]
	v_mfma_f32_16x16x32_bf16 v[50:53], v[168:171], v[176:179], v[50:53]
	v_mfma_f32_16x16x32_bf16 v[38:41], v[156:159], v[184:187], v[38:41]
	v_mfma_f32_16x16x32_bf16 v[34:37], v[168:171], v[184:187], v[34:37]
	v_mfma_f32_16x16x32_bf16 v[22:25], v[156:159], v[192:195], v[22:25]
	v_mfma_f32_16x16x32_bf16 v[18:21], v[168:171], v[192:195], v[18:21]
	v_mfma_f32_16x16x32_bf16 v[6:9], v[156:159], v[200:203], v[6:9]
	v_mfma_f32_16x16x32_bf16 v[2:5], v[168:171], v[200:203], v[2:5]
	v_mfma_f32_16x16x32_bf16 v[54:57], v[160:163], v[180:183], v[54:57]
	v_mfma_f32_16x16x32_bf16 v[50:53], v[172:175], v[180:183], v[50:53]
	v_mfma_f32_16x16x32_bf16 v[38:41], v[160:163], v[188:191], v[38:41]
	v_mfma_f32_16x16x32_bf16 v[34:37], v[172:175], v[188:191], v[34:37]
	v_mfma_f32_16x16x32_bf16 v[22:25], v[160:163], v[196:199], v[22:25]
	v_mfma_f32_16x16x32_bf16 v[18:21], v[172:175], v[196:199], v[18:21]
	v_mfma_f32_16x16x32_bf16 v[6:9], v[160:163], v[204:207], v[6:9]
	v_mfma_f32_16x16x32_bf16 v[2:5], v[172:175], v[204:207], v[2:5]
	s_setprio 0
	s_barrier
	s_movk_i32 s38, 0x100
	s_andn2_b64 vcc, exec, s[52:53]
	s_mov_b64 s[62:63], -1
	s_mov_b64 s[52:53], 0
	s_cbranch_vccz .LBB0_2367
	s_andn2_b64 vcc, exec, s[42:43]
	s_cbranch_vccnz .LBB0_2359
	v_mov_b32_e32 v2, 0
	s_mov_b32 s16, s36
	s_mov_b32 s94, s44
	s_mov_b64 s[30:31], s[48:49]
	s_mov_b64 s[34:35], s[46:47]
	s_mov_b32 s58, s23
	v_mov_b32_e32 v3, v2
	v_mov_b32_e32 v4, v2
	v_mov_b32_e32 v5, v2
	v_mov_b32_e32 v6, v2
	v_mov_b32_e32 v7, v2
	v_mov_b32_e32 v8, v2
	v_mov_b32_e32 v9, v2
	v_mov_b32_e32 v18, v2
	v_mov_b32_e32 v19, v2
	v_mov_b32_e32 v20, v2
	v_mov_b32_e32 v21, v2
	v_mov_b32_e32 v22, v2
	v_mov_b32_e32 v23, v2
	v_mov_b32_e32 v24, v2
	v_mov_b32_e32 v25, v2
	v_mov_b32_e32 v34, v2
	v_mov_b32_e32 v35, v2
	v_mov_b32_e32 v36, v2
	v_mov_b32_e32 v37, v2
	v_mov_b32_e32 v38, v2
	v_mov_b32_e32 v39, v2
	v_mov_b32_e32 v40, v2
	v_mov_b32_e32 v41, v2
	v_mov_b32_e32 v50, v2
	v_mov_b32_e32 v51, v2
	v_mov_b32_e32 v52, v2
	v_mov_b32_e32 v53, v2
	v_mov_b32_e32 v54, v2
	v_mov_b32_e32 v55, v2
	v_mov_b32_e32 v56, v2
	v_mov_b32_e32 v57, v2
	v_mov_b32_e32 v10, v2
	v_mov_b32_e32 v11, v2
	v_mov_b32_e32 v12, v2
	v_mov_b32_e32 v13, v2
	v_mov_b32_e32 v14, v2
	v_mov_b32_e32 v15, v2
	v_mov_b32_e32 v16, v2
	v_mov_b32_e32 v17, v2
	v_mov_b32_e32 v26, v2
	v_mov_b32_e32 v27, v2
	v_mov_b32_e32 v28, v2
	v_mov_b32_e32 v29, v2
	v_mov_b32_e32 v30, v2
	v_mov_b32_e32 v31, v2
	v_mov_b32_e32 v32, v2
	v_mov_b32_e32 v33, v2
	v_mov_b32_e32 v42, v2
	v_mov_b32_e32 v43, v2
	v_mov_b32_e32 v44, v2
	v_mov_b32_e32 v45, v2
	v_mov_b32_e32 v46, v2
	v_mov_b32_e32 v47, v2
	v_mov_b32_e32 v48, v2
	v_mov_b32_e32 v49, v2
	v_mov_b32_e32 v58, v2
	v_mov_b32_e32 v59, v2
	v_mov_b32_e32 v60, v2
	v_mov_b32_e32 v61, v2
	v_mov_b32_e32 v62, v2
	v_mov_b32_e32 v63, v2
	v_mov_b32_e32 v64, v2
	v_mov_b32_e32 v65, v2
	v_mov_b32_e32 v66, v2
	v_mov_b32_e32 v67, v2
	v_mov_b32_e32 v68, v2
	v_mov_b32_e32 v69, v2
	v_mov_b32_e32 v70, v2
	v_mov_b32_e32 v71, v2
	v_mov_b32_e32 v72, v2
	v_mov_b32_e32 v73, v2
	v_mov_b32_e32 v82, v2
	v_mov_b32_e32 v83, v2
	v_mov_b32_e32 v84, v2
	v_mov_b32_e32 v85, v2
	v_mov_b32_e32 v86, v2
	v_mov_b32_e32 v87, v2
	v_mov_b32_e32 v88, v2
	v_mov_b32_e32 v89, v2
	v_mov_b32_e32 v98, v2
	v_mov_b32_e32 v99, v2
	v_mov_b32_e32 v100, v2
	v_mov_b32_e32 v101, v2
	v_mov_b32_e32 v102, v2
	v_mov_b32_e32 v103, v2
	v_mov_b32_e32 v104, v2
	v_mov_b32_e32 v105, v2
	v_mov_b32_e32 v114, v2
	v_mov_b32_e32 v115, v2
	v_mov_b32_e32 v116, v2
	v_mov_b32_e32 v117, v2
	v_mov_b32_e32 v118, v2
	v_mov_b32_e32 v119, v2
	v_mov_b32_e32 v120, v2
	v_mov_b32_e32 v121, v2
	v_mov_b32_e32 v74, v2
	v_mov_b32_e32 v75, v2
	v_mov_b32_e32 v76, v2
	v_mov_b32_e32 v77, v2
	v_mov_b32_e32 v78, v2
	v_mov_b32_e32 v79, v2
	v_mov_b32_e32 v80, v2
	v_mov_b32_e32 v81, v2
	v_mov_b32_e32 v90, v2
	v_mov_b32_e32 v91, v2
	v_mov_b32_e32 v92, v2
	v_mov_b32_e32 v93, v2
	v_mov_b32_e32 v94, v2
	v_mov_b32_e32 v95, v2
	v_mov_b32_e32 v96, v2
	v_mov_b32_e32 v97, v2
	v_mov_b32_e32 v106, v2
	v_mov_b32_e32 v107, v2
	v_mov_b32_e32 v108, v2
	v_mov_b32_e32 v109, v2
	v_mov_b32_e32 v110, v2
	v_mov_b32_e32 v111, v2
	v_mov_b32_e32 v112, v2
	v_mov_b32_e32 v113, v2
	v_mov_b32_e32 v130, v2
	v_mov_b32_e32 v131, v2
	v_mov_b32_e32 v132, v2
	v_mov_b32_e32 v133, v2
	v_mov_b32_e32 v134, v2
	v_mov_b32_e32 v135, v2
	v_mov_b32_e32 v136, v2
	v_mov_b32_e32 v137, v2
	s_branch .LBB0_2359

.LBB0_2467:
	s_add_u32 s8, s30, s12
	s_addc_u32 s9, s31, 0
	s_add_u32 s13, s8, 0x100
	s_addc_u32 s50, s9, 0
	s_and_b64 s[10:11], s[48:49], exec
	s_cselect_b32 s63, s37, s50
	s_cselect_b32 s62, s59, s13
	s_add_u32 s10, s28, s12
	s_addc_u32 s11, s29, 0
	s_add_u32 s12, s10, 0x100
	s_addc_u32 s13, s11, 0
	s_add_i32 s50, 0, 0x10000
	s_and_b64 s[10:11], s[48:49], exec
	s_cselect_b32 s71, s35, s13
	s_cselect_b32 s70, s96, s12
	s_add_i32 s12, 0, 0x14000
	s_add_u32 s10, s8, 0x10080
	s_addc_u32 s11, s9, 0
	s_add_i32 s9, s50, s81
	s_add_i32 m0, s82, 0xc000
	s_add_i32 s8, s82, 0xe000
	s_add_i32 s64, s9, 0x2000
	s_add_u32 s76, s70, 0x10000
	s_addc_u32 s77, s71, 0
	s_add_i32 s65, s12, s81
	v_add_u32_e32 v152, s50, v138
	v_add_u32_e32 v168, s12, v138
	s_add_i32 s74, s65, 0x2000
	s_add_i32 s91, 0, 0x18000
	s_add_i32 s13, 0, 0x1c000
	ds_read_b128 v[140:143], v152
	ds_read_b128 v[144:147], v152 offset:1024
	ds_read_b128 v[148:151], v152 offset:2048
	ds_read_b128 v[152:155], v152 offset:3072
	ds_read_b128 v[156:159], v168
	ds_read_b128 v[160:163], v168 offset:1024
	ds_read_b128 v[164:167], v168 offset:2048
	ds_read_b128 v[168:171], v168 offset:3072
	s_add_u32 s52, s62, 0x10000
	s_addc_u32 s53, s63, 0
	s_add_i32 vcc_hi, s91, s81
	s_add_i32 vcc_lo, vcc_hi, 0x2000
	s_add_u32 s48, s70, 0x10080
	s_addc_u32 s49, s71, 0
	s_add_i32 s50, s13, s81
	s_add_i32 s12, s50, 0x2000
	v_lshl_add_u64 v[204:205], s[10:11], 0, v[128:129]
	ds_read_b128 v[172:175], v139
	ds_read_b128 v[176:179], v139 offset:1024
	ds_read_b128 v[180:183], v139 offset:2048
	ds_read_b128 v[184:187], v139 offset:3072
	ds_read_b128 v[188:191], v139 offset:4096
	ds_read_b128 v[192:195], v139 offset:5120
	ds_read_b128 v[196:199], v139 offset:6144
	ds_read_b128 v[200:203], v139 offset:7168
	global_load_lds_dwordx4 v[204:205], off
	s_mov_b32 m0, s8
	v_lshl_add_u64 v[204:205], s[10:11], 0, v[124:125]
	global_load_lds_dwordx4 v[204:205], off
	s_waitcnt vmcnt(8)
	s_waitcnt lgkmcnt(0)
	s_barrier
	s_setprio 1
	s_waitcnt lgkmcnt(0)
	v_mfma_f32_16x16x32_bf16 v[134:137], v[140:143], v[172:175], v[134:137]
	v_mfma_f32_16x16x32_bf16 v[130:133], v[148:151], v[172:175], v[130:133]
	v_mfma_f32_16x16x32_bf16 v[110:113], v[140:143], v[180:183], v[110:113]
	v_mfma_f32_16x16x32_bf16 v[106:109], v[148:151], v[180:183], v[106:109]
	v_mfma_f32_16x16x32_bf16 v[94:97], v[140:143], v[188:191], v[94:97]
	v_mfma_f32_16x16x32_bf16 v[90:93], v[148:151], v[188:191], v[90:93]
	v_mfma_f32_16x16x32_bf16 v[78:81], v[140:143], v[196:199], v[78:81]
	v_mfma_f32_16x16x32_bf16 v[74:77], v[148:151], v[196:199], v[74:77]
	v_mfma_f32_16x16x32_bf16 v[134:137], v[144:147], v[176:179], v[134:137]
	v_mfma_f32_16x16x32_bf16 v[130:133], v[152:155], v[176:179], v[130:133]
	v_mfma_f32_16x16x32_bf16 v[110:113], v[144:147], v[184:187], v[110:113]
	v_mfma_f32_16x16x32_bf16 v[106:109], v[152:155], v[184:187], v[106:109]
	v_mfma_f32_16x16x32_bf16 v[94:97], v[144:147], v[192:195], v[94:97]
	v_mfma_f32_16x16x32_bf16 v[90:93], v[152:155], v[192:195], v[90:93]
	v_mfma_f32_16x16x32_bf16 v[78:81], v[144:147], v[200:203], v[78:81]
	v_mfma_f32_16x16x32_bf16 v[74:77], v[152:155], v[200:203], v[74:77]
	s_setprio 0
	s_setprio 1
	v_mfma_f32_16x16x32_bf16 v[118:121], v[156:159], v[172:175], v[118:121]
	v_mfma_f32_16x16x32_bf16 v[114:117], v[164:167], v[172:175], v[114:117]
	v_mfma_f32_16x16x32_bf16 v[102:105], v[156:159], v[180:183], v[102:105]
	v_mfma_f32_16x16x32_bf16 v[98:101], v[164:167], v[180:183], v[98:101]
	v_mfma_f32_16x16x32_bf16 v[86:89], v[156:159], v[188:191], v[86:89]
	v_mfma_f32_16x16x32_bf16 v[82:85], v[164:167], v[188:191], v[82:85]
	v_mfma_f32_16x16x32_bf16 v[70:73], v[156:159], v[196:199], v[70:73]
	v_mfma_f32_16x16x32_bf16 v[66:69], v[164:167], v[196:199], v[66:69]
	v_mfma_f32_16x16x32_bf16 v[118:121], v[160:163], v[176:179], v[118:121]
	v_mfma_f32_16x16x32_bf16 v[114:117], v[168:171], v[176:179], v[114:117]
	v_mfma_f32_16x16x32_bf16 v[102:105], v[160:163], v[184:187], v[102:105]
	v_mfma_f32_16x16x32_bf16 v[98:101], v[168:171], v[184:187], v[98:101]
	v_mfma_f32_16x16x32_bf16 v[86:89], v[160:163], v[192:195], v[86:89]
	v_mfma_f32_16x16x32_bf16 v[82:85], v[168:171], v[192:195], v[82:85]
	v_mfma_f32_16x16x32_bf16 v[70:73], v[160:163], v[200:203], v[70:73]
	v_mfma_f32_16x16x32_bf16 v[66:69], v[168:171], v[200:203], v[66:69]
	s_setprio 0
	s_barrier
	s_mov_b32 m0, s9
	v_lshl_add_u64 v[204:205], s[70:71], 0, v[126:127]
	ds_read_b128 v[172:175], v139 offset:16384
	ds_read_b128 v[176:179], v139 offset:17408
	ds_read_b128 v[180:183], v139 offset:18432
	ds_read_b128 v[184:187], v139 offset:19456
	ds_read_b128 v[188:191], v139 offset:20480
	ds_read_b128 v[192:195], v139 offset:21504
	ds_read_b128 v[196:199], v139 offset:22528
	ds_read_b128 v[200:203], v139 offset:23552
	global_load_lds_dwordx4 v[204:205], off
	v_lshl_add_u64 v[206:207], s[70:71], 0, v[122:123]
	s_mov_b32 m0, s64
	v_lshl_add_u64 v[208:209], s[76:77], 0, v[126:127]
	global_load_lds_dwordx4 v[206:207], off
	s_mov_b32 m0, s65
	v_lshl_add_u64 v[216:217], s[62:63], 0, v[124:125]
	global_load_lds_dwordx4 v[208:209], off
	s_mov_b32 m0, s74
	v_lshl_add_u64 v[208:209], s[76:77], 0, v[122:123]
	global_load_lds_dwordx4 v[208:209], off
	s_mov_b32 m0, s82
	v_lshl_add_u64 v[208:209], s[62:63], 0, v[128:129]
	global_load_lds_dwordx4 v[208:209], off
	s_mov_b32 m0, s92
	s_nop 0
	global_load_lds_dwordx4 v[216:217], off
	s_waitcnt vmcnt(8)
	s_waitcnt lgkmcnt(0)
	s_barrier
	s_setprio 1
	s_waitcnt lgkmcnt(0)
	v_mfma_f32_16x16x32_bf16 v[62:65], v[140:143], v[172:175], v[62:65]
	v_mfma_f32_16x16x32_bf16 v[58:61], v[148:151], v[172:175], v[58:61]
	v_mfma_f32_16x16x32_bf16 v[46:49], v[140:143], v[180:183], v[46:49]
	v_mfma_f32_16x16x32_bf16 v[42:45], v[148:151], v[180:183], v[42:45]
	v_mfma_f32_16x16x32_bf16 v[30:33], v[140:143], v[188:191], v[30:33]
	v_mfma_f32_16x16x32_bf16 v[26:29], v[148:151], v[188:191], v[26:29]
	v_mfma_f32_16x16x32_bf16 v[14:17], v[140:143], v[196:199], v[14:17]
	v_mfma_f32_16x16x32_bf16 v[10:13], v[148:151], v[196:199], v[10:13]
	v_mfma_f32_16x16x32_bf16 v[62:65], v[144:147], v[176:179], v[62:65]
	v_mfma_f32_16x16x32_bf16 v[58:61], v[152:155], v[176:179], v[58:61]
	v_mfma_f32_16x16x32_bf16 v[46:49], v[144:147], v[184:187], v[46:49]
	v_mfma_f32_16x16x32_bf16 v[42:45], v[152:155], v[184:187], v[42:45]
	v_mfma_f32_16x16x32_bf16 v[30:33], v[144:147], v[192:195], v[30:33]
	v_mfma_f32_16x16x32_bf16 v[26:29], v[152:155], v[192:195], v[26:29]
	v_mfma_f32_16x16x32_bf16 v[14:17], v[144:147], v[200:203], v[14:17]
	v_mfma_f32_16x16x32_bf16 v[10:13], v[152:155], v[200:203], v[10:13]
	s_setprio 0
	s_setprio 1
	v_mfma_f32_16x16x32_bf16 v[54:57], v[156:159], v[172:175], v[54:57]
	v_mfma_f32_16x16x32_bf16 v[50:53], v[164:167], v[172:175], v[50:53]
	v_mfma_f32_16x16x32_bf16 v[38:41], v[156:159], v[180:183], v[38:41]
	v_mfma_f32_16x16x32_bf16 v[34:37], v[164:167], v[180:183], v[34:37]
	v_mfma_f32_16x16x32_bf16 v[22:25], v[156:159], v[188:191], v[22:25]
	v_mfma_f32_16x16x32_bf16 v[18:21], v[164:167], v[188:191], v[18:21]
	v_mfma_f32_16x16x32_bf16 v[6:9], v[156:159], v[196:199], v[6:9]
	v_mfma_f32_16x16x32_bf16 v[2:5], v[164:167], v[196:199], v[2:5]
	v_mfma_f32_16x16x32_bf16 v[54:57], v[160:163], v[176:179], v[54:57]
	v_mfma_f32_16x16x32_bf16 v[50:53], v[168:171], v[176:179], v[50:53]
	v_mfma_f32_16x16x32_bf16 v[38:41], v[160:163], v[184:187], v[38:41]
	v_mfma_f32_16x16x32_bf16 v[34:37], v[168:171], v[184:187], v[34:37]
	v_mfma_f32_16x16x32_bf16 v[22:25], v[160:163], v[192:195], v[22:25]
	v_mfma_f32_16x16x32_bf16 v[18:21], v[168:171], v[192:195], v[18:21]
	v_mfma_f32_16x16x32_bf16 v[6:9], v[160:163], v[200:203], v[6:9]
	v_mfma_f32_16x16x32_bf16 v[2:5], v[168:171], v[200:203], v[2:5]
	s_setprio 0
	s_barrier
	v_add_u32_e32 v152, s91, v138
	v_add_u32_e32 v168, s13, v138
	ds_read_b128 v[140:143], v152
	ds_read_b128 v[144:147], v152 offset:1024
	ds_read_b128 v[148:151], v152 offset:2048
	ds_read_b128 v[152:155], v152 offset:3072
	ds_read_b128 v[156:159], v168
	ds_read_b128 v[160:163], v168 offset:1024
	ds_read_b128 v[164:167], v168 offset:2048
	ds_read_b128 v[168:171], v168 offset:3072
	s_mov_b32 m0, s84
	v_lshl_add_u64 v[218:219], s[52:53], 0, v[128:129]
	ds_read_b128 v[172:175], v139 offset:32768
	ds_read_b128 v[176:179], v139 offset:33792
	ds_read_b128 v[180:183], v139 offset:34816
	ds_read_b128 v[184:187], v139 offset:35840
	ds_read_b128 v[188:191], v139 offset:36864
	ds_read_b128 v[192:195], v139 offset:37888
	ds_read_b128 v[196:199], v139 offset:38912
	ds_read_b128 v[200:203], v139 offset:39936
	global_load_lds_dwordx4 v[218:219], off
	s_mov_b32 m0, s90
	v_lshl_add_u64 v[218:219], s[52:53], 0, v[124:125]
	global_load_lds_dwordx4 v[218:219], off
	s_waitcnt vmcnt(8)
	s_waitcnt lgkmcnt(0)
	s_barrier
	s_setprio 1
	s_waitcnt lgkmcnt(0)
	v_mfma_f32_16x16x32_bf16 v[134:137], v[140:143], v[172:175], v[134:137]
	v_mfma_f32_16x16x32_bf16 v[130:133], v[148:151], v[172:175], v[130:133]
	v_mfma_f32_16x16x32_bf16 v[110:113], v[140:143], v[180:183], v[110:113]
	v_mfma_f32_16x16x32_bf16 v[106:109], v[148:151], v[180:183], v[106:109]
	v_mfma_f32_16x16x32_bf16 v[94:97], v[140:143], v[188:191], v[94:97]
	v_mfma_f32_16x16x32_bf16 v[90:93], v[148:151], v[188:191], v[90:93]
	v_mfma_f32_16x16x32_bf16 v[78:81], v[140:143], v[196:199], v[78:81]
	v_mfma_f32_16x16x32_bf16 v[74:77], v[148:151], v[196:199], v[74:77]
	v_mfma_f32_16x16x32_bf16 v[134:137], v[144:147], v[176:179], v[134:137]
	v_mfma_f32_16x16x32_bf16 v[130:133], v[152:155], v[176:179], v[130:133]
	v_mfma_f32_16x16x32_bf16 v[110:113], v[144:147], v[184:187], v[110:113]
	v_mfma_f32_16x16x32_bf16 v[106:109], v[152:155], v[184:187], v[106:109]
	v_mfma_f32_16x16x32_bf16 v[94:97], v[144:147], v[192:195], v[94:97]
	v_mfma_f32_16x16x32_bf16 v[90:93], v[152:155], v[192:195], v[90:93]
	v_mfma_f32_16x16x32_bf16 v[78:81], v[144:147], v[200:203], v[78:81]
	v_mfma_f32_16x16x32_bf16 v[74:77], v[152:155], v[200:203], v[74:77]
	s_setprio 0
	s_setprio 1
	v_mfma_f32_16x16x32_bf16 v[118:121], v[156:159], v[172:175], v[118:121]
	v_mfma_f32_16x16x32_bf16 v[114:117], v[164:167], v[172:175], v[114:117]
	v_mfma_f32_16x16x32_bf16 v[102:105], v[156:159], v[180:183], v[102:105]
	v_mfma_f32_16x16x32_bf16 v[98:101], v[164:167], v[180:183], v[98:101]
	v_mfma_f32_16x16x32_bf16 v[86:89], v[156:159], v[188:191], v[86:89]
	v_mfma_f32_16x16x32_bf16 v[82:85], v[164:167], v[188:191], v[82:85]
	v_mfma_f32_16x16x32_bf16 v[70:73], v[156:159], v[196:199], v[70:73]
	v_mfma_f32_16x16x32_bf16 v[66:69], v[164:167], v[196:199], v[66:69]
	v_mfma_f32_16x16x32_bf16 v[118:121], v[160:163], v[176:179], v[118:121]
	v_mfma_f32_16x16x32_bf16 v[114:117], v[168:171], v[176:179], v[114:117]
	v_mfma_f32_16x16x32_bf16 v[102:105], v[160:163], v[184:187], v[102:105]
	v_mfma_f32_16x16x32_bf16 v[98:101], v[168:171], v[184:187], v[98:101]
	v_mfma_f32_16x16x32_bf16 v[86:89], v[160:163], v[192:195], v[86:89]
	v_mfma_f32_16x16x32_bf16 v[82:85], v[168:171], v[192:195], v[82:85]
	v_mfma_f32_16x16x32_bf16 v[70:73], v[160:163], v[200:203], v[70:73]
	v_mfma_f32_16x16x32_bf16 v[66:69], v[168:171], v[200:203], v[66:69]
	s_setprio 0
	s_barrier
	s_mov_b32 m0, vcc_hi
	v_lshl_add_u64 v[204:205], v[204:205], 0, s[56:57]
	ds_read_b128 v[172:175], v139 offset:49152
	ds_read_b128 v[176:179], v139 offset:50176
	ds_read_b128 v[180:183], v139 offset:51200
	ds_read_b128 v[184:187], v139 offset:52224
	ds_read_b128 v[188:191], v139 offset:53248
	ds_read_b128 v[192:195], v139 offset:54272
	ds_read_b128 v[196:199], v139 offset:55296
	ds_read_b128 v[200:203], v139 offset:56320
	global_load_lds_dwordx4 v[204:205], off
	s_mov_b32 m0, vcc_lo
	v_lshl_add_u64 v[204:205], v[206:207], 0, s[56:57]
	global_load_lds_dwordx4 v[204:205], off
	s_mov_b32 m0, s50
	v_lshl_add_u64 v[204:205], s[48:49], 0, v[126:127]
	global_load_lds_dwordx4 v[204:205], off
	s_mov_b32 m0, s12
	v_lshl_add_u64 v[204:205], s[48:49], 0, v[122:123]
	global_load_lds_dwordx4 v[204:205], off
	s_mov_b32 m0, s68
	v_lshl_add_u64 v[204:205], v[208:209], 0, s[56:57]
	global_load_lds_dwordx4 v[204:205], off
	s_mov_b32 m0, s93
	v_lshl_add_u64 v[204:205], v[216:217], 0, s[56:57]
	global_load_lds_dwordx4 v[204:205], off
	s_waitcnt vmcnt(8)
	s_waitcnt lgkmcnt(0)
	s_barrier
	s_setprio 1
	s_waitcnt lgkmcnt(0)
	v_mfma_f32_16x16x32_bf16 v[62:65], v[140:143], v[172:175], v[62:65]
	v_mfma_f32_16x16x32_bf16 v[58:61], v[148:151], v[172:175], v[58:61]
	v_mfma_f32_16x16x32_bf16 v[46:49], v[140:143], v[180:183], v[46:49]
	v_mfma_f32_16x16x32_bf16 v[42:45], v[148:151], v[180:183], v[42:45]
	v_mfma_f32_16x16x32_bf16 v[30:33], v[140:143], v[188:191], v[30:33]
	v_mfma_f32_16x16x32_bf16 v[26:29], v[148:151], v[188:191], v[26:29]
	v_mfma_f32_16x16x32_bf16 v[14:17], v[140:143], v[196:199], v[14:17]
	v_mfma_f32_16x16x32_bf16 v[10:13], v[148:151], v[196:199], v[10:13]
	v_mfma_f32_16x16x32_bf16 v[62:65], v[144:147], v[176:179], v[62:65]
	v_mfma_f32_16x16x32_bf16 v[58:61], v[152:155], v[176:179], v[58:61]
	v_mfma_f32_16x16x32_bf16 v[46:49], v[144:147], v[184:187], v[46:49]
	v_mfma_f32_16x16x32_bf16 v[42:45], v[152:155], v[184:187], v[42:45]
	v_mfma_f32_16x16x32_bf16 v[30:33], v[144:147], v[192:195], v[30:33]
	v_mfma_f32_16x16x32_bf16 v[26:29], v[152:155], v[192:195], v[26:29]
	v_mfma_f32_16x16x32_bf16 v[14:17], v[144:147], v[200:203], v[14:17]
	v_mfma_f32_16x16x32_bf16 v[10:13], v[152:155], v[200:203], v[10:13]
	s_setprio 0
	s_setprio 1
	v_mfma_f32_16x16x32_bf16 v[54:57], v[156:159], v[172:175], v[54:57]
	v_mfma_f32_16x16x32_bf16 v[50:53], v[164:167], v[172:175], v[50:53]
	v_mfma_f32_16x16x32_bf16 v[38:41], v[156:159], v[180:183], v[38:41]
	v_mfma_f32_16x16x32_bf16 v[34:37], v[164:167], v[180:183], v[34:37]
	v_mfma_f32_16x16x32_bf16 v[22:25], v[156:159], v[188:191], v[22:25]
	v_mfma_f32_16x16x32_bf16 v[18:21], v[164:167], v[188:191], v[18:21]
	v_mfma_f32_16x16x32_bf16 v[6:9], v[156:159], v[196:199], v[6:9]
	v_mfma_f32_16x16x32_bf16 v[2:5], v[164:167], v[196:199], v[2:5]
	v_mfma_f32_16x16x32_bf16 v[54:57], v[160:163], v[176:179], v[54:57]
	v_mfma_f32_16x16x32_bf16 v[50:53], v[168:171], v[176:179], v[50:53]
	v_mfma_f32_16x16x32_bf16 v[38:41], v[160:163], v[184:187], v[38:41]
	v_mfma_f32_16x16x32_bf16 v[34:37], v[168:171], v[184:187], v[34:37]
	v_mfma_f32_16x16x32_bf16 v[22:25], v[160:163], v[192:195], v[22:25]
	v_mfma_f32_16x16x32_bf16 v[18:21], v[168:171], v[192:195], v[18:21]
	v_mfma_f32_16x16x32_bf16 v[6:9], v[160:163], v[200:203], v[6:9]
	v_mfma_f32_16x16x32_bf16 v[2:5], v[168:171], v[200:203], v[2:5]
	s_setprio 0
	s_barrier
	s_movk_i32 s12, 0x100
	s_andn2_b64 vcc, exec, s[46:47]
	s_mov_b64 s[48:49], -1
	s_mov_b64 s[46:47], 0
	s_cbranch_vccz .LBB0_2467
	s_andn2_b64 vcc, exec, s[40:41]
	s_cbranch_vccnz .LBB0_2459
	v_mov_b32_e32 v2, 0
	s_mov_b32 s14, s34
	s_mov_b32 s95, s36
	s_mov_b64 s[28:29], s[44:45]
	s_mov_b64 s[30:31], s[42:43]
	s_mov_b32 s94, s58
	v_mov_b32_e32 v3, v2
	v_mov_b32_e32 v4, v2
	v_mov_b32_e32 v5, v2
	v_mov_b32_e32 v6, v2
	v_mov_b32_e32 v7, v2
	v_mov_b32_e32 v8, v2
	v_mov_b32_e32 v9, v2
	v_mov_b32_e32 v18, v2
	v_mov_b32_e32 v19, v2
	v_mov_b32_e32 v20, v2
	v_mov_b32_e32 v21, v2
	v_mov_b32_e32 v22, v2
	v_mov_b32_e32 v23, v2
	v_mov_b32_e32 v24, v2
	v_mov_b32_e32 v25, v2
	v_mov_b32_e32 v34, v2
	v_mov_b32_e32 v35, v2
	v_mov_b32_e32 v36, v2
	v_mov_b32_e32 v37, v2
	v_mov_b32_e32 v38, v2
	v_mov_b32_e32 v39, v2
	v_mov_b32_e32 v40, v2
	v_mov_b32_e32 v41, v2
	v_mov_b32_e32 v50, v2
	v_mov_b32_e32 v51, v2
	v_mov_b32_e32 v52, v2
	v_mov_b32_e32 v53, v2
	v_mov_b32_e32 v54, v2
	v_mov_b32_e32 v55, v2
	v_mov_b32_e32 v56, v2
	v_mov_b32_e32 v57, v2
	v_mov_b32_e32 v10, v2
	v_mov_b32_e32 v11, v2
	v_mov_b32_e32 v12, v2
	v_mov_b32_e32 v13, v2
	v_mov_b32_e32 v14, v2
	v_mov_b32_e32 v15, v2
	v_mov_b32_e32 v16, v2
	v_mov_b32_e32 v17, v2
	v_mov_b32_e32 v26, v2
	v_mov_b32_e32 v27, v2
	v_mov_b32_e32 v28, v2
	v_mov_b32_e32 v29, v2
	v_mov_b32_e32 v30, v2
	v_mov_b32_e32 v31, v2
	v_mov_b32_e32 v32, v2
	v_mov_b32_e32 v33, v2
	v_mov_b32_e32 v42, v2
	v_mov_b32_e32 v43, v2
	v_mov_b32_e32 v44, v2
	v_mov_b32_e32 v45, v2
	v_mov_b32_e32 v46, v2
	v_mov_b32_e32 v47, v2
	v_mov_b32_e32 v48, v2
	v_mov_b32_e32 v49, v2
	v_mov_b32_e32 v58, v2
	v_mov_b32_e32 v59, v2
	v_mov_b32_e32 v60, v2
	v_mov_b32_e32 v61, v2
	v_mov_b32_e32 v62, v2
	v_mov_b32_e32 v63, v2
	v_mov_b32_e32 v64, v2
	v_mov_b32_e32 v65, v2
	v_mov_b32_e32 v66, v2
	v_mov_b32_e32 v67, v2
	v_mov_b32_e32 v68, v2
	v_mov_b32_e32 v69, v2
	v_mov_b32_e32 v70, v2
	v_mov_b32_e32 v71, v2
	v_mov_b32_e32 v72, v2
	v_mov_b32_e32 v73, v2
	v_mov_b32_e32 v82, v2
	v_mov_b32_e32 v83, v2
	v_mov_b32_e32 v84, v2
	v_mov_b32_e32 v85, v2
	v_mov_b32_e32 v86, v2
	v_mov_b32_e32 v87, v2
	v_mov_b32_e32 v88, v2
	v_mov_b32_e32 v89, v2
	v_mov_b32_e32 v98, v2
	v_mov_b32_e32 v99, v2
	v_mov_b32_e32 v100, v2
	v_mov_b32_e32 v101, v2
	v_mov_b32_e32 v102, v2
	v_mov_b32_e32 v103, v2
	v_mov_b32_e32 v104, v2
	v_mov_b32_e32 v105, v2
	v_mov_b32_e32 v114, v2
	v_mov_b32_e32 v115, v2
	v_mov_b32_e32 v116, v2
	v_mov_b32_e32 v117, v2
	v_mov_b32_e32 v118, v2
	v_mov_b32_e32 v119, v2
	v_mov_b32_e32 v120, v2
	v_mov_b32_e32 v121, v2
	v_mov_b32_e32 v74, v2
	v_mov_b32_e32 v75, v2
	v_mov_b32_e32 v76, v2
	v_mov_b32_e32 v77, v2
	v_mov_b32_e32 v78, v2
	v_mov_b32_e32 v79, v2
	v_mov_b32_e32 v80, v2
	v_mov_b32_e32 v81, v2
	v_mov_b32_e32 v90, v2
	v_mov_b32_e32 v91, v2
	v_mov_b32_e32 v92, v2
	v_mov_b32_e32 v93, v2
	v_mov_b32_e32 v94, v2
	v_mov_b32_e32 v95, v2
	v_mov_b32_e32 v96, v2
	v_mov_b32_e32 v97, v2
	v_mov_b32_e32 v106, v2
	v_mov_b32_e32 v107, v2
	v_mov_b32_e32 v108, v2
	v_mov_b32_e32 v109, v2
	v_mov_b32_e32 v110, v2
	v_mov_b32_e32 v111, v2
	v_mov_b32_e32 v112, v2
	v_mov_b32_e32 v113, v2
	v_mov_b32_e32 v130, v2
	v_mov_b32_e32 v131, v2
	v_mov_b32_e32 v132, v2
	v_mov_b32_e32 v133, v2
	v_mov_b32_e32 v134, v2
	v_mov_b32_e32 v135, v2
	v_mov_b32_e32 v136, v2
	v_mov_b32_e32 v137, v2
	s_branch .LBB0_2459

.Lnobar_c6:
.LBB0_2626:
	s_add_u32 s26, s6, 0xfffc0080
	s_addc_u32 s27, s7, -1
	s_add_i32 s50, 0, 0x10000
	s_cmp_eq_u32 s49, 12
	s_cselect_b32 s29, s21, s27
	s_cselect_b32 s28, s33, s26
	v_add_u32_e32 v0, s50, v181
	s_cselect_b32 s27, s19, s48
	s_cselect_b32 s26, s40, s41
	s_add_i32 s58, 0, 0x14000
	ds_read_b128 v[130:133], v0
	ds_read_b128 v[134:137], v0 offset:1024
	ds_read_b128 v[138:141], v0 offset:2048
	ds_read_b128 v[142:145], v0 offset:3072
	v_add_u32_e32 v0, s58, v181
	ds_read_b128 v[146:149], v0
	ds_read_b128 v[150:153], v0 offset:1024
	ds_read_b128 v[154:157], v0 offset:2048
	ds_read_b128 v[170:173], v0 offset:3072
	v_lshl_add_u64 v[178:179], s[6:7], 0, v[168:169]
	s_add_i32 m0, s36, 0xc000
	ds_read_b128 v[174:177], v183
	ds_read_b128 v[184:187], v183 offset:1024
	ds_read_b128 v[188:191], v183 offset:2048
	ds_read_b128 v[192:195], v183 offset:3072
	ds_read_b128 v[196:199], v183 offset:4096
	ds_read_b128 v[200:203], v183 offset:5120
	ds_read_b128 v[204:207], v183 offset:6144
	ds_read_b128 v[216:219], v183 offset:7168
	global_load_lds_dwordx4 v[178:179], off
	s_add_i32 m0, s36, 0xe000
	v_lshl_add_u64 v[178:179], s[6:7], 0, v[166:167]
	global_load_lds_dwordx4 v[178:179], off
	s_waitcnt vmcnt(8)
	s_waitcnt lgkmcnt(0)
	s_barrier
	s_setprio 1
	s_waitcnt lgkmcnt(0)
	v_mfma_f32_16x16x32_bf16 v[126:129], v[130:133], v[174:177], v[126:129]
	v_mfma_f32_16x16x32_bf16 v[122:125], v[138:141], v[174:177], v[122:125]
	v_mfma_f32_16x16x32_bf16 v[110:113], v[130:133], v[188:191], v[110:113]
	v_mfma_f32_16x16x32_bf16 v[106:109], v[138:141], v[188:191], v[106:109]
	v_mfma_f32_16x16x32_bf16 v[94:97], v[130:133], v[196:199], v[94:97]
	v_mfma_f32_16x16x32_bf16 v[90:93], v[138:141], v[196:199], v[90:93]
	v_mfma_f32_16x16x32_bf16 v[78:81], v[130:133], v[204:207], v[78:81]
	v_mfma_f32_16x16x32_bf16 v[74:77], v[138:141], v[204:207], v[74:77]
	v_mfma_f32_16x16x32_bf16 v[126:129], v[134:137], v[184:187], v[126:129]
	v_mfma_f32_16x16x32_bf16 v[122:125], v[142:145], v[184:187], v[122:125]
	v_mfma_f32_16x16x32_bf16 v[110:113], v[134:137], v[192:195], v[110:113]
	v_mfma_f32_16x16x32_bf16 v[106:109], v[142:145], v[192:195], v[106:109]
	v_mfma_f32_16x16x32_bf16 v[94:97], v[134:137], v[200:203], v[94:97]
	v_mfma_f32_16x16x32_bf16 v[90:93], v[142:145], v[200:203], v[90:93]
	v_mfma_f32_16x16x32_bf16 v[78:81], v[134:137], v[216:219], v[78:81]
	v_mfma_f32_16x16x32_bf16 v[74:77], v[142:145], v[216:219], v[74:77]
	s_setprio 0
	s_setprio 1
	v_mfma_f32_16x16x32_bf16 v[118:121], v[146:149], v[174:177], v[118:121]
	v_mfma_f32_16x16x32_bf16 v[114:117], v[154:157], v[174:177], v[114:117]
	v_mfma_f32_16x16x32_bf16 v[102:105], v[146:149], v[188:191], v[102:105]
	v_mfma_f32_16x16x32_bf16 v[98:101], v[154:157], v[188:191], v[98:101]
	v_mfma_f32_16x16x32_bf16 v[86:89], v[146:149], v[196:199], v[86:89]
	v_mfma_f32_16x16x32_bf16 v[82:85], v[154:157], v[196:199], v[82:85]
	v_mfma_f32_16x16x32_bf16 v[70:73], v[146:149], v[204:207], v[70:73]
	v_mfma_f32_16x16x32_bf16 v[66:69], v[154:157], v[204:207], v[66:69]
	v_mfma_f32_16x16x32_bf16 v[118:121], v[150:153], v[184:187], v[118:121]
	v_mfma_f32_16x16x32_bf16 v[114:117], v[170:173], v[184:187], v[114:117]
	v_mfma_f32_16x16x32_bf16 v[102:105], v[150:153], v[192:195], v[102:105]
	v_mfma_f32_16x16x32_bf16 v[98:101], v[170:173], v[192:195], v[98:101]
	v_mfma_f32_16x16x32_bf16 v[86:89], v[150:153], v[200:203], v[86:89]
	v_mfma_f32_16x16x32_bf16 v[82:85], v[170:173], v[200:203], v[82:85]
	v_mfma_f32_16x16x32_bf16 v[70:73], v[150:153], v[216:219], v[70:73]
	v_mfma_f32_16x16x32_bf16 v[66:69], v[170:173], v[216:219], v[66:69]
	s_setprio 0
	s_barrier
	s_add_i32 s50, s50, s35
	v_lshl_add_u64 v[178:179], s[26:27], 0, v[162:163]
	s_mov_b32 m0, s50
	ds_read_b128 v[174:177], v183 offset:16384
	ds_read_b128 v[184:187], v183 offset:17408
	ds_read_b128 v[188:191], v183 offset:18432
	ds_read_b128 v[192:195], v183 offset:19456
	ds_read_b128 v[196:199], v183 offset:20480
	ds_read_b128 v[200:203], v183 offset:21504
	ds_read_b128 v[204:207], v183 offset:22528
	ds_read_b128 v[216:219], v183 offset:23552
	global_load_lds_dwordx4 v[178:179], off
	s_add_i32 m0, s50, 0x2000
	s_add_u32 s52, s26, 0x40000
	v_lshl_add_u64 v[208:209], s[26:27], 0, v[158:159]
	s_addc_u32 s53, s27, 0
	s_add_i32 s50, s58, s35
	global_load_lds_dwordx4 v[208:209], off
	v_lshl_add_u64 v[220:221], s[52:53], 0, v[162:163]
	s_mov_b32 m0, s50
	v_lshl_add_u64 v[222:223], s[28:29], 0, v[160:161]
	global_load_lds_dwordx4 v[220:221], off
	s_add_i32 m0, s50, 0x2000
	v_lshl_add_u64 v[220:221], s[52:53], 0, v[158:159]
	global_load_lds_dwordx4 v[220:221], off
	s_mov_b32 m0, s36
	v_lshl_add_u64 v[220:221], s[28:29], 0, v[164:165]
	global_load_lds_dwordx4 v[220:221], off
	s_mov_b32 m0, s37
	s_nop 0
	global_load_lds_dwordx4 v[222:223], off
	s_waitcnt vmcnt(8)
	s_waitcnt lgkmcnt(0)
	s_barrier
	s_setprio 1
	s_waitcnt lgkmcnt(0)
	v_mfma_f32_16x16x32_bf16 v[62:65], v[130:133], v[174:177], v[62:65]
	v_mfma_f32_16x16x32_bf16 v[58:61], v[138:141], v[174:177], v[58:61]
	v_mfma_f32_16x16x32_bf16 v[46:49], v[130:133], v[188:191], v[46:49]
	v_mfma_f32_16x16x32_bf16 v[42:45], v[138:141], v[188:191], v[42:45]
	v_mfma_f32_16x16x32_bf16 v[30:33], v[130:133], v[196:199], v[30:33]
	v_mfma_f32_16x16x32_bf16 v[26:29], v[138:141], v[196:199], v[26:29]
	v_mfma_f32_16x16x32_bf16 v[14:17], v[130:133], v[204:207], v[14:17]
	v_mfma_f32_16x16x32_bf16 v[10:13], v[138:141], v[204:207], v[10:13]
	v_mfma_f32_16x16x32_bf16 v[62:65], v[134:137], v[184:187], v[62:65]
	v_mfma_f32_16x16x32_bf16 v[58:61], v[142:145], v[184:187], v[58:61]
	v_mfma_f32_16x16x32_bf16 v[46:49], v[134:137], v[192:195], v[46:49]
	v_mfma_f32_16x16x32_bf16 v[42:45], v[142:145], v[192:195], v[42:45]
	v_mfma_f32_16x16x32_bf16 v[30:33], v[134:137], v[200:203], v[30:33]
	v_mfma_f32_16x16x32_bf16 v[26:29], v[142:145], v[200:203], v[26:29]
	v_mfma_f32_16x16x32_bf16 v[14:17], v[134:137], v[216:219], v[14:17]
	v_mfma_f32_16x16x32_bf16 v[10:13], v[142:145], v[216:219], v[10:13]
	s_setprio 0
	s_setprio 1
	v_mfma_f32_16x16x32_bf16 v[54:57], v[146:149], v[174:177], v[54:57]
	v_mfma_f32_16x16x32_bf16 v[50:53], v[154:157], v[174:177], v[50:53]
	v_mfma_f32_16x16x32_bf16 v[38:41], v[146:149], v[188:191], v[38:41]
	v_mfma_f32_16x16x32_bf16 v[34:37], v[154:157], v[188:191], v[34:37]
	v_mfma_f32_16x16x32_bf16 v[22:25], v[146:149], v[196:199], v[22:25]
	v_mfma_f32_16x16x32_bf16 v[18:21], v[154:157], v[196:199], v[18:21]
	v_mfma_f32_16x16x32_bf16 v[6:9], v[146:149], v[204:207], v[6:9]
	v_mfma_f32_16x16x32_bf16 v[2:5], v[154:157], v[204:207], v[2:5]
	v_mfma_f32_16x16x32_bf16 v[54:57], v[150:153], v[184:187], v[54:57]
	v_mfma_f32_16x16x32_bf16 v[50:53], v[170:173], v[184:187], v[50:53]
	v_mfma_f32_16x16x32_bf16 v[38:41], v[150:153], v[192:195], v[38:41]
	v_mfma_f32_16x16x32_bf16 v[34:37], v[170:173], v[192:195], v[34:37]
	v_mfma_f32_16x16x32_bf16 v[22:25], v[150:153], v[200:203], v[22:25]
	v_mfma_f32_16x16x32_bf16 v[18:21], v[170:173], v[200:203], v[18:21]
	v_mfma_f32_16x16x32_bf16 v[6:9], v[150:153], v[216:219], v[6:9]
	v_mfma_f32_16x16x32_bf16 v[2:5], v[170:173], v[216:219], v[2:5]
	s_setprio 0
	s_barrier
	s_add_i32 s50, 0, 0x18000
	v_add_u32_e32 v0, s50, v181
	s_add_i32 s52, 0, 0x1c000
	ds_read_b128 v[130:133], v0
	ds_read_b128 v[134:137], v0 offset:1024
	ds_read_b128 v[138:141], v0 offset:2048
	ds_read_b128 v[142:145], v0 offset:3072
	v_add_u32_e32 v0, s52, v181
	ds_read_b128 v[146:149], v0
	ds_read_b128 v[150:153], v0 offset:1024
	ds_read_b128 v[154:157], v0 offset:2048
	ds_read_b128 v[170:173], v0 offset:3072
	s_add_u32 s28, s28, 0x40000
	s_addc_u32 s29, s29, 0
	s_mov_b32 m0, s42
	v_lshl_add_u64 v[224:225], s[28:29], 0, v[164:165]
	ds_read_b128 v[174:177], v183 offset:32768
	ds_read_b128 v[184:187], v183 offset:33792
	ds_read_b128 v[188:191], v183 offset:34816
	ds_read_b128 v[192:195], v183 offset:35840
	ds_read_b128 v[196:199], v183 offset:36864
	ds_read_b128 v[200:203], v183 offset:37888
	ds_read_b128 v[204:207], v183 offset:38912
	ds_read_b128 v[216:219], v183 offset:39936
	global_load_lds_dwordx4 v[224:225], off
	s_mov_b32 m0, s43
	v_lshl_add_u64 v[224:225], s[28:29], 0, v[160:161]
	global_load_lds_dwordx4 v[224:225], off
	s_waitcnt vmcnt(8)
	s_waitcnt lgkmcnt(0)
	s_barrier
	s_setprio 1
	s_waitcnt lgkmcnt(0)
	v_mfma_f32_16x16x32_bf16 v[126:129], v[130:133], v[174:177], v[126:129]
	v_mfma_f32_16x16x32_bf16 v[122:125], v[138:141], v[174:177], v[122:125]
	v_mfma_f32_16x16x32_bf16 v[110:113], v[130:133], v[188:191], v[110:113]
	v_mfma_f32_16x16x32_bf16 v[106:109], v[138:141], v[188:191], v[106:109]
	v_mfma_f32_16x16x32_bf16 v[94:97], v[130:133], v[196:199], v[94:97]
	v_mfma_f32_16x16x32_bf16 v[90:93], v[138:141], v[196:199], v[90:93]
	v_mfma_f32_16x16x32_bf16 v[78:81], v[130:133], v[204:207], v[78:81]
	v_mfma_f32_16x16x32_bf16 v[74:77], v[138:141], v[204:207], v[74:77]
	v_mfma_f32_16x16x32_bf16 v[126:129], v[134:137], v[184:187], v[126:129]
	v_mfma_f32_16x16x32_bf16 v[122:125], v[142:145], v[184:187], v[122:125]
	v_mfma_f32_16x16x32_bf16 v[110:113], v[134:137], v[192:195], v[110:113]
	v_mfma_f32_16x16x32_bf16 v[106:109], v[142:145], v[192:195], v[106:109]
	v_mfma_f32_16x16x32_bf16 v[94:97], v[134:137], v[200:203], v[94:97]
	v_mfma_f32_16x16x32_bf16 v[90:93], v[142:145], v[200:203], v[90:93]
	v_mfma_f32_16x16x32_bf16 v[78:81], v[134:137], v[216:219], v[78:81]
	v_mfma_f32_16x16x32_bf16 v[74:77], v[142:145], v[216:219], v[74:77]
	s_setprio 0
	s_setprio 1
	v_mfma_f32_16x16x32_bf16 v[118:121], v[146:149], v[174:177], v[118:121]
	v_mfma_f32_16x16x32_bf16 v[114:117], v[154:157], v[174:177], v[114:117]
	v_mfma_f32_16x16x32_bf16 v[102:105], v[146:149], v[188:191], v[102:105]
	v_mfma_f32_16x16x32_bf16 v[98:101], v[154:157], v[188:191], v[98:101]
	v_mfma_f32_16x16x32_bf16 v[86:89], v[146:149], v[196:199], v[86:89]
	v_mfma_f32_16x16x32_bf16 v[82:85], v[154:157], v[196:199], v[82:85]
	v_mfma_f32_16x16x32_bf16 v[70:73], v[146:149], v[204:207], v[70:73]
	v_mfma_f32_16x16x32_bf16 v[66:69], v[154:157], v[204:207], v[66:69]
	v_mfma_f32_16x16x32_bf16 v[118:121], v[150:153], v[184:187], v[118:121]
	v_mfma_f32_16x16x32_bf16 v[114:117], v[170:173], v[184:187], v[114:117]
	v_mfma_f32_16x16x32_bf16 v[102:105], v[150:153], v[192:195], v[102:105]
	v_mfma_f32_16x16x32_bf16 v[98:101], v[170:173], v[192:195], v[98:101]
	v_mfma_f32_16x16x32_bf16 v[86:89], v[150:153], v[200:203], v[86:89]
	v_mfma_f32_16x16x32_bf16 v[82:85], v[170:173], v[200:203], v[82:85]
	v_mfma_f32_16x16x32_bf16 v[70:73], v[150:153], v[216:219], v[70:73]
	v_mfma_f32_16x16x32_bf16 v[66:69], v[170:173], v[216:219], v[66:69]
	s_setprio 0
	s_barrier
	s_add_i32 s28, s50, s35
	v_lshl_add_u64 v[178:179], v[178:179], 0, s[56:57]
	s_mov_b32 m0, s28
	ds_read_b128 v[174:177], v183 offset:49152
	ds_read_b128 v[184:187], v183 offset:50176
	ds_read_b128 v[188:191], v183 offset:51200
	ds_read_b128 v[192:195], v183 offset:52224
	ds_read_b128 v[196:199], v183 offset:53248
	ds_read_b128 v[200:203], v183 offset:54272
	ds_read_b128 v[204:207], v183 offset:55296
	ds_read_b128 v[216:219], v183 offset:56320
	global_load_lds_dwordx4 v[178:179], off
	s_add_i32 m0, s28, 0x2000
	s_add_u32 s26, s26, 0x40080
	v_lshl_add_u64 v[178:179], v[208:209], 0, s[56:57]
	s_addc_u32 s27, s27, 0
	s_add_i32 s28, s52, s35
	global_load_lds_dwordx4 v[178:179], off
	s_mov_b32 m0, s28
	v_lshl_add_u64 v[178:179], s[26:27], 0, v[162:163]
	global_load_lds_dwordx4 v[178:179], off
	s_add_i32 m0, s28, 0x2000
	v_lshl_add_u64 v[178:179], s[26:27], 0, v[158:159]
	global_load_lds_dwordx4 v[178:179], off
	s_mov_b32 m0, s44
	v_lshl_add_u64 v[178:179], v[220:221], 0, s[56:57]
	global_load_lds_dwordx4 v[178:179], off
	s_mov_b32 m0, s45
	v_lshl_add_u64 v[178:179], v[222:223], 0, s[56:57]
	global_load_lds_dwordx4 v[178:179], off
	s_waitcnt vmcnt(8)
	s_waitcnt lgkmcnt(0)
	s_barrier
	s_setprio 1
	s_waitcnt lgkmcnt(0)
	v_mfma_f32_16x16x32_bf16 v[62:65], v[130:133], v[174:177], v[62:65]
	v_mfma_f32_16x16x32_bf16 v[58:61], v[138:141], v[174:177], v[58:61]
	v_mfma_f32_16x16x32_bf16 v[46:49], v[130:133], v[188:191], v[46:49]
	v_mfma_f32_16x16x32_bf16 v[42:45], v[138:141], v[188:191], v[42:45]
	v_mfma_f32_16x16x32_bf16 v[30:33], v[130:133], v[196:199], v[30:33]
	v_mfma_f32_16x16x32_bf16 v[26:29], v[138:141], v[196:199], v[26:29]
	v_mfma_f32_16x16x32_bf16 v[14:17], v[130:133], v[204:207], v[14:17]
	v_mfma_f32_16x16x32_bf16 v[10:13], v[138:141], v[204:207], v[10:13]
	v_mfma_f32_16x16x32_bf16 v[62:65], v[134:137], v[184:187], v[62:65]
	v_mfma_f32_16x16x32_bf16 v[58:61], v[142:145], v[184:187], v[58:61]
	v_mfma_f32_16x16x32_bf16 v[46:49], v[134:137], v[192:195], v[46:49]
	v_mfma_f32_16x16x32_bf16 v[42:45], v[142:145], v[192:195], v[42:45]
	v_mfma_f32_16x16x32_bf16 v[30:33], v[134:137], v[200:203], v[30:33]
	v_mfma_f32_16x16x32_bf16 v[26:29], v[142:145], v[200:203], v[26:29]
	v_mfma_f32_16x16x32_bf16 v[14:17], v[134:137], v[216:219], v[14:17]
	v_mfma_f32_16x16x32_bf16 v[10:13], v[142:145], v[216:219], v[10:13]
	s_setprio 0
	s_setprio 1
	v_mfma_f32_16x16x32_bf16 v[54:57], v[146:149], v[174:177], v[54:57]
	v_mfma_f32_16x16x32_bf16 v[50:53], v[154:157], v[174:177], v[50:53]
	v_mfma_f32_16x16x32_bf16 v[38:41], v[146:149], v[188:191], v[38:41]
	v_mfma_f32_16x16x32_bf16 v[34:37], v[154:157], v[188:191], v[34:37]
	v_mfma_f32_16x16x32_bf16 v[22:25], v[146:149], v[196:199], v[22:25]
	v_mfma_f32_16x16x32_bf16 v[18:21], v[154:157], v[196:199], v[18:21]
	v_mfma_f32_16x16x32_bf16 v[6:9], v[146:149], v[204:207], v[6:9]
	v_mfma_f32_16x16x32_bf16 v[2:5], v[154:157], v[204:207], v[2:5]
	v_mfma_f32_16x16x32_bf16 v[54:57], v[150:153], v[184:187], v[54:57]
	v_mfma_f32_16x16x32_bf16 v[50:53], v[170:173], v[184:187], v[50:53]
	v_mfma_f32_16x16x32_bf16 v[38:41], v[150:153], v[192:195], v[38:41]
	v_mfma_f32_16x16x32_bf16 v[34:37], v[170:173], v[192:195], v[34:37]
	v_mfma_f32_16x16x32_bf16 v[22:25], v[150:153], v[200:203], v[22:25]
	v_mfma_f32_16x16x32_bf16 v[18:21], v[170:173], v[200:203], v[18:21]
	v_mfma_f32_16x16x32_bf16 v[6:9], v[150:153], v[216:219], v[6:9]
	v_mfma_f32_16x16x32_bf16 v[2:5], v[170:173], v[216:219], v[2:5]
	s_setprio 0
	s_barrier
	s_add_i32 s49, s49, 2
	s_add_u32 s41, s41, 0x100
	s_addc_u32 s48, s48, 0
	s_add_u32 s6, s6, 0x100
	s_addc_u32 s7, s7, 0
	s_cmp_gt_u32 s49, 13
	s_cbranch_scc0 .LBB0_2626
	s_and_b64 vcc, exec, s[16:17]
	s_cbranch_vccz .LBB0_2629
	s_barrier

.LBB0_2703:
	s_add_u32 s44, s24, s36
	s_addc_u32 s45, s25, s37
	s_add_u32 s44, s44, 0x100
	s_addc_u32 s45, s45, 0
	s_add_u32 s50, s59, s36
	s_addc_u32 s64, s82, s37
	s_add_i32 s65, 0, 0x10000
	s_cmpk_eq_i32 s36, 0x1f00
	s_cselect_b32 s47, s29, s45
	s_cselect_b32 s46, s83, s44
	s_cselect_b32 s45, s27, s64
	s_cselect_b32 s44, s84, s50
	s_add_i32 s50, 0, 0x14000
	v_add_u32_e32 v160, s65, v146
	v_add_u32_e32 v164, s50, v146
	ds_read_b128 v[148:151], v160
	ds_read_b128 v[152:155], v160 offset:1024
	ds_read_b128 v[156:159], v160 offset:2048
	ds_read_b128 v[160:163], v160 offset:3072
	ds_read_b128 v[168:171], v164
	ds_read_b128 v[172:175], v164 offset:1024
	ds_read_b128 v[176:179], v164 offset:2048
	ds_read_b128 v[180:183], v164 offset:3072
	v_lshl_add_u64 v[164:165], v[144:145], 0, s[36:37]
	s_add_i32 m0, s4, 0xc000
	ds_read_b128 v[184:187], v147
	ds_read_b128 v[188:191], v147 offset:1024
	ds_read_b128 v[192:195], v147 offset:2048
	ds_read_b128 v[196:199], v147 offset:3072
	ds_read_b128 v[200:203], v147 offset:4096
	ds_read_b128 v[204:207], v147 offset:5120
	ds_read_b128 v[216:219], v147 offset:6144
	ds_read_b128 v[220:223], v147 offset:7168
	global_load_lds_dwordx4 v[164:165], off
	s_add_i32 m0, s4, 0xe000
	v_lshl_add_u64 v[164:165], v[142:143], 0, s[36:37]
	global_load_lds_dwordx4 v[164:165], off
	s_waitcnt vmcnt(8)
	s_waitcnt lgkmcnt(0)
	s_barrier
	s_setprio 1
	s_waitcnt lgkmcnt(0)
	v_mfma_f32_16x16x32_bf16 v[134:137], v[148:151], v[184:187], v[134:137]
	v_mfma_f32_16x16x32_bf16 v[130:133], v[156:159], v[184:187], v[130:133]
	v_mfma_f32_16x16x32_bf16 v[110:113], v[148:151], v[192:195], v[110:113]
	v_mfma_f32_16x16x32_bf16 v[106:109], v[156:159], v[192:195], v[106:109]
	v_mfma_f32_16x16x32_bf16 v[94:97], v[148:151], v[200:203], v[94:97]
	v_mfma_f32_16x16x32_bf16 v[90:93], v[156:159], v[200:203], v[90:93]
	v_mfma_f32_16x16x32_bf16 v[78:81], v[148:151], v[216:219], v[78:81]
	v_mfma_f32_16x16x32_bf16 v[74:77], v[156:159], v[216:219], v[74:77]
	v_mfma_f32_16x16x32_bf16 v[134:137], v[152:155], v[188:191], v[134:137]
	v_mfma_f32_16x16x32_bf16 v[130:133], v[160:163], v[188:191], v[130:133]
	v_mfma_f32_16x16x32_bf16 v[110:113], v[152:155], v[196:199], v[110:113]
	v_mfma_f32_16x16x32_bf16 v[106:109], v[160:163], v[196:199], v[106:109]
	v_mfma_f32_16x16x32_bf16 v[94:97], v[152:155], v[204:207], v[94:97]
	v_mfma_f32_16x16x32_bf16 v[90:93], v[160:163], v[204:207], v[90:93]
	v_mfma_f32_16x16x32_bf16 v[78:81], v[152:155], v[220:223], v[78:81]
	v_mfma_f32_16x16x32_bf16 v[74:77], v[160:163], v[220:223], v[74:77]
	s_setprio 0
	s_setprio 1
	v_mfma_f32_16x16x32_bf16 v[122:125], v[168:171], v[184:187], v[122:125]
	v_mfma_f32_16x16x32_bf16 v[114:117], v[176:179], v[184:187], v[114:117]
	v_mfma_f32_16x16x32_bf16 v[102:105], v[168:171], v[192:195], v[102:105]
	v_mfma_f32_16x16x32_bf16 v[98:101], v[176:179], v[192:195], v[98:101]
	v_mfma_f32_16x16x32_bf16 v[86:89], v[168:171], v[200:203], v[86:89]
	v_mfma_f32_16x16x32_bf16 v[82:85], v[176:179], v[200:203], v[82:85]
	v_mfma_f32_16x16x32_bf16 v[70:73], v[168:171], v[216:219], v[70:73]
	v_mfma_f32_16x16x32_bf16 v[66:69], v[176:179], v[216:219], v[66:69]
	v_mfma_f32_16x16x32_bf16 v[122:125], v[172:175], v[188:191], v[122:125]
	v_mfma_f32_16x16x32_bf16 v[114:117], v[180:183], v[188:191], v[114:117]
	v_mfma_f32_16x16x32_bf16 v[102:105], v[172:175], v[196:199], v[102:105]
	v_mfma_f32_16x16x32_bf16 v[98:101], v[180:183], v[196:199], v[98:101]
	v_mfma_f32_16x16x32_bf16 v[86:89], v[172:175], v[204:207], v[86:89]
	v_mfma_f32_16x16x32_bf16 v[82:85], v[180:183], v[204:207], v[82:85]
	v_mfma_f32_16x16x32_bf16 v[70:73], v[172:175], v[220:223], v[70:73]
	v_mfma_f32_16x16x32_bf16 v[66:69], v[180:183], v[220:223], v[66:69]
	s_setprio 0
	s_barrier
	s_add_i32 s64, s65, s77
	v_lshl_add_u64 v[164:165], s[44:45], 0, v[126:127]
	s_mov_b32 m0, s64
	ds_read_b128 v[184:187], v147 offset:16384
	ds_read_b128 v[188:191], v147 offset:17408
	ds_read_b128 v[192:195], v147 offset:18432
	ds_read_b128 v[196:199], v147 offset:19456
	ds_read_b128 v[200:203], v147 offset:20480
	ds_read_b128 v[204:207], v147 offset:21504
	ds_read_b128 v[216:219], v147 offset:22528
	ds_read_b128 v[220:223], v147 offset:23552
	global_load_lds_dwordx4 v[164:165], off
	s_add_i32 m0, s64, 0x2000
	s_add_u32 s92, s44, 0x100000
	v_lshl_add_u64 v[208:209], s[44:45], 0, v[118:119]
	s_addc_u32 s93, s45, 0
	s_add_i32 s50, s50, s77
	global_load_lds_dwordx4 v[208:209], off
	v_lshl_add_u64 v[224:225], s[92:93], 0, v[126:127]
	s_mov_b32 m0, s50
	v_lshl_add_u64 v[242:243], s[46:47], 0, v[120:121]
	global_load_lds_dwordx4 v[224:225], off
	s_add_i32 m0, s50, 0x2000
	v_lshl_add_u64 v[224:225], s[92:93], 0, v[118:119]
	global_load_lds_dwordx4 v[224:225], off
	s_mov_b32 m0, s4
	v_lshl_add_u64 v[224:225], s[46:47], 0, v[128:129]
	global_load_lds_dwordx4 v[224:225], off
	s_mov_b32 m0, s33
	s_nop 0
	global_load_lds_dwordx4 v[242:243], off
	s_waitcnt vmcnt(8)
	s_waitcnt lgkmcnt(0)
	s_barrier
	s_setprio 1
	s_waitcnt lgkmcnt(0)
	v_mfma_f32_16x16x32_bf16 v[62:65], v[148:151], v[184:187], v[62:65]
	v_mfma_f32_16x16x32_bf16 v[58:61], v[156:159], v[184:187], v[58:61]
	v_mfma_f32_16x16x32_bf16 v[46:49], v[148:151], v[192:195], v[46:49]
	v_mfma_f32_16x16x32_bf16 v[42:45], v[156:159], v[192:195], v[42:45]
	v_mfma_f32_16x16x32_bf16 v[30:33], v[148:151], v[200:203], v[30:33]
	v_mfma_f32_16x16x32_bf16 v[26:29], v[156:159], v[200:203], v[26:29]
	v_mfma_f32_16x16x32_bf16 v[14:17], v[148:151], v[216:219], v[14:17]
	v_mfma_f32_16x16x32_bf16 v[10:13], v[156:159], v[216:219], v[10:13]
	v_mfma_f32_16x16x32_bf16 v[62:65], v[152:155], v[188:191], v[62:65]
	v_mfma_f32_16x16x32_bf16 v[58:61], v[160:163], v[188:191], v[58:61]
	v_mfma_f32_16x16x32_bf16 v[46:49], v[152:155], v[196:199], v[46:49]
	v_mfma_f32_16x16x32_bf16 v[42:45], v[160:163], v[196:199], v[42:45]
	v_mfma_f32_16x16x32_bf16 v[30:33], v[152:155], v[204:207], v[30:33]
	v_mfma_f32_16x16x32_bf16 v[26:29], v[160:163], v[204:207], v[26:29]
	v_mfma_f32_16x16x32_bf16 v[14:17], v[152:155], v[220:223], v[14:17]
	v_mfma_f32_16x16x32_bf16 v[10:13], v[160:163], v[220:223], v[10:13]
	s_setprio 0
	s_setprio 1
	v_mfma_f32_16x16x32_bf16 v[54:57], v[168:171], v[184:187], v[54:57]
	v_mfma_f32_16x16x32_bf16 v[50:53], v[176:179], v[184:187], v[50:53]
	v_mfma_f32_16x16x32_bf16 v[38:41], v[168:171], v[192:195], v[38:41]
	v_mfma_f32_16x16x32_bf16 v[34:37], v[176:179], v[192:195], v[34:37]
	v_mfma_f32_16x16x32_bf16 v[22:25], v[168:171], v[200:203], v[22:25]
	v_mfma_f32_16x16x32_bf16 v[18:21], v[176:179], v[200:203], v[18:21]
	v_mfma_f32_16x16x32_bf16 v[6:9], v[168:171], v[216:219], v[6:9]
	v_mfma_f32_16x16x32_bf16 v[2:5], v[176:179], v[216:219], v[2:5]
	v_mfma_f32_16x16x32_bf16 v[54:57], v[172:175], v[188:191], v[54:57]
	v_mfma_f32_16x16x32_bf16 v[50:53], v[180:183], v[188:191], v[50:53]
	v_mfma_f32_16x16x32_bf16 v[38:41], v[172:175], v[196:199], v[38:41]
	v_mfma_f32_16x16x32_bf16 v[34:37], v[180:183], v[196:199], v[34:37]
	v_mfma_f32_16x16x32_bf16 v[22:25], v[172:175], v[204:207], v[22:25]
	v_mfma_f32_16x16x32_bf16 v[18:21], v[180:183], v[204:207], v[18:21]
	v_mfma_f32_16x16x32_bf16 v[6:9], v[172:175], v[220:223], v[6:9]
	v_mfma_f32_16x16x32_bf16 v[2:5], v[180:183], v[220:223], v[2:5]
	s_setprio 0
	s_barrier
	s_add_i32 s50, 0, 0x18000
	s_add_i32 s64, 0, 0x1c000
	v_add_u32_e32 v160, s50, v146
	v_add_u32_e32 v167, s64, v146
	ds_read_b128 v[148:151], v160
	ds_read_b128 v[152:155], v160 offset:1024
	ds_read_b128 v[156:159], v160 offset:2048
	ds_read_b128 v[160:163], v160 offset:3072
	ds_read_b128 v[168:171], v167
	ds_read_b128 v[172:175], v167 offset:1024
	ds_read_b128 v[176:179], v167 offset:2048
	ds_read_b128 v[180:183], v167 offset:3072
	s_add_u32 s46, s46, 0x100000
	s_addc_u32 s47, s47, 0
	s_mov_b32 m0, s78
	v_lshl_add_u64 v[244:245], s[46:47], 0, v[128:129]
	ds_read_b128 v[184:187], v147 offset:32768
	ds_read_b128 v[188:191], v147 offset:33792
	ds_read_b128 v[192:195], v147 offset:34816
	ds_read_b128 v[196:199], v147 offset:35840
	ds_read_b128 v[200:203], v147 offset:36864
	ds_read_b128 v[204:207], v147 offset:37888
	ds_read_b128 v[216:219], v147 offset:38912
	ds_read_b128 v[220:223], v147 offset:39936
	global_load_lds_dwordx4 v[244:245], off
	s_mov_b32 m0, s79
	v_lshl_add_u64 v[244:245], s[46:47], 0, v[120:121]
	global_load_lds_dwordx4 v[244:245], off
	s_waitcnt vmcnt(8)
	s_waitcnt lgkmcnt(0)
	s_barrier
	s_setprio 1
	s_waitcnt lgkmcnt(0)
	v_mfma_f32_16x16x32_bf16 v[134:137], v[148:151], v[184:187], v[134:137]
	v_mfma_f32_16x16x32_bf16 v[130:133], v[156:159], v[184:187], v[130:133]
	v_mfma_f32_16x16x32_bf16 v[110:113], v[148:151], v[192:195], v[110:113]
	v_mfma_f32_16x16x32_bf16 v[106:109], v[156:159], v[192:195], v[106:109]
	v_mfma_f32_16x16x32_bf16 v[94:97], v[148:151], v[200:203], v[94:97]
	v_mfma_f32_16x16x32_bf16 v[90:93], v[156:159], v[200:203], v[90:93]
	v_mfma_f32_16x16x32_bf16 v[78:81], v[148:151], v[216:219], v[78:81]
	v_mfma_f32_16x16x32_bf16 v[74:77], v[156:159], v[216:219], v[74:77]
	v_mfma_f32_16x16x32_bf16 v[134:137], v[152:155], v[188:191], v[134:137]
	v_mfma_f32_16x16x32_bf16 v[130:133], v[160:163], v[188:191], v[130:133]
	v_mfma_f32_16x16x32_bf16 v[110:113], v[152:155], v[196:199], v[110:113]
	v_mfma_f32_16x16x32_bf16 v[106:109], v[160:163], v[196:199], v[106:109]
	v_mfma_f32_16x16x32_bf16 v[94:97], v[152:155], v[204:207], v[94:97]
	v_mfma_f32_16x16x32_bf16 v[90:93], v[160:163], v[204:207], v[90:93]
	v_mfma_f32_16x16x32_bf16 v[78:81], v[152:155], v[220:223], v[78:81]
	v_mfma_f32_16x16x32_bf16 v[74:77], v[160:163], v[220:223], v[74:77]
	s_setprio 0
	s_setprio 1
	v_mfma_f32_16x16x32_bf16 v[122:125], v[168:171], v[184:187], v[122:125]
	v_mfma_f32_16x16x32_bf16 v[114:117], v[176:179], v[184:187], v[114:117]
	v_mfma_f32_16x16x32_bf16 v[102:105], v[168:171], v[192:195], v[102:105]
	v_mfma_f32_16x16x32_bf16 v[98:101], v[176:179], v[192:195], v[98:101]
	v_mfma_f32_16x16x32_bf16 v[86:89], v[168:171], v[200:203], v[86:89]
	v_mfma_f32_16x16x32_bf16 v[82:85], v[176:179], v[200:203], v[82:85]
	v_mfma_f32_16x16x32_bf16 v[70:73], v[168:171], v[216:219], v[70:73]
	v_mfma_f32_16x16x32_bf16 v[66:69], v[176:179], v[216:219], v[66:69]
	v_mfma_f32_16x16x32_bf16 v[122:125], v[172:175], v[188:191], v[122:125]
	v_mfma_f32_16x16x32_bf16 v[114:117], v[180:183], v[188:191], v[114:117]
	v_mfma_f32_16x16x32_bf16 v[102:105], v[172:175], v[196:199], v[102:105]
	v_mfma_f32_16x16x32_bf16 v[98:101], v[180:183], v[196:199], v[98:101]
	v_mfma_f32_16x16x32_bf16 v[86:89], v[172:175], v[204:207], v[86:89]
	v_mfma_f32_16x16x32_bf16 v[82:85], v[180:183], v[204:207], v[82:85]
	v_mfma_f32_16x16x32_bf16 v[70:73], v[172:175], v[220:223], v[70:73]
	v_mfma_f32_16x16x32_bf16 v[66:69], v[180:183], v[220:223], v[66:69]
	s_setprio 0
	s_barrier
	s_add_i32 s46, s50, s77
	v_lshl_add_u64 v[164:165], v[164:165], 0, s[56:57]
	s_mov_b32 m0, s46
	ds_read_b128 v[184:187], v147 offset:49152
	ds_read_b128 v[188:191], v147 offset:50176
	ds_read_b128 v[192:195], v147 offset:51200
	ds_read_b128 v[196:199], v147 offset:52224
	ds_read_b128 v[200:203], v147 offset:53248
	ds_read_b128 v[204:207], v147 offset:54272
	ds_read_b128 v[216:219], v147 offset:55296
	ds_read_b128 v[220:223], v147 offset:56320
	global_load_lds_dwordx4 v[164:165], off
	s_add_i32 m0, s46, 0x2000
	s_add_u32 s44, s44, 0x100080
	v_lshl_add_u64 v[164:165], v[208:209], 0, s[56:57]
	s_addc_u32 s45, s45, 0
	s_add_i32 s46, s64, s77
	global_load_lds_dwordx4 v[164:165], off
	s_mov_b32 m0, s46
	v_lshl_add_u64 v[164:165], s[44:45], 0, v[126:127]
	global_load_lds_dwordx4 v[164:165], off
	s_add_i32 m0, s46, 0x2000
	v_lshl_add_u64 v[164:165], s[44:45], 0, v[118:119]
	global_load_lds_dwordx4 v[164:165], off
	s_mov_b32 m0, s80
	v_lshl_add_u64 v[164:165], v[224:225], 0, s[56:57]
	global_load_lds_dwordx4 v[164:165], off
	s_mov_b32 m0, s81
	v_lshl_add_u64 v[164:165], v[242:243], 0, s[56:57]
	global_load_lds_dwordx4 v[164:165], off
	s_waitcnt vmcnt(8)
	s_waitcnt lgkmcnt(0)
	s_barrier
	s_setprio 1
	s_waitcnt lgkmcnt(0)
	v_mfma_f32_16x16x32_bf16 v[62:65], v[148:151], v[184:187], v[62:65]
	v_mfma_f32_16x16x32_bf16 v[58:61], v[156:159], v[184:187], v[58:61]
	v_mfma_f32_16x16x32_bf16 v[46:49], v[148:151], v[192:195], v[46:49]
	v_mfma_f32_16x16x32_bf16 v[42:45], v[156:159], v[192:195], v[42:45]
	v_mfma_f32_16x16x32_bf16 v[30:33], v[148:151], v[200:203], v[30:33]
	v_mfma_f32_16x16x32_bf16 v[26:29], v[156:159], v[200:203], v[26:29]
	v_mfma_f32_16x16x32_bf16 v[14:17], v[148:151], v[216:219], v[14:17]
	v_mfma_f32_16x16x32_bf16 v[10:13], v[156:159], v[216:219], v[10:13]
	v_mfma_f32_16x16x32_bf16 v[62:65], v[152:155], v[188:191], v[62:65]
	v_mfma_f32_16x16x32_bf16 v[58:61], v[160:163], v[188:191], v[58:61]
	v_mfma_f32_16x16x32_bf16 v[46:49], v[152:155], v[196:199], v[46:49]
	v_mfma_f32_16x16x32_bf16 v[42:45], v[160:163], v[196:199], v[42:45]
	v_mfma_f32_16x16x32_bf16 v[30:33], v[152:155], v[204:207], v[30:33]
	v_mfma_f32_16x16x32_bf16 v[26:29], v[160:163], v[204:207], v[26:29]
	v_mfma_f32_16x16x32_bf16 v[14:17], v[152:155], v[220:223], v[14:17]
	v_mfma_f32_16x16x32_bf16 v[10:13], v[160:163], v[220:223], v[10:13]
	s_setprio 0
	s_setprio 1
	v_mfma_f32_16x16x32_bf16 v[54:57], v[168:171], v[184:187], v[54:57]
	v_mfma_f32_16x16x32_bf16 v[50:53], v[176:179], v[184:187], v[50:53]
	v_mfma_f32_16x16x32_bf16 v[38:41], v[168:171], v[192:195], v[38:41]
	v_mfma_f32_16x16x32_bf16 v[34:37], v[176:179], v[192:195], v[34:37]
	v_mfma_f32_16x16x32_bf16 v[22:25], v[168:171], v[200:203], v[22:25]
	v_mfma_f32_16x16x32_bf16 v[18:21], v[176:179], v[200:203], v[18:21]
	v_mfma_f32_16x16x32_bf16 v[6:9], v[168:171], v[216:219], v[6:9]
	v_mfma_f32_16x16x32_bf16 v[2:5], v[176:179], v[216:219], v[2:5]
	v_mfma_f32_16x16x32_bf16 v[54:57], v[172:175], v[188:191], v[54:57]
	v_mfma_f32_16x16x32_bf16 v[50:53], v[180:183], v[188:191], v[50:53]
	v_mfma_f32_16x16x32_bf16 v[38:41], v[172:175], v[196:199], v[38:41]
	v_mfma_f32_16x16x32_bf16 v[34:37], v[180:183], v[196:199], v[34:37]
	v_mfma_f32_16x16x32_bf16 v[22:25], v[172:175], v[204:207], v[22:25]
	v_mfma_f32_16x16x32_bf16 v[18:21], v[180:183], v[204:207], v[18:21]
	v_mfma_f32_16x16x32_bf16 v[6:9], v[172:175], v[220:223], v[6:9]
	v_mfma_f32_16x16x32_bf16 v[2:5], v[180:183], v[220:223], v[2:5]
	s_setprio 0
	s_barrier
	s_add_i32 s85, s85, 2
	s_add_u32 s36, s36, 0x100
	s_addc_u32 s37, s37, 0
	s_cmp_gt_u32 s85, 61
	s_cbranch_scc0 .LBB0_2703
	s_add_u32 s36, s59, 0xffffff00
	s_addc_u32 s37, s82, -1
	s_andn2_b64 vcc, exec, s[42:43]
	s_cbranch_vccnz .LBB0_2706
	v_mov_b32_e32 v2, 0
	s_mov_b32 s12, s26
	s_mov_b32 s53, s28
	s_mov_b64 s[24:25], s[34:35]
	s_mov_b32 s68, s58
	v_mov_b32_e32 v3, v2
	v_mov_b32_e32 v4, v2
	v_mov_b32_e32 v5, v2
	v_mov_b32_e32 v6, v2
	v_mov_b32_e32 v7, v2
	v_mov_b32_e32 v8, v2
	v_mov_b32_e32 v9, v2
	v_mov_b32_e32 v18, v2
	v_mov_b32_e32 v19, v2
	v_mov_b32_e32 v20, v2
	v_mov_b32_e32 v21, v2
	v_mov_b32_e32 v22, v2
	v_mov_b32_e32 v23, v2
	v_mov_b32_e32 v24, v2
	v_mov_b32_e32 v25, v2
	v_mov_b32_e32 v34, v2
	v_mov_b32_e32 v35, v2
	v_mov_b32_e32 v36, v2
	v_mov_b32_e32 v37, v2
	v_mov_b32_e32 v38, v2
	v_mov_b32_e32 v39, v2
	v_mov_b32_e32 v40, v2
	v_mov_b32_e32 v41, v2
	v_mov_b32_e32 v50, v2
	v_mov_b32_e32 v51, v2
	v_mov_b32_e32 v52, v2
	v_mov_b32_e32 v53, v2
	v_mov_b32_e32 v54, v2
	v_mov_b32_e32 v55, v2
	v_mov_b32_e32 v56, v2
	v_mov_b32_e32 v57, v2
	v_mov_b32_e32 v10, v2
	v_mov_b32_e32 v11, v2
	v_mov_b32_e32 v12, v2
	v_mov_b32_e32 v13, v2
	v_mov_b32_e32 v14, v2
	v_mov_b32_e32 v15, v2
	v_mov_b32_e32 v16, v2
	v_mov_b32_e32 v17, v2
	v_mov_b32_e32 v26, v2
	v_mov_b32_e32 v27, v2
	v_mov_b32_e32 v28, v2
	v_mov_b32_e32 v29, v2
	v_mov_b32_e32 v30, v2
	v_mov_b32_e32 v31, v2
	v_mov_b32_e32 v32, v2
	v_mov_b32_e32 v33, v2
	v_mov_b32_e32 v42, v2
	v_mov_b32_e32 v43, v2
	v_mov_b32_e32 v44, v2
	v_mov_b32_e32 v45, v2
	v_mov_b32_e32 v46, v2
	v_mov_b32_e32 v47, v2
	v_mov_b32_e32 v48, v2
	v_mov_b32_e32 v49, v2
	v_mov_b32_e32 v58, v2
	v_mov_b32_e32 v59, v2
	v_mov_b32_e32 v60, v2
	v_mov_b32_e32 v61, v2
	v_mov_b32_e32 v62, v2
	v_mov_b32_e32 v63, v2
	v_mov_b32_e32 v64, v2
	v_mov_b32_e32 v65, v2
	v_mov_b32_e32 v66, v2
	v_mov_b32_e32 v67, v2
	v_mov_b32_e32 v68, v2
	v_mov_b32_e32 v69, v2
	v_mov_b32_e32 v70, v2
	v_mov_b32_e32 v71, v2
	v_mov_b32_e32 v72, v2
	v_mov_b32_e32 v73, v2
	v_mov_b32_e32 v82, v2
	v_mov_b32_e32 v83, v2
	v_mov_b32_e32 v84, v2
	v_mov_b32_e32 v85, v2
	v_mov_b32_e32 v86, v2
	v_mov_b32_e32 v87, v2
	v_mov_b32_e32 v88, v2
	v_mov_b32_e32 v89, v2
	v_mov_b32_e32 v98, v2
	v_mov_b32_e32 v99, v2
	v_mov_b32_e32 v100, v2
	v_mov_b32_e32 v101, v2
	v_mov_b32_e32 v102, v2
	v_mov_b32_e32 v103, v2
	v_mov_b32_e32 v104, v2
	v_mov_b32_e32 v105, v2
	v_mov_b32_e32 v114, v2
	v_mov_b32_e32 v115, v2
	v_mov_b32_e32 v116, v2
	v_mov_b32_e32 v117, v2
	v_mov_b32_e32 v122, v2
	v_mov_b32_e32 v123, v2
	v_mov_b32_e32 v124, v2
	v_mov_b32_e32 v125, v2
	v_mov_b32_e32 v74, v2
	v_mov_b32_e32 v75, v2
	v_mov_b32_e32 v76, v2
	v_mov_b32_e32 v77, v2
	v_mov_b32_e32 v78, v2
	v_mov_b32_e32 v79, v2
	v_mov_b32_e32 v80, v2
	v_mov_b32_e32 v81, v2
	v_mov_b32_e32 v90, v2
	v_mov_b32_e32 v91, v2
	v_mov_b32_e32 v92, v2
	v_mov_b32_e32 v93, v2
	v_mov_b32_e32 v94, v2
	v_mov_b32_e32 v95, v2
	v_mov_b32_e32 v96, v2
	v_mov_b32_e32 v97, v2
	v_mov_b32_e32 v106, v2
	v_mov_b32_e32 v107, v2
	v_mov_b32_e32 v108, v2
	v_mov_b32_e32 v109, v2
	v_mov_b32_e32 v110, v2
	v_mov_b32_e32 v111, v2
	v_mov_b32_e32 v112, v2
	v_mov_b32_e32 v113, v2
	v_mov_b32_e32 v130, v2
	v_mov_b32_e32 v131, v2
	v_mov_b32_e32 v132, v2
	v_mov_b32_e32 v133, v2
	v_mov_b32_e32 v134, v2
	v_mov_b32_e32 v135, v2
	v_mov_b32_e32 v136, v2
	v_mov_b32_e32 v137, v2
	s_movk_i32 s92, 0x2b20
	s_andn2_b64 vcc, exec, s[40:41]
	s_cbranch_vccnz .LBB0_2707
	s_branch .LBB0_2708

.LBB0_2796:
	s_add_u32 s44, s24, s36
	s_addc_u32 s45, s25, s37
	s_add_u32 s44, s44, 0x100
	s_addc_u32 s45, s45, 0
	s_add_u32 s50, s59, s36
	s_addc_u32 s64, s81, s37
	s_add_i32 s65, 0, 0x10000
	s_cmpk_eq_i32 s36, 0x1f00
	s_cselect_b32 s47, s29, s45
	s_cselect_b32 s46, s82, s44
	s_cselect_b32 s45, s27, s64
	s_cselect_b32 s44, s83, s50
	s_add_i32 s50, 0, 0x14000
	v_add_u32_e32 v160, s65, v146
	v_add_u32_e32 v164, s50, v146
	ds_read_b128 v[148:151], v160
	ds_read_b128 v[152:155], v160 offset:1024
	ds_read_b128 v[156:159], v160 offset:2048
	ds_read_b128 v[160:163], v160 offset:3072
	ds_read_b128 v[168:171], v164
	ds_read_b128 v[172:175], v164 offset:1024
	ds_read_b128 v[176:179], v164 offset:2048
	ds_read_b128 v[180:183], v164 offset:3072
	v_lshl_add_u64 v[164:165], v[144:145], 0, s[36:37]
	s_add_i32 m0, s4, 0xc000
	ds_read_b128 v[184:187], v147
	ds_read_b128 v[188:191], v147 offset:1024
	ds_read_b128 v[192:195], v147 offset:2048
	ds_read_b128 v[196:199], v147 offset:3072
	ds_read_b128 v[200:203], v147 offset:4096
	ds_read_b128 v[204:207], v147 offset:5120
	ds_read_b128 v[216:219], v147 offset:6144
	ds_read_b128 v[220:223], v147 offset:7168
	global_load_lds_dwordx4 v[164:165], off
	s_add_i32 m0, s4, 0xe000
	v_lshl_add_u64 v[164:165], v[142:143], 0, s[36:37]
	global_load_lds_dwordx4 v[164:165], off
	s_waitcnt vmcnt(8)
	s_waitcnt lgkmcnt(0)
	s_barrier
	s_setprio 1
	s_waitcnt lgkmcnt(0)
	v_mfma_f32_16x16x32_bf16 v[134:137], v[148:151], v[184:187], v[134:137]
	v_mfma_f32_16x16x32_bf16 v[130:133], v[156:159], v[184:187], v[130:133]
	v_mfma_f32_16x16x32_bf16 v[110:113], v[148:151], v[192:195], v[110:113]
	v_mfma_f32_16x16x32_bf16 v[106:109], v[156:159], v[192:195], v[106:109]
	v_mfma_f32_16x16x32_bf16 v[94:97], v[148:151], v[200:203], v[94:97]
	v_mfma_f32_16x16x32_bf16 v[90:93], v[156:159], v[200:203], v[90:93]
	v_mfma_f32_16x16x32_bf16 v[78:81], v[148:151], v[216:219], v[78:81]
	v_mfma_f32_16x16x32_bf16 v[74:77], v[156:159], v[216:219], v[74:77]
	v_mfma_f32_16x16x32_bf16 v[134:137], v[152:155], v[188:191], v[134:137]
	v_mfma_f32_16x16x32_bf16 v[130:133], v[160:163], v[188:191], v[130:133]
	v_mfma_f32_16x16x32_bf16 v[110:113], v[152:155], v[196:199], v[110:113]
	v_mfma_f32_16x16x32_bf16 v[106:109], v[160:163], v[196:199], v[106:109]
	v_mfma_f32_16x16x32_bf16 v[94:97], v[152:155], v[204:207], v[94:97]
	v_mfma_f32_16x16x32_bf16 v[90:93], v[160:163], v[204:207], v[90:93]
	v_mfma_f32_16x16x32_bf16 v[78:81], v[152:155], v[220:223], v[78:81]
	v_mfma_f32_16x16x32_bf16 v[74:77], v[160:163], v[220:223], v[74:77]
	s_setprio 0
	s_setprio 1
	v_mfma_f32_16x16x32_bf16 v[122:125], v[168:171], v[184:187], v[122:125]
	v_mfma_f32_16x16x32_bf16 v[114:117], v[176:179], v[184:187], v[114:117]
	v_mfma_f32_16x16x32_bf16 v[102:105], v[168:171], v[192:195], v[102:105]
	v_mfma_f32_16x16x32_bf16 v[98:101], v[176:179], v[192:195], v[98:101]
	v_mfma_f32_16x16x32_bf16 v[86:89], v[168:171], v[200:203], v[86:89]
	v_mfma_f32_16x16x32_bf16 v[82:85], v[176:179], v[200:203], v[82:85]
	v_mfma_f32_16x16x32_bf16 v[70:73], v[168:171], v[216:219], v[70:73]
	v_mfma_f32_16x16x32_bf16 v[66:69], v[176:179], v[216:219], v[66:69]
	v_mfma_f32_16x16x32_bf16 v[122:125], v[172:175], v[188:191], v[122:125]
	v_mfma_f32_16x16x32_bf16 v[114:117], v[180:183], v[188:191], v[114:117]
	v_mfma_f32_16x16x32_bf16 v[102:105], v[172:175], v[196:199], v[102:105]
	v_mfma_f32_16x16x32_bf16 v[98:101], v[180:183], v[196:199], v[98:101]
	v_mfma_f32_16x16x32_bf16 v[86:89], v[172:175], v[204:207], v[86:89]
	v_mfma_f32_16x16x32_bf16 v[82:85], v[180:183], v[204:207], v[82:85]
	v_mfma_f32_16x16x32_bf16 v[70:73], v[172:175], v[220:223], v[70:73]
	v_mfma_f32_16x16x32_bf16 v[66:69], v[180:183], v[220:223], v[66:69]
	s_setprio 0
	s_barrier
	s_add_i32 s64, s65, s71
	v_lshl_add_u64 v[164:165], s[44:45], 0, v[126:127]
	s_mov_b32 m0, s64
	ds_read_b128 v[184:187], v147 offset:16384
	ds_read_b128 v[188:191], v147 offset:17408
	ds_read_b128 v[192:195], v147 offset:18432
	ds_read_b128 v[196:199], v147 offset:19456
	ds_read_b128 v[200:203], v147 offset:20480
	ds_read_b128 v[204:207], v147 offset:21504
	ds_read_b128 v[216:219], v147 offset:22528
	ds_read_b128 v[220:223], v147 offset:23552
	global_load_lds_dwordx4 v[164:165], off
	s_add_i32 m0, s64, 0x2000
	s_add_u32 s92, s44, 0x100000
	v_lshl_add_u64 v[208:209], s[44:45], 0, v[118:119]
	s_addc_u32 s93, s45, 0
	s_add_i32 s50, s50, s71
	global_load_lds_dwordx4 v[208:209], off
	v_lshl_add_u64 v[224:225], s[92:93], 0, v[126:127]
	s_mov_b32 m0, s50
	v_lshl_add_u64 v[242:243], s[46:47], 0, v[120:121]
	global_load_lds_dwordx4 v[224:225], off
	s_add_i32 m0, s50, 0x2000
	v_lshl_add_u64 v[224:225], s[92:93], 0, v[118:119]
	global_load_lds_dwordx4 v[224:225], off
	s_mov_b32 m0, s4
	v_lshl_add_u64 v[224:225], s[46:47], 0, v[128:129]
	global_load_lds_dwordx4 v[224:225], off
	s_mov_b32 m0, s33
	s_nop 0
	global_load_lds_dwordx4 v[242:243], off
	s_waitcnt vmcnt(8)
	s_waitcnt lgkmcnt(0)
	s_barrier
	s_setprio 1
	s_waitcnt lgkmcnt(0)
	v_mfma_f32_16x16x32_bf16 v[62:65], v[148:151], v[184:187], v[62:65]
	v_mfma_f32_16x16x32_bf16 v[58:61], v[156:159], v[184:187], v[58:61]
	v_mfma_f32_16x16x32_bf16 v[46:49], v[148:151], v[192:195], v[46:49]
	v_mfma_f32_16x16x32_bf16 v[42:45], v[156:159], v[192:195], v[42:45]
	v_mfma_f32_16x16x32_bf16 v[30:33], v[148:151], v[200:203], v[30:33]
	v_mfma_f32_16x16x32_bf16 v[26:29], v[156:159], v[200:203], v[26:29]
	v_mfma_f32_16x16x32_bf16 v[14:17], v[148:151], v[216:219], v[14:17]
	v_mfma_f32_16x16x32_bf16 v[10:13], v[156:159], v[216:219], v[10:13]
	v_mfma_f32_16x16x32_bf16 v[62:65], v[152:155], v[188:191], v[62:65]
	v_mfma_f32_16x16x32_bf16 v[58:61], v[160:163], v[188:191], v[58:61]
	v_mfma_f32_16x16x32_bf16 v[46:49], v[152:155], v[196:199], v[46:49]
	v_mfma_f32_16x16x32_bf16 v[42:45], v[160:163], v[196:199], v[42:45]
	v_mfma_f32_16x16x32_bf16 v[30:33], v[152:155], v[204:207], v[30:33]
	v_mfma_f32_16x16x32_bf16 v[26:29], v[160:163], v[204:207], v[26:29]
	v_mfma_f32_16x16x32_bf16 v[14:17], v[152:155], v[220:223], v[14:17]
	v_mfma_f32_16x16x32_bf16 v[10:13], v[160:163], v[220:223], v[10:13]
	s_setprio 0
	s_setprio 1
	v_mfma_f32_16x16x32_bf16 v[54:57], v[168:171], v[184:187], v[54:57]
	v_mfma_f32_16x16x32_bf16 v[50:53], v[176:179], v[184:187], v[50:53]
	v_mfma_f32_16x16x32_bf16 v[38:41], v[168:171], v[192:195], v[38:41]
	v_mfma_f32_16x16x32_bf16 v[34:37], v[176:179], v[192:195], v[34:37]
	v_mfma_f32_16x16x32_bf16 v[22:25], v[168:171], v[200:203], v[22:25]
	v_mfma_f32_16x16x32_bf16 v[18:21], v[176:179], v[200:203], v[18:21]
	v_mfma_f32_16x16x32_bf16 v[6:9], v[168:171], v[216:219], v[6:9]
	v_mfma_f32_16x16x32_bf16 v[2:5], v[176:179], v[216:219], v[2:5]
	v_mfma_f32_16x16x32_bf16 v[54:57], v[172:175], v[188:191], v[54:57]
	v_mfma_f32_16x16x32_bf16 v[50:53], v[180:183], v[188:191], v[50:53]
	v_mfma_f32_16x16x32_bf16 v[38:41], v[172:175], v[196:199], v[38:41]
	v_mfma_f32_16x16x32_bf16 v[34:37], v[180:183], v[196:199], v[34:37]
	v_mfma_f32_16x16x32_bf16 v[22:25], v[172:175], v[204:207], v[22:25]
	v_mfma_f32_16x16x32_bf16 v[18:21], v[180:183], v[204:207], v[18:21]
	v_mfma_f32_16x16x32_bf16 v[6:9], v[172:175], v[220:223], v[6:9]
	v_mfma_f32_16x16x32_bf16 v[2:5], v[180:183], v[220:223], v[2:5]
	s_setprio 0
	s_barrier
	s_add_i32 s50, 0, 0x18000
	s_add_i32 s64, 0, 0x1c000
	v_add_u32_e32 v160, s50, v146
	v_add_u32_e32 v167, s64, v146
	ds_read_b128 v[148:151], v160
	ds_read_b128 v[152:155], v160 offset:1024
	ds_read_b128 v[156:159], v160 offset:2048
	ds_read_b128 v[160:163], v160 offset:3072
	ds_read_b128 v[168:171], v167
	ds_read_b128 v[172:175], v167 offset:1024
	ds_read_b128 v[176:179], v167 offset:2048
	ds_read_b128 v[180:183], v167 offset:3072
	s_add_u32 s46, s46, 0x100000
	s_addc_u32 s47, s47, 0
	s_mov_b32 m0, s76
	v_lshl_add_u64 v[244:245], s[46:47], 0, v[128:129]
	ds_read_b128 v[184:187], v147 offset:32768
	ds_read_b128 v[188:191], v147 offset:33792
	ds_read_b128 v[192:195], v147 offset:34816
	ds_read_b128 v[196:199], v147 offset:35840
	ds_read_b128 v[200:203], v147 offset:36864
	ds_read_b128 v[204:207], v147 offset:37888
	ds_read_b128 v[216:219], v147 offset:38912
	ds_read_b128 v[220:223], v147 offset:39936
	global_load_lds_dwordx4 v[244:245], off
	s_mov_b32 m0, s77
	v_lshl_add_u64 v[244:245], s[46:47], 0, v[120:121]
	global_load_lds_dwordx4 v[244:245], off
	s_waitcnt vmcnt(8)
	s_waitcnt lgkmcnt(0)
	s_barrier
	s_setprio 1
	s_waitcnt lgkmcnt(0)
	v_mfma_f32_16x16x32_bf16 v[134:137], v[148:151], v[184:187], v[134:137]
	v_mfma_f32_16x16x32_bf16 v[130:133], v[156:159], v[184:187], v[130:133]
	v_mfma_f32_16x16x32_bf16 v[110:113], v[148:151], v[192:195], v[110:113]
	v_mfma_f32_16x16x32_bf16 v[106:109], v[156:159], v[192:195], v[106:109]
	v_mfma_f32_16x16x32_bf16 v[94:97], v[148:151], v[200:203], v[94:97]
	v_mfma_f32_16x16x32_bf16 v[90:93], v[156:159], v[200:203], v[90:93]
	v_mfma_f32_16x16x32_bf16 v[78:81], v[148:151], v[216:219], v[78:81]
	v_mfma_f32_16x16x32_bf16 v[74:77], v[156:159], v[216:219], v[74:77]
	v_mfma_f32_16x16x32_bf16 v[134:137], v[152:155], v[188:191], v[134:137]
	v_mfma_f32_16x16x32_bf16 v[130:133], v[160:163], v[188:191], v[130:133]
	v_mfma_f32_16x16x32_bf16 v[110:113], v[152:155], v[196:199], v[110:113]
	v_mfma_f32_16x16x32_bf16 v[106:109], v[160:163], v[196:199], v[106:109]
	v_mfma_f32_16x16x32_bf16 v[94:97], v[152:155], v[204:207], v[94:97]
	v_mfma_f32_16x16x32_bf16 v[90:93], v[160:163], v[204:207], v[90:93]
	v_mfma_f32_16x16x32_bf16 v[78:81], v[152:155], v[220:223], v[78:81]
	v_mfma_f32_16x16x32_bf16 v[74:77], v[160:163], v[220:223], v[74:77]
	s_setprio 0
	s_setprio 1
	v_mfma_f32_16x16x32_bf16 v[122:125], v[168:171], v[184:187], v[122:125]
	v_mfma_f32_16x16x32_bf16 v[114:117], v[176:179], v[184:187], v[114:117]
	v_mfma_f32_16x16x32_bf16 v[102:105], v[168:171], v[192:195], v[102:105]
	v_mfma_f32_16x16x32_bf16 v[98:101], v[176:179], v[192:195], v[98:101]
	v_mfma_f32_16x16x32_bf16 v[86:89], v[168:171], v[200:203], v[86:89]
	v_mfma_f32_16x16x32_bf16 v[82:85], v[176:179], v[200:203], v[82:85]
	v_mfma_f32_16x16x32_bf16 v[70:73], v[168:171], v[216:219], v[70:73]
	v_mfma_f32_16x16x32_bf16 v[66:69], v[176:179], v[216:219], v[66:69]
	v_mfma_f32_16x16x32_bf16 v[122:125], v[172:175], v[188:191], v[122:125]
	v_mfma_f32_16x16x32_bf16 v[114:117], v[180:183], v[188:191], v[114:117]
	v_mfma_f32_16x16x32_bf16 v[102:105], v[172:175], v[196:199], v[102:105]
	v_mfma_f32_16x16x32_bf16 v[98:101], v[180:183], v[196:199], v[98:101]
	v_mfma_f32_16x16x32_bf16 v[86:89], v[172:175], v[204:207], v[86:89]
	v_mfma_f32_16x16x32_bf16 v[82:85], v[180:183], v[204:207], v[82:85]
	v_mfma_f32_16x16x32_bf16 v[70:73], v[172:175], v[220:223], v[70:73]
	v_mfma_f32_16x16x32_bf16 v[66:69], v[180:183], v[220:223], v[66:69]
	s_setprio 0
	s_barrier
	s_add_i32 s46, s50, s71
	v_lshl_add_u64 v[164:165], v[164:165], 0, s[56:57]
	s_mov_b32 m0, s46
	ds_read_b128 v[184:187], v147 offset:49152
	ds_read_b128 v[188:191], v147 offset:50176
	ds_read_b128 v[192:195], v147 offset:51200
	ds_read_b128 v[196:199], v147 offset:52224
	ds_read_b128 v[200:203], v147 offset:53248
	ds_read_b128 v[204:207], v147 offset:54272
	ds_read_b128 v[216:219], v147 offset:55296
	ds_read_b128 v[220:223], v147 offset:56320
	global_load_lds_dwordx4 v[164:165], off
	s_add_i32 m0, s46, 0x2000
	s_add_u32 s44, s44, 0x100080
	v_lshl_add_u64 v[164:165], v[208:209], 0, s[56:57]
	s_addc_u32 s45, s45, 0
	s_add_i32 s46, s64, s71
	global_load_lds_dwordx4 v[164:165], off
	s_mov_b32 m0, s46
	v_lshl_add_u64 v[164:165], s[44:45], 0, v[126:127]
	global_load_lds_dwordx4 v[164:165], off
	s_add_i32 m0, s46, 0x2000
	v_lshl_add_u64 v[164:165], s[44:45], 0, v[118:119]
	global_load_lds_dwordx4 v[164:165], off
	s_mov_b32 m0, s78
	v_lshl_add_u64 v[164:165], v[224:225], 0, s[56:57]
	global_load_lds_dwordx4 v[164:165], off
	s_mov_b32 m0, s79
	v_lshl_add_u64 v[164:165], v[242:243], 0, s[56:57]
	global_load_lds_dwordx4 v[164:165], off
	s_waitcnt vmcnt(8)
	s_waitcnt lgkmcnt(0)
	s_barrier
	s_setprio 1
	s_waitcnt lgkmcnt(0)
	v_mfma_f32_16x16x32_bf16 v[62:65], v[148:151], v[184:187], v[62:65]
	v_mfma_f32_16x16x32_bf16 v[58:61], v[156:159], v[184:187], v[58:61]
	v_mfma_f32_16x16x32_bf16 v[46:49], v[148:151], v[192:195], v[46:49]
	v_mfma_f32_16x16x32_bf16 v[42:45], v[156:159], v[192:195], v[42:45]
	v_mfma_f32_16x16x32_bf16 v[30:33], v[148:151], v[200:203], v[30:33]
	v_mfma_f32_16x16x32_bf16 v[26:29], v[156:159], v[200:203], v[26:29]
	v_mfma_f32_16x16x32_bf16 v[14:17], v[148:151], v[216:219], v[14:17]
	v_mfma_f32_16x16x32_bf16 v[10:13], v[156:159], v[216:219], v[10:13]
	v_mfma_f32_16x16x32_bf16 v[62:65], v[152:155], v[188:191], v[62:65]
	v_mfma_f32_16x16x32_bf16 v[58:61], v[160:163], v[188:191], v[58:61]
	v_mfma_f32_16x16x32_bf16 v[46:49], v[152:155], v[196:199], v[46:49]
	v_mfma_f32_16x16x32_bf16 v[42:45], v[160:163], v[196:199], v[42:45]
	v_mfma_f32_16x16x32_bf16 v[30:33], v[152:155], v[204:207], v[30:33]
	v_mfma_f32_16x16x32_bf16 v[26:29], v[160:163], v[204:207], v[26:29]
	v_mfma_f32_16x16x32_bf16 v[14:17], v[152:155], v[220:223], v[14:17]
	v_mfma_f32_16x16x32_bf16 v[10:13], v[160:163], v[220:223], v[10:13]
	s_setprio 0
	s_setprio 1
	v_mfma_f32_16x16x32_bf16 v[54:57], v[168:171], v[184:187], v[54:57]
	v_mfma_f32_16x16x32_bf16 v[50:53], v[176:179], v[184:187], v[50:53]
	v_mfma_f32_16x16x32_bf16 v[38:41], v[168:171], v[192:195], v[38:41]
	v_mfma_f32_16x16x32_bf16 v[34:37], v[176:179], v[192:195], v[34:37]
	v_mfma_f32_16x16x32_bf16 v[22:25], v[168:171], v[200:203], v[22:25]
	v_mfma_f32_16x16x32_bf16 v[18:21], v[176:179], v[200:203], v[18:21]
	v_mfma_f32_16x16x32_bf16 v[6:9], v[168:171], v[216:219], v[6:9]
	v_mfma_f32_16x16x32_bf16 v[2:5], v[176:179], v[216:219], v[2:5]
	v_mfma_f32_16x16x32_bf16 v[54:57], v[172:175], v[188:191], v[54:57]
	v_mfma_f32_16x16x32_bf16 v[50:53], v[180:183], v[188:191], v[50:53]
	v_mfma_f32_16x16x32_bf16 v[38:41], v[172:175], v[196:199], v[38:41]
	v_mfma_f32_16x16x32_bf16 v[34:37], v[180:183], v[196:199], v[34:37]
	v_mfma_f32_16x16x32_bf16 v[22:25], v[172:175], v[204:207], v[22:25]
	v_mfma_f32_16x16x32_bf16 v[18:21], v[180:183], v[204:207], v[18:21]
	v_mfma_f32_16x16x32_bf16 v[6:9], v[172:175], v[220:223], v[6:9]
	v_mfma_f32_16x16x32_bf16 v[2:5], v[180:183], v[220:223], v[2:5]
	s_setprio 0
	s_barrier
	s_add_i32 s84, s84, 2
	s_add_u32 s36, s36, 0x100
	s_addc_u32 s37, s37, 0
	s_cmp_gt_u32 s84, 61
	s_cbranch_scc0 .LBB0_2796
	s_add_u32 s36, s59, 0xffffff00
	s_addc_u32 s37, s81, -1
	s_andn2_b64 vcc, exec, s[42:43]
	s_cbranch_vccnz .LBB0_2799
	v_mov_b32_e32 v2, 0
	s_mov_b32 s12, s26
	s_mov_b32 s80, s28
	s_mov_b64 s[24:25], s[34:35]
	s_mov_b32 s68, s58
	v_mov_b32_e32 v3, v2
	v_mov_b32_e32 v4, v2
	v_mov_b32_e32 v5, v2
	v_mov_b32_e32 v6, v2
	v_mov_b32_e32 v7, v2
	v_mov_b32_e32 v8, v2
	v_mov_b32_e32 v9, v2
	v_mov_b32_e32 v18, v2
	v_mov_b32_e32 v19, v2
	v_mov_b32_e32 v20, v2
	v_mov_b32_e32 v21, v2
	v_mov_b32_e32 v22, v2
	v_mov_b32_e32 v23, v2
	v_mov_b32_e32 v24, v2
	v_mov_b32_e32 v25, v2
	v_mov_b32_e32 v34, v2
	v_mov_b32_e32 v35, v2
	v_mov_b32_e32 v36, v2
	v_mov_b32_e32 v37, v2
	v_mov_b32_e32 v38, v2
	v_mov_b32_e32 v39, v2
	v_mov_b32_e32 v40, v2
	v_mov_b32_e32 v41, v2
	v_mov_b32_e32 v50, v2
	v_mov_b32_e32 v51, v2
	v_mov_b32_e32 v52, v2
	v_mov_b32_e32 v53, v2
	v_mov_b32_e32 v54, v2
	v_mov_b32_e32 v55, v2
	v_mov_b32_e32 v56, v2
	v_mov_b32_e32 v57, v2
	v_mov_b32_e32 v10, v2
	v_mov_b32_e32 v11, v2
	v_mov_b32_e32 v12, v2
	v_mov_b32_e32 v13, v2
	v_mov_b32_e32 v14, v2
	v_mov_b32_e32 v15, v2
	v_mov_b32_e32 v16, v2
	v_mov_b32_e32 v17, v2
	v_mov_b32_e32 v26, v2
	v_mov_b32_e32 v27, v2
	v_mov_b32_e32 v28, v2
	v_mov_b32_e32 v29, v2
	v_mov_b32_e32 v30, v2
	v_mov_b32_e32 v31, v2
	v_mov_b32_e32 v32, v2
	v_mov_b32_e32 v33, v2
	v_mov_b32_e32 v42, v2
	v_mov_b32_e32 v43, v2
	v_mov_b32_e32 v44, v2
	v_mov_b32_e32 v45, v2
	v_mov_b32_e32 v46, v2
	v_mov_b32_e32 v47, v2
	v_mov_b32_e32 v48, v2
	v_mov_b32_e32 v49, v2
	v_mov_b32_e32 v58, v2
	v_mov_b32_e32 v59, v2
	v_mov_b32_e32 v60, v2
	v_mov_b32_e32 v61, v2
	v_mov_b32_e32 v62, v2
	v_mov_b32_e32 v63, v2
	v_mov_b32_e32 v64, v2
	v_mov_b32_e32 v65, v2
	v_mov_b32_e32 v66, v2
	v_mov_b32_e32 v67, v2
	v_mov_b32_e32 v68, v2
	v_mov_b32_e32 v69, v2
	v_mov_b32_e32 v70, v2
	v_mov_b32_e32 v71, v2
	v_mov_b32_e32 v72, v2
	v_mov_b32_e32 v73, v2
	v_mov_b32_e32 v82, v2
	v_mov_b32_e32 v83, v2
	v_mov_b32_e32 v84, v2
	v_mov_b32_e32 v85, v2
	v_mov_b32_e32 v86, v2
	v_mov_b32_e32 v87, v2
	v_mov_b32_e32 v88, v2
	v_mov_b32_e32 v89, v2
	v_mov_b32_e32 v98, v2
	v_mov_b32_e32 v99, v2
	v_mov_b32_e32 v100, v2
	v_mov_b32_e32 v101, v2
	v_mov_b32_e32 v102, v2
	v_mov_b32_e32 v103, v2
	v_mov_b32_e32 v104, v2
	v_mov_b32_e32 v105, v2
	v_mov_b32_e32 v114, v2
	v_mov_b32_e32 v115, v2
	v_mov_b32_e32 v116, v2
	v_mov_b32_e32 v117, v2
	v_mov_b32_e32 v122, v2
	v_mov_b32_e32 v123, v2
	v_mov_b32_e32 v124, v2
	v_mov_b32_e32 v125, v2
	v_mov_b32_e32 v74, v2
	v_mov_b32_e32 v75, v2
	v_mov_b32_e32 v76, v2
	v_mov_b32_e32 v77, v2
	v_mov_b32_e32 v78, v2
	v_mov_b32_e32 v79, v2
	v_mov_b32_e32 v80, v2
	v_mov_b32_e32 v81, v2
	v_mov_b32_e32 v90, v2
	v_mov_b32_e32 v91, v2
	v_mov_b32_e32 v92, v2
	v_mov_b32_e32 v93, v2
	v_mov_b32_e32 v94, v2
	v_mov_b32_e32 v95, v2
	v_mov_b32_e32 v96, v2
	v_mov_b32_e32 v97, v2
	v_mov_b32_e32 v106, v2
	v_mov_b32_e32 v107, v2
	v_mov_b32_e32 v108, v2
	v_mov_b32_e32 v109, v2
	v_mov_b32_e32 v110, v2
	v_mov_b32_e32 v111, v2
	v_mov_b32_e32 v112, v2
	v_mov_b32_e32 v113, v2
	v_mov_b32_e32 v130, v2
	v_mov_b32_e32 v131, v2
	v_mov_b32_e32 v132, v2
	v_mov_b32_e32 v133, v2
	v_mov_b32_e32 v134, v2
	v_mov_b32_e32 v135, v2
	v_mov_b32_e32 v136, v2
	v_mov_b32_e32 v137, v2
	s_movk_i32 s92, 0x2b20
	s_andn2_b64 vcc, exec, s[40:41]
	s_cbranch_vccnz .LBB0_2800
	s_branch .LBB0_2801

.LBB0_2891:
	s_add_u32 s44, s24, s36
	s_addc_u32 s45, s25, s37
	s_add_u32 s44, s44, 0x100
	s_addc_u32 s45, s45, 0
	s_add_u32 s50, s59, s36
	s_addc_u32 s64, s81, s37
	s_add_i32 s65, 0, 0x10000
	s_cmpk_eq_i32 s36, 0x1f00
	s_cselect_b32 s47, s29, s45
	s_cselect_b32 s46, s82, s44
	s_cselect_b32 s45, s27, s64
	s_cselect_b32 s44, s83, s50
	s_add_i32 s50, 0, 0x14000
	v_add_u32_e32 v160, s65, v146
	v_add_u32_e32 v164, s50, v146
	ds_read_b128 v[148:151], v160
	ds_read_b128 v[152:155], v160 offset:1024
	ds_read_b128 v[156:159], v160 offset:2048
	ds_read_b128 v[160:163], v160 offset:3072
	ds_read_b128 v[168:171], v164
	ds_read_b128 v[172:175], v164 offset:1024
	ds_read_b128 v[176:179], v164 offset:2048
	ds_read_b128 v[180:183], v164 offset:3072
	v_lshl_add_u64 v[164:165], v[144:145], 0, s[36:37]
	s_add_i32 m0, s4, 0xc000
	ds_read_b128 v[184:187], v147
	ds_read_b128 v[188:191], v147 offset:1024
	ds_read_b128 v[192:195], v147 offset:2048
	ds_read_b128 v[196:199], v147 offset:3072
	ds_read_b128 v[200:203], v147 offset:4096
	ds_read_b128 v[204:207], v147 offset:5120
	ds_read_b128 v[216:219], v147 offset:6144
	ds_read_b128 v[220:223], v147 offset:7168
	global_load_lds_dwordx4 v[164:165], off
	s_add_i32 m0, s4, 0xe000
	v_lshl_add_u64 v[164:165], v[142:143], 0, s[36:37]
	global_load_lds_dwordx4 v[164:165], off
	s_waitcnt vmcnt(8)
	s_waitcnt lgkmcnt(0)
	s_barrier
	s_setprio 1
	s_waitcnt lgkmcnt(0)
	v_mfma_f32_16x16x32_bf16 v[134:137], v[148:151], v[184:187], v[134:137]
	v_mfma_f32_16x16x32_bf16 v[130:133], v[156:159], v[184:187], v[130:133]
	v_mfma_f32_16x16x32_bf16 v[110:113], v[148:151], v[192:195], v[110:113]
	v_mfma_f32_16x16x32_bf16 v[106:109], v[156:159], v[192:195], v[106:109]
	v_mfma_f32_16x16x32_bf16 v[94:97], v[148:151], v[200:203], v[94:97]
	v_mfma_f32_16x16x32_bf16 v[90:93], v[156:159], v[200:203], v[90:93]
	v_mfma_f32_16x16x32_bf16 v[78:81], v[148:151], v[216:219], v[78:81]
	v_mfma_f32_16x16x32_bf16 v[74:77], v[156:159], v[216:219], v[74:77]
	v_mfma_f32_16x16x32_bf16 v[134:137], v[152:155], v[188:191], v[134:137]
	v_mfma_f32_16x16x32_bf16 v[130:133], v[160:163], v[188:191], v[130:133]
	v_mfma_f32_16x16x32_bf16 v[110:113], v[152:155], v[196:199], v[110:113]
	v_mfma_f32_16x16x32_bf16 v[106:109], v[160:163], v[196:199], v[106:109]
	v_mfma_f32_16x16x32_bf16 v[94:97], v[152:155], v[204:207], v[94:97]
	v_mfma_f32_16x16x32_bf16 v[90:93], v[160:163], v[204:207], v[90:93]
	v_mfma_f32_16x16x32_bf16 v[78:81], v[152:155], v[220:223], v[78:81]
	v_mfma_f32_16x16x32_bf16 v[74:77], v[160:163], v[220:223], v[74:77]
	s_setprio 0
	s_setprio 1
	v_mfma_f32_16x16x32_bf16 v[118:121], v[168:171], v[184:187], v[118:121]
	v_mfma_f32_16x16x32_bf16 v[114:117], v[176:179], v[184:187], v[114:117]
	v_mfma_f32_16x16x32_bf16 v[102:105], v[168:171], v[192:195], v[102:105]
	v_mfma_f32_16x16x32_bf16 v[98:101], v[176:179], v[192:195], v[98:101]
	v_mfma_f32_16x16x32_bf16 v[86:89], v[168:171], v[200:203], v[86:89]
	v_mfma_f32_16x16x32_bf16 v[82:85], v[176:179], v[200:203], v[82:85]
	v_mfma_f32_16x16x32_bf16 v[70:73], v[168:171], v[216:219], v[70:73]
	v_mfma_f32_16x16x32_bf16 v[66:69], v[176:179], v[216:219], v[66:69]
	v_mfma_f32_16x16x32_bf16 v[118:121], v[172:175], v[188:191], v[118:121]
	v_mfma_f32_16x16x32_bf16 v[114:117], v[180:183], v[188:191], v[114:117]
	v_mfma_f32_16x16x32_bf16 v[102:105], v[172:175], v[196:199], v[102:105]
	v_mfma_f32_16x16x32_bf16 v[98:101], v[180:183], v[196:199], v[98:101]
	v_mfma_f32_16x16x32_bf16 v[86:89], v[172:175], v[204:207], v[86:89]
	v_mfma_f32_16x16x32_bf16 v[82:85], v[180:183], v[204:207], v[82:85]
	v_mfma_f32_16x16x32_bf16 v[70:73], v[172:175], v[220:223], v[70:73]
	v_mfma_f32_16x16x32_bf16 v[66:69], v[180:183], v[220:223], v[66:69]
	s_setprio 0
	s_barrier
	s_add_i32 s64, s65, s76
	v_lshl_add_u64 v[164:165], s[44:45], 0, v[126:127]
	s_mov_b32 m0, s64
	ds_read_b128 v[184:187], v147 offset:16384
	ds_read_b128 v[188:191], v147 offset:17408
	ds_read_b128 v[192:195], v147 offset:18432
	ds_read_b128 v[196:199], v147 offset:19456
	ds_read_b128 v[200:203], v147 offset:20480
	ds_read_b128 v[204:207], v147 offset:21504
	ds_read_b128 v[216:219], v147 offset:22528
	ds_read_b128 v[220:223], v147 offset:23552
	global_load_lds_dwordx4 v[164:165], off
	s_add_i32 m0, s64, 0x2000
	s_add_u32 s92, s44, 0x100000
	v_lshl_add_u64 v[208:209], s[44:45], 0, v[122:123]
	s_addc_u32 s93, s45, 0
	s_add_i32 s50, s50, s76
	global_load_lds_dwordx4 v[208:209], off
	v_lshl_add_u64 v[240:241], s[92:93], 0, v[126:127]
	s_mov_b32 m0, s50
	v_lshl_add_u64 v[242:243], s[46:47], 0, v[124:125]
	global_load_lds_dwordx4 v[240:241], off
	s_add_i32 m0, s50, 0x2000
	v_lshl_add_u64 v[240:241], s[92:93], 0, v[122:123]
	global_load_lds_dwordx4 v[240:241], off
	s_mov_b32 m0, s4
	v_lshl_add_u64 v[240:241], s[46:47], 0, v[128:129]
	global_load_lds_dwordx4 v[240:241], off
	s_mov_b32 m0, s33
	s_nop 0
	global_load_lds_dwordx4 v[242:243], off
	s_waitcnt vmcnt(8)
	s_waitcnt lgkmcnt(0)
	s_barrier
	s_setprio 1
	s_waitcnt lgkmcnt(0)
	v_mfma_f32_16x16x32_bf16 v[62:65], v[148:151], v[184:187], v[62:65]
	v_mfma_f32_16x16x32_bf16 v[58:61], v[156:159], v[184:187], v[58:61]
	v_mfma_f32_16x16x32_bf16 v[46:49], v[148:151], v[192:195], v[46:49]
	v_mfma_f32_16x16x32_bf16 v[42:45], v[156:159], v[192:195], v[42:45]
	v_mfma_f32_16x16x32_bf16 v[30:33], v[148:151], v[200:203], v[30:33]
	v_mfma_f32_16x16x32_bf16 v[26:29], v[156:159], v[200:203], v[26:29]
	v_mfma_f32_16x16x32_bf16 v[14:17], v[148:151], v[216:219], v[14:17]
	v_mfma_f32_16x16x32_bf16 v[10:13], v[156:159], v[216:219], v[10:13]
	v_mfma_f32_16x16x32_bf16 v[62:65], v[152:155], v[188:191], v[62:65]
	v_mfma_f32_16x16x32_bf16 v[58:61], v[160:163], v[188:191], v[58:61]
	v_mfma_f32_16x16x32_bf16 v[46:49], v[152:155], v[196:199], v[46:49]
	v_mfma_f32_16x16x32_bf16 v[42:45], v[160:163], v[196:199], v[42:45]
	v_mfma_f32_16x16x32_bf16 v[30:33], v[152:155], v[204:207], v[30:33]
	v_mfma_f32_16x16x32_bf16 v[26:29], v[160:163], v[204:207], v[26:29]
	v_mfma_f32_16x16x32_bf16 v[14:17], v[152:155], v[220:223], v[14:17]
	v_mfma_f32_16x16x32_bf16 v[10:13], v[160:163], v[220:223], v[10:13]
	s_setprio 0
	s_setprio 1
	v_mfma_f32_16x16x32_bf16 v[54:57], v[168:171], v[184:187], v[54:57]
	v_mfma_f32_16x16x32_bf16 v[50:53], v[176:179], v[184:187], v[50:53]
	v_mfma_f32_16x16x32_bf16 v[38:41], v[168:171], v[192:195], v[38:41]
	v_mfma_f32_16x16x32_bf16 v[34:37], v[176:179], v[192:195], v[34:37]
	v_mfma_f32_16x16x32_bf16 v[22:25], v[168:171], v[200:203], v[22:25]
	v_mfma_f32_16x16x32_bf16 v[18:21], v[176:179], v[200:203], v[18:21]
	v_mfma_f32_16x16x32_bf16 v[6:9], v[168:171], v[216:219], v[6:9]
	v_mfma_f32_16x16x32_bf16 v[2:5], v[176:179], v[216:219], v[2:5]
	v_mfma_f32_16x16x32_bf16 v[54:57], v[172:175], v[188:191], v[54:57]
	v_mfma_f32_16x16x32_bf16 v[50:53], v[180:183], v[188:191], v[50:53]
	v_mfma_f32_16x16x32_bf16 v[38:41], v[172:175], v[196:199], v[38:41]
	v_mfma_f32_16x16x32_bf16 v[34:37], v[180:183], v[196:199], v[34:37]
	v_mfma_f32_16x16x32_bf16 v[22:25], v[172:175], v[204:207], v[22:25]
	v_mfma_f32_16x16x32_bf16 v[18:21], v[180:183], v[204:207], v[18:21]
	v_mfma_f32_16x16x32_bf16 v[6:9], v[172:175], v[220:223], v[6:9]
	v_mfma_f32_16x16x32_bf16 v[2:5], v[180:183], v[220:223], v[2:5]
	s_setprio 0
	s_barrier
	s_add_i32 s50, 0, 0x18000
	s_add_i32 s64, 0, 0x1c000
	v_add_u32_e32 v160, s50, v146
	v_add_u32_e32 v167, s64, v146
	ds_read_b128 v[148:151], v160
	ds_read_b128 v[152:155], v160 offset:1024
	ds_read_b128 v[156:159], v160 offset:2048
	ds_read_b128 v[160:163], v160 offset:3072
	ds_read_b128 v[168:171], v167
	ds_read_b128 v[172:175], v167 offset:1024
	ds_read_b128 v[176:179], v167 offset:2048
	ds_read_b128 v[180:183], v167 offset:3072
	s_add_u32 s46, s46, 0x100000
	s_addc_u32 s47, s47, 0
	s_mov_b32 m0, s77
	v_lshl_add_u64 v[244:245], s[46:47], 0, v[128:129]
	ds_read_b128 v[184:187], v147 offset:32768
	ds_read_b128 v[188:191], v147 offset:33792
	ds_read_b128 v[192:195], v147 offset:34816
	ds_read_b128 v[196:199], v147 offset:35840
	ds_read_b128 v[200:203], v147 offset:36864
	ds_read_b128 v[204:207], v147 offset:37888
	ds_read_b128 v[216:219], v147 offset:38912
	ds_read_b128 v[220:223], v147 offset:39936
	global_load_lds_dwordx4 v[244:245], off
	s_mov_b32 m0, s78
	v_lshl_add_u64 v[244:245], s[46:47], 0, v[124:125]
	global_load_lds_dwordx4 v[244:245], off
	s_waitcnt vmcnt(8)
	s_waitcnt lgkmcnt(0)
	s_barrier
	s_setprio 1
	s_waitcnt lgkmcnt(0)
	v_mfma_f32_16x16x32_bf16 v[134:137], v[148:151], v[184:187], v[134:137]
	v_mfma_f32_16x16x32_bf16 v[130:133], v[156:159], v[184:187], v[130:133]
	v_mfma_f32_16x16x32_bf16 v[110:113], v[148:151], v[192:195], v[110:113]
	v_mfma_f32_16x16x32_bf16 v[106:109], v[156:159], v[192:195], v[106:109]
	v_mfma_f32_16x16x32_bf16 v[94:97], v[148:151], v[200:203], v[94:97]
	v_mfma_f32_16x16x32_bf16 v[90:93], v[156:159], v[200:203], v[90:93]
	v_mfma_f32_16x16x32_bf16 v[78:81], v[148:151], v[216:219], v[78:81]
	v_mfma_f32_16x16x32_bf16 v[74:77], v[156:159], v[216:219], v[74:77]
	v_mfma_f32_16x16x32_bf16 v[134:137], v[152:155], v[188:191], v[134:137]
	v_mfma_f32_16x16x32_bf16 v[130:133], v[160:163], v[188:191], v[130:133]
	v_mfma_f32_16x16x32_bf16 v[110:113], v[152:155], v[196:199], v[110:113]
	v_mfma_f32_16x16x32_bf16 v[106:109], v[160:163], v[196:199], v[106:109]
	v_mfma_f32_16x16x32_bf16 v[94:97], v[152:155], v[204:207], v[94:97]
	v_mfma_f32_16x16x32_bf16 v[90:93], v[160:163], v[204:207], v[90:93]
	v_mfma_f32_16x16x32_bf16 v[78:81], v[152:155], v[220:223], v[78:81]
	v_mfma_f32_16x16x32_bf16 v[74:77], v[160:163], v[220:223], v[74:77]
	s_setprio 0
	s_setprio 1
	v_mfma_f32_16x16x32_bf16 v[118:121], v[168:171], v[184:187], v[118:121]
	v_mfma_f32_16x16x32_bf16 v[114:117], v[176:179], v[184:187], v[114:117]
	v_mfma_f32_16x16x32_bf16 v[102:105], v[168:171], v[192:195], v[102:105]
	v_mfma_f32_16x16x32_bf16 v[98:101], v[176:179], v[192:195], v[98:101]
	v_mfma_f32_16x16x32_bf16 v[86:89], v[168:171], v[200:203], v[86:89]
	v_mfma_f32_16x16x32_bf16 v[82:85], v[176:179], v[200:203], v[82:85]
	v_mfma_f32_16x16x32_bf16 v[70:73], v[168:171], v[216:219], v[70:73]
	v_mfma_f32_16x16x32_bf16 v[66:69], v[176:179], v[216:219], v[66:69]
	v_mfma_f32_16x16x32_bf16 v[118:121], v[172:175], v[188:191], v[118:121]
	v_mfma_f32_16x16x32_bf16 v[114:117], v[180:183], v[188:191], v[114:117]
	v_mfma_f32_16x16x32_bf16 v[102:105], v[172:175], v[196:199], v[102:105]
	v_mfma_f32_16x16x32_bf16 v[98:101], v[180:183], v[196:199], v[98:101]
	v_mfma_f32_16x16x32_bf16 v[86:89], v[172:175], v[204:207], v[86:89]
	v_mfma_f32_16x16x32_bf16 v[82:85], v[180:183], v[204:207], v[82:85]
	v_mfma_f32_16x16x32_bf16 v[70:73], v[172:175], v[220:223], v[70:73]
	v_mfma_f32_16x16x32_bf16 v[66:69], v[180:183], v[220:223], v[66:69]
	s_setprio 0
	s_barrier
	s_add_i32 s46, s50, s76
	v_lshl_add_u64 v[164:165], v[164:165], 0, s[56:57]
	s_mov_b32 m0, s46
	ds_read_b128 v[184:187], v147 offset:49152
	ds_read_b128 v[188:191], v147 offset:50176
	ds_read_b128 v[192:195], v147 offset:51200
	ds_read_b128 v[196:199], v147 offset:52224
	ds_read_b128 v[200:203], v147 offset:53248
	ds_read_b128 v[204:207], v147 offset:54272
	ds_read_b128 v[216:219], v147 offset:55296
	ds_read_b128 v[220:223], v147 offset:56320
	global_load_lds_dwordx4 v[164:165], off
	s_add_i32 m0, s46, 0x2000
	s_add_u32 s44, s44, 0x100080
	v_lshl_add_u64 v[164:165], v[208:209], 0, s[56:57]
	s_addc_u32 s45, s45, 0
	s_add_i32 s46, s64, s76
	global_load_lds_dwordx4 v[164:165], off
	s_mov_b32 m0, s46
	v_lshl_add_u64 v[164:165], s[44:45], 0, v[126:127]
	global_load_lds_dwordx4 v[164:165], off
	s_add_i32 m0, s46, 0x2000
	v_lshl_add_u64 v[164:165], s[44:45], 0, v[122:123]
	global_load_lds_dwordx4 v[164:165], off
	s_mov_b32 m0, s79
	v_lshl_add_u64 v[164:165], v[240:241], 0, s[56:57]
	global_load_lds_dwordx4 v[164:165], off
	s_mov_b32 m0, s80
	v_lshl_add_u64 v[164:165], v[242:243], 0, s[56:57]
	global_load_lds_dwordx4 v[164:165], off
	s_waitcnt vmcnt(8)
	s_waitcnt lgkmcnt(0)
	s_barrier
	s_setprio 1
	s_waitcnt lgkmcnt(0)
	v_mfma_f32_16x16x32_bf16 v[62:65], v[148:151], v[184:187], v[62:65]
	v_mfma_f32_16x16x32_bf16 v[58:61], v[156:159], v[184:187], v[58:61]
	v_mfma_f32_16x16x32_bf16 v[46:49], v[148:151], v[192:195], v[46:49]
	v_mfma_f32_16x16x32_bf16 v[42:45], v[156:159], v[192:195], v[42:45]
	v_mfma_f32_16x16x32_bf16 v[30:33], v[148:151], v[200:203], v[30:33]
	v_mfma_f32_16x16x32_bf16 v[26:29], v[156:159], v[200:203], v[26:29]
	v_mfma_f32_16x16x32_bf16 v[14:17], v[148:151], v[216:219], v[14:17]
	v_mfma_f32_16x16x32_bf16 v[10:13], v[156:159], v[216:219], v[10:13]
	v_mfma_f32_16x16x32_bf16 v[62:65], v[152:155], v[188:191], v[62:65]
	v_mfma_f32_16x16x32_bf16 v[58:61], v[160:163], v[188:191], v[58:61]
	v_mfma_f32_16x16x32_bf16 v[46:49], v[152:155], v[196:199], v[46:49]
	v_mfma_f32_16x16x32_bf16 v[42:45], v[160:163], v[196:199], v[42:45]
	v_mfma_f32_16x16x32_bf16 v[30:33], v[152:155], v[204:207], v[30:33]
	v_mfma_f32_16x16x32_bf16 v[26:29], v[160:163], v[204:207], v[26:29]
	v_mfma_f32_16x16x32_bf16 v[14:17], v[152:155], v[220:223], v[14:17]
	v_mfma_f32_16x16x32_bf16 v[10:13], v[160:163], v[220:223], v[10:13]
	s_setprio 0
	s_setprio 1
	v_mfma_f32_16x16x32_bf16 v[54:57], v[168:171], v[184:187], v[54:57]
	v_mfma_f32_16x16x32_bf16 v[50:53], v[176:179], v[184:187], v[50:53]
	v_mfma_f32_16x16x32_bf16 v[38:41], v[168:171], v[192:195], v[38:41]
	v_mfma_f32_16x16x32_bf16 v[34:37], v[176:179], v[192:195], v[34:37]
	v_mfma_f32_16x16x32_bf16 v[22:25], v[168:171], v[200:203], v[22:25]
	v_mfma_f32_16x16x32_bf16 v[18:21], v[176:179], v[200:203], v[18:21]
	v_mfma_f32_16x16x32_bf16 v[6:9], v[168:171], v[216:219], v[6:9]
	v_mfma_f32_16x16x32_bf16 v[2:5], v[176:179], v[216:219], v[2:5]
	v_mfma_f32_16x16x32_bf16 v[54:57], v[172:175], v[188:191], v[54:57]
	v_mfma_f32_16x16x32_bf16 v[50:53], v[180:183], v[188:191], v[50:53]
	v_mfma_f32_16x16x32_bf16 v[38:41], v[172:175], v[196:199], v[38:41]
	v_mfma_f32_16x16x32_bf16 v[34:37], v[180:183], v[196:199], v[34:37]
	v_mfma_f32_16x16x32_bf16 v[22:25], v[172:175], v[204:207], v[22:25]
	v_mfma_f32_16x16x32_bf16 v[18:21], v[180:183], v[204:207], v[18:21]
	v_mfma_f32_16x16x32_bf16 v[6:9], v[172:175], v[220:223], v[6:9]
	v_mfma_f32_16x16x32_bf16 v[2:5], v[180:183], v[220:223], v[2:5]
	s_setprio 0
	s_barrier
	s_add_i32 s84, s84, 2
	s_add_u32 s36, s36, 0x100
	s_addc_u32 s37, s37, 0
	s_cmp_gt_u32 s84, 61
	s_cbranch_scc0 .LBB0_2891
	s_add_u32 s36, s59, 0xffffff00
	s_addc_u32 s37, s81, -1
	s_andn2_b64 vcc, exec, s[42:43]
	s_cbranch_vccnz .LBB0_2894
	v_mov_b32_e32 v2, 0
	s_mov_b32 s20, s26
	s_mov_b32 s52, s28
	s_mov_b64 s[24:25], s[34:35]
	s_mov_b32 s68, s58
	v_mov_b32_e32 v3, v2
	v_mov_b32_e32 v4, v2
	v_mov_b32_e32 v5, v2
	v_mov_b32_e32 v6, v2
	v_mov_b32_e32 v7, v2
	v_mov_b32_e32 v8, v2
	v_mov_b32_e32 v9, v2
	v_mov_b32_e32 v18, v2
	v_mov_b32_e32 v19, v2
	v_mov_b32_e32 v20, v2
	v_mov_b32_e32 v21, v2
	v_mov_b32_e32 v22, v2
	v_mov_b32_e32 v23, v2
	v_mov_b32_e32 v24, v2
	v_mov_b32_e32 v25, v2
	v_mov_b32_e32 v34, v2
	v_mov_b32_e32 v35, v2
	v_mov_b32_e32 v36, v2
	v_mov_b32_e32 v37, v2
	v_mov_b32_e32 v38, v2
	v_mov_b32_e32 v39, v2
	v_mov_b32_e32 v40, v2
	v_mov_b32_e32 v41, v2
	v_mov_b32_e32 v50, v2
	v_mov_b32_e32 v51, v2
	v_mov_b32_e32 v52, v2
	v_mov_b32_e32 v53, v2
	v_mov_b32_e32 v54, v2
	v_mov_b32_e32 v55, v2
	v_mov_b32_e32 v56, v2
	v_mov_b32_e32 v57, v2
	v_mov_b32_e32 v10, v2
	v_mov_b32_e32 v11, v2
	v_mov_b32_e32 v12, v2
	v_mov_b32_e32 v13, v2
	v_mov_b32_e32 v14, v2
	v_mov_b32_e32 v15, v2
	v_mov_b32_e32 v16, v2
	v_mov_b32_e32 v17, v2
	v_mov_b32_e32 v26, v2
	v_mov_b32_e32 v27, v2
	v_mov_b32_e32 v28, v2
	v_mov_b32_e32 v29, v2
	v_mov_b32_e32 v30, v2
	v_mov_b32_e32 v31, v2
	v_mov_b32_e32 v32, v2
	v_mov_b32_e32 v33, v2
	v_mov_b32_e32 v42, v2
	v_mov_b32_e32 v43, v2
	v_mov_b32_e32 v44, v2
	v_mov_b32_e32 v45, v2
	v_mov_b32_e32 v46, v2
	v_mov_b32_e32 v47, v2
	v_mov_b32_e32 v48, v2
	v_mov_b32_e32 v49, v2
	v_mov_b32_e32 v58, v2
	v_mov_b32_e32 v59, v2
	v_mov_b32_e32 v60, v2
	v_mov_b32_e32 v61, v2
	v_mov_b32_e32 v62, v2
	v_mov_b32_e32 v63, v2
	v_mov_b32_e32 v64, v2
	v_mov_b32_e32 v65, v2
	v_mov_b32_e32 v66, v2
	v_mov_b32_e32 v67, v2
	v_mov_b32_e32 v68, v2
	v_mov_b32_e32 v69, v2
	v_mov_b32_e32 v70, v2
	v_mov_b32_e32 v71, v2
	v_mov_b32_e32 v72, v2
	v_mov_b32_e32 v73, v2
	v_mov_b32_e32 v82, v2
	v_mov_b32_e32 v83, v2
	v_mov_b32_e32 v84, v2
	v_mov_b32_e32 v85, v2
	v_mov_b32_e32 v86, v2
	v_mov_b32_e32 v87, v2
	v_mov_b32_e32 v88, v2
	v_mov_b32_e32 v89, v2
	v_mov_b32_e32 v98, v2
	v_mov_b32_e32 v99, v2
	v_mov_b32_e32 v100, v2
	v_mov_b32_e32 v101, v2
	v_mov_b32_e32 v102, v2
	v_mov_b32_e32 v103, v2
	v_mov_b32_e32 v104, v2
	v_mov_b32_e32 v105, v2
	v_mov_b32_e32 v114, v2
	v_mov_b32_e32 v115, v2
	v_mov_b32_e32 v116, v2
	v_mov_b32_e32 v117, v2
	v_mov_b32_e32 v118, v2
	v_mov_b32_e32 v119, v2
	v_mov_b32_e32 v120, v2
	v_mov_b32_e32 v121, v2
	v_mov_b32_e32 v74, v2
	v_mov_b32_e32 v75, v2
	v_mov_b32_e32 v76, v2
	v_mov_b32_e32 v77, v2
	v_mov_b32_e32 v78, v2
	v_mov_b32_e32 v79, v2
	v_mov_b32_e32 v80, v2
	v_mov_b32_e32 v81, v2
	v_mov_b32_e32 v90, v2
	v_mov_b32_e32 v91, v2
	v_mov_b32_e32 v92, v2
	v_mov_b32_e32 v93, v2
	v_mov_b32_e32 v94, v2
	v_mov_b32_e32 v95, v2
	v_mov_b32_e32 v96, v2
	v_mov_b32_e32 v97, v2
	v_mov_b32_e32 v106, v2
	v_mov_b32_e32 v107, v2
	v_mov_b32_e32 v108, v2
	v_mov_b32_e32 v109, v2
	v_mov_b32_e32 v110, v2
	v_mov_b32_e32 v111, v2
	v_mov_b32_e32 v112, v2
	v_mov_b32_e32 v113, v2
	v_mov_b32_e32 v130, v2
	v_mov_b32_e32 v131, v2
	v_mov_b32_e32 v132, v2
	v_mov_b32_e32 v133, v2
	v_mov_b32_e32 v134, v2
	v_mov_b32_e32 v135, v2
	v_mov_b32_e32 v136, v2
	v_mov_b32_e32 v137, v2
	s_movk_i32 s92, 0x2b20
	s_andn2_b64 vcc, exec, s[40:41]
	s_cbranch_vccnz .LBB0_2895
	s_branch .LBB0_2896

.LBB0_2982:
	s_add_u32 s42, s24, s36
	s_addc_u32 s43, s25, s37
	s_add_u32 s42, s42, 0x100
	s_addc_u32 s43, s43, 0
	s_add_u32 s50, s59, s36
	s_addc_u32 s64, s79, s37
	s_add_i32 s65, 0, 0x10000
	s_cmpk_eq_i32 s36, 0x1f00
	s_cselect_b32 s45, s29, s43
	s_cselect_b32 s44, s80, s42
	s_cselect_b32 s43, s27, s64
	s_cselect_b32 s42, s81, s50
	s_add_i32 s50, 0, 0x14000
	v_add_u32_e32 v160, s65, v146
	v_add_u32_e32 v176, s50, v146
	ds_read_b128 v[148:151], v160
	ds_read_b128 v[152:155], v160 offset:1024
	ds_read_b128 v[156:159], v160 offset:2048
	ds_read_b128 v[160:163], v160 offset:3072
	ds_read_b128 v[164:167], v176
	ds_read_b128 v[168:171], v176 offset:1024
	ds_read_b128 v[172:175], v176 offset:2048
	ds_read_b128 v[176:179], v176 offset:3072
	v_lshl_add_u64 v[208:209], v[144:145], 0, s[36:37]
	s_add_i32 m0, s4, 0xc000
	ds_read_b128 v[180:183], v147
	ds_read_b128 v[184:187], v147 offset:1024
	ds_read_b128 v[188:191], v147 offset:2048
	ds_read_b128 v[192:195], v147 offset:3072
	ds_read_b128 v[196:199], v147 offset:4096
	ds_read_b128 v[200:203], v147 offset:5120
	ds_read_b128 v[204:207], v147 offset:6144
	ds_read_b128 v[216:219], v147 offset:7168
	global_load_lds_dwordx4 v[208:209], off
	s_add_i32 m0, s4, 0xe000
	v_lshl_add_u64 v[208:209], v[142:143], 0, s[36:37]
	global_load_lds_dwordx4 v[208:209], off
	s_waitcnt vmcnt(8)
	s_waitcnt lgkmcnt(0)
	s_barrier
	s_setprio 1
	s_waitcnt lgkmcnt(0)
	v_mfma_f32_16x16x32_bf16 v[134:137], v[148:151], v[180:183], v[134:137]
	v_mfma_f32_16x16x32_bf16 v[130:133], v[156:159], v[180:183], v[130:133]
	v_mfma_f32_16x16x32_bf16 v[110:113], v[148:151], v[188:191], v[110:113]
	v_mfma_f32_16x16x32_bf16 v[106:109], v[156:159], v[188:191], v[106:109]
	v_mfma_f32_16x16x32_bf16 v[94:97], v[148:151], v[196:199], v[94:97]
	v_mfma_f32_16x16x32_bf16 v[90:93], v[156:159], v[196:199], v[90:93]
	v_mfma_f32_16x16x32_bf16 v[78:81], v[148:151], v[204:207], v[78:81]
	v_mfma_f32_16x16x32_bf16 v[74:77], v[156:159], v[204:207], v[74:77]
	v_mfma_f32_16x16x32_bf16 v[134:137], v[152:155], v[184:187], v[134:137]
	v_mfma_f32_16x16x32_bf16 v[130:133], v[160:163], v[184:187], v[130:133]
	v_mfma_f32_16x16x32_bf16 v[110:113], v[152:155], v[192:195], v[110:113]
	v_mfma_f32_16x16x32_bf16 v[106:109], v[160:163], v[192:195], v[106:109]
	v_mfma_f32_16x16x32_bf16 v[94:97], v[152:155], v[200:203], v[94:97]
	v_mfma_f32_16x16x32_bf16 v[90:93], v[160:163], v[200:203], v[90:93]
	v_mfma_f32_16x16x32_bf16 v[78:81], v[152:155], v[216:219], v[78:81]
	v_mfma_f32_16x16x32_bf16 v[74:77], v[160:163], v[216:219], v[74:77]
	s_setprio 0
	s_setprio 1
	v_mfma_f32_16x16x32_bf16 v[118:121], v[164:167], v[180:183], v[118:121]
	v_mfma_f32_16x16x32_bf16 v[114:117], v[172:175], v[180:183], v[114:117]
	v_mfma_f32_16x16x32_bf16 v[102:105], v[164:167], v[188:191], v[102:105]
	v_mfma_f32_16x16x32_bf16 v[98:101], v[172:175], v[188:191], v[98:101]
	v_mfma_f32_16x16x32_bf16 v[86:89], v[164:167], v[196:199], v[86:89]
	v_mfma_f32_16x16x32_bf16 v[82:85], v[172:175], v[196:199], v[82:85]
	v_mfma_f32_16x16x32_bf16 v[70:73], v[164:167], v[204:207], v[70:73]
	v_mfma_f32_16x16x32_bf16 v[66:69], v[172:175], v[204:207], v[66:69]
	v_mfma_f32_16x16x32_bf16 v[118:121], v[168:171], v[184:187], v[118:121]
	v_mfma_f32_16x16x32_bf16 v[114:117], v[176:179], v[184:187], v[114:117]
	v_mfma_f32_16x16x32_bf16 v[102:105], v[168:171], v[192:195], v[102:105]
	v_mfma_f32_16x16x32_bf16 v[98:101], v[176:179], v[192:195], v[98:101]
	v_mfma_f32_16x16x32_bf16 v[86:89], v[168:171], v[200:203], v[86:89]
	v_mfma_f32_16x16x32_bf16 v[82:85], v[176:179], v[200:203], v[82:85]
	v_mfma_f32_16x16x32_bf16 v[70:73], v[168:171], v[216:219], v[70:73]
	v_mfma_f32_16x16x32_bf16 v[66:69], v[176:179], v[216:219], v[66:69]
	s_setprio 0
	s_barrier
	s_add_i32 s64, s65, s63
	v_lshl_add_u64 v[208:209], s[42:43], 0, v[126:127]
	s_mov_b32 m0, s64
	ds_read_b128 v[180:183], v147 offset:16384
	ds_read_b128 v[184:187], v147 offset:17408
	ds_read_b128 v[188:191], v147 offset:18432
	ds_read_b128 v[192:195], v147 offset:19456
	ds_read_b128 v[196:199], v147 offset:20480
	ds_read_b128 v[200:203], v147 offset:21504
	ds_read_b128 v[204:207], v147 offset:22528
	ds_read_b128 v[216:219], v147 offset:23552
	global_load_lds_dwordx4 v[208:209], off
	s_add_i32 m0, s64, 0x2000
	s_add_u32 s84, s42, 0x100000
	v_lshl_add_u64 v[220:221], s[42:43], 0, v[122:123]
	s_addc_u32 s85, s43, 0
	s_add_i32 s50, s50, s63
	global_load_lds_dwordx4 v[220:221], off
	v_lshl_add_u64 v[222:223], s[84:85], 0, v[126:127]
	s_mov_b32 m0, s50
	v_lshl_add_u64 v[240:241], s[44:45], 0, v[124:125]
	global_load_lds_dwordx4 v[222:223], off
	s_add_i32 m0, s50, 0x2000
	v_lshl_add_u64 v[222:223], s[84:85], 0, v[122:123]
	global_load_lds_dwordx4 v[222:223], off
	s_mov_b32 m0, s4
	v_lshl_add_u64 v[222:223], s[44:45], 0, v[128:129]
	global_load_lds_dwordx4 v[222:223], off
	s_mov_b32 m0, s33
	s_nop 0
	global_load_lds_dwordx4 v[240:241], off
	s_waitcnt vmcnt(8)
	s_waitcnt lgkmcnt(0)
	s_barrier
	s_setprio 1
	s_waitcnt lgkmcnt(0)
	v_mfma_f32_16x16x32_bf16 v[62:65], v[148:151], v[180:183], v[62:65]
	v_mfma_f32_16x16x32_bf16 v[58:61], v[156:159], v[180:183], v[58:61]
	v_mfma_f32_16x16x32_bf16 v[46:49], v[148:151], v[188:191], v[46:49]
	v_mfma_f32_16x16x32_bf16 v[42:45], v[156:159], v[188:191], v[42:45]
	v_mfma_f32_16x16x32_bf16 v[30:33], v[148:151], v[196:199], v[30:33]
	v_mfma_f32_16x16x32_bf16 v[26:29], v[156:159], v[196:199], v[26:29]
	v_mfma_f32_16x16x32_bf16 v[14:17], v[148:151], v[204:207], v[14:17]
	v_mfma_f32_16x16x32_bf16 v[10:13], v[156:159], v[204:207], v[10:13]
	v_mfma_f32_16x16x32_bf16 v[62:65], v[152:155], v[184:187], v[62:65]
	v_mfma_f32_16x16x32_bf16 v[58:61], v[160:163], v[184:187], v[58:61]
	v_mfma_f32_16x16x32_bf16 v[46:49], v[152:155], v[192:195], v[46:49]
	v_mfma_f32_16x16x32_bf16 v[42:45], v[160:163], v[192:195], v[42:45]
	v_mfma_f32_16x16x32_bf16 v[30:33], v[152:155], v[200:203], v[30:33]
	v_mfma_f32_16x16x32_bf16 v[26:29], v[160:163], v[200:203], v[26:29]
	v_mfma_f32_16x16x32_bf16 v[14:17], v[152:155], v[216:219], v[14:17]
	v_mfma_f32_16x16x32_bf16 v[10:13], v[160:163], v[216:219], v[10:13]
	s_setprio 0
	s_setprio 1
	v_mfma_f32_16x16x32_bf16 v[54:57], v[164:167], v[180:183], v[54:57]
	v_mfma_f32_16x16x32_bf16 v[50:53], v[172:175], v[180:183], v[50:53]
	v_mfma_f32_16x16x32_bf16 v[38:41], v[164:167], v[188:191], v[38:41]
	v_mfma_f32_16x16x32_bf16 v[34:37], v[172:175], v[188:191], v[34:37]
	v_mfma_f32_16x16x32_bf16 v[22:25], v[164:167], v[196:199], v[22:25]
	v_mfma_f32_16x16x32_bf16 v[18:21], v[172:175], v[196:199], v[18:21]
	v_mfma_f32_16x16x32_bf16 v[6:9], v[164:167], v[204:207], v[6:9]
	v_mfma_f32_16x16x32_bf16 v[2:5], v[172:175], v[204:207], v[2:5]
	v_mfma_f32_16x16x32_bf16 v[54:57], v[168:171], v[184:187], v[54:57]
	v_mfma_f32_16x16x32_bf16 v[50:53], v[176:179], v[184:187], v[50:53]
	v_mfma_f32_16x16x32_bf16 v[38:41], v[168:171], v[192:195], v[38:41]
	v_mfma_f32_16x16x32_bf16 v[34:37], v[176:179], v[192:195], v[34:37]
	v_mfma_f32_16x16x32_bf16 v[22:25], v[168:171], v[200:203], v[22:25]
	v_mfma_f32_16x16x32_bf16 v[18:21], v[176:179], v[200:203], v[18:21]
	v_mfma_f32_16x16x32_bf16 v[6:9], v[168:171], v[216:219], v[6:9]
	v_mfma_f32_16x16x32_bf16 v[2:5], v[176:179], v[216:219], v[2:5]
	s_setprio 0
	s_barrier
	s_add_i32 s50, 0, 0x18000
	s_add_i32 s64, 0, 0x1c000
	v_add_u32_e32 v160, s50, v146
	v_add_u32_e32 v176, s64, v146
	ds_read_b128 v[148:151], v160
	ds_read_b128 v[152:155], v160 offset:1024
	ds_read_b128 v[156:159], v160 offset:2048
	ds_read_b128 v[160:163], v160 offset:3072
	ds_read_b128 v[164:167], v176
	ds_read_b128 v[168:171], v176 offset:1024
	ds_read_b128 v[172:175], v176 offset:2048
	ds_read_b128 v[176:179], v176 offset:3072
	s_add_u32 s44, s44, 0x100000
	s_addc_u32 s45, s45, 0
	s_mov_b32 m0, s70
	v_lshl_add_u64 v[242:243], s[44:45], 0, v[128:129]
	ds_read_b128 v[180:183], v147 offset:32768
	ds_read_b128 v[184:187], v147 offset:33792
	ds_read_b128 v[188:191], v147 offset:34816
	ds_read_b128 v[192:195], v147 offset:35840
	ds_read_b128 v[196:199], v147 offset:36864
	ds_read_b128 v[200:203], v147 offset:37888
	ds_read_b128 v[204:207], v147 offset:38912
	ds_read_b128 v[216:219], v147 offset:39936
	global_load_lds_dwordx4 v[242:243], off
	s_mov_b32 m0, s71
	v_lshl_add_u64 v[242:243], s[44:45], 0, v[124:125]
	global_load_lds_dwordx4 v[242:243], off
	s_waitcnt vmcnt(8)
	s_waitcnt lgkmcnt(0)
	s_barrier
	s_setprio 1
	s_waitcnt lgkmcnt(0)
	v_mfma_f32_16x16x32_bf16 v[134:137], v[148:151], v[180:183], v[134:137]
	v_mfma_f32_16x16x32_bf16 v[130:133], v[156:159], v[180:183], v[130:133]
	v_mfma_f32_16x16x32_bf16 v[110:113], v[148:151], v[188:191], v[110:113]
	v_mfma_f32_16x16x32_bf16 v[106:109], v[156:159], v[188:191], v[106:109]
	v_mfma_f32_16x16x32_bf16 v[94:97], v[148:151], v[196:199], v[94:97]
	v_mfma_f32_16x16x32_bf16 v[90:93], v[156:159], v[196:199], v[90:93]
	v_mfma_f32_16x16x32_bf16 v[78:81], v[148:151], v[204:207], v[78:81]
	v_mfma_f32_16x16x32_bf16 v[74:77], v[156:159], v[204:207], v[74:77]
	v_mfma_f32_16x16x32_bf16 v[134:137], v[152:155], v[184:187], v[134:137]
	v_mfma_f32_16x16x32_bf16 v[130:133], v[160:163], v[184:187], v[130:133]
	v_mfma_f32_16x16x32_bf16 v[110:113], v[152:155], v[192:195], v[110:113]
	v_mfma_f32_16x16x32_bf16 v[106:109], v[160:163], v[192:195], v[106:109]
	v_mfma_f32_16x16x32_bf16 v[94:97], v[152:155], v[200:203], v[94:97]
	v_mfma_f32_16x16x32_bf16 v[90:93], v[160:163], v[200:203], v[90:93]
	v_mfma_f32_16x16x32_bf16 v[78:81], v[152:155], v[216:219], v[78:81]
	v_mfma_f32_16x16x32_bf16 v[74:77], v[160:163], v[216:219], v[74:77]
	s_setprio 0
	s_setprio 1
	v_mfma_f32_16x16x32_bf16 v[118:121], v[164:167], v[180:183], v[118:121]
	v_mfma_f32_16x16x32_bf16 v[114:117], v[172:175], v[180:183], v[114:117]
	v_mfma_f32_16x16x32_bf16 v[102:105], v[164:167], v[188:191], v[102:105]
	v_mfma_f32_16x16x32_bf16 v[98:101], v[172:175], v[188:191], v[98:101]
	v_mfma_f32_16x16x32_bf16 v[86:89], v[164:167], v[196:199], v[86:89]
	v_mfma_f32_16x16x32_bf16 v[82:85], v[172:175], v[196:199], v[82:85]
	v_mfma_f32_16x16x32_bf16 v[70:73], v[164:167], v[204:207], v[70:73]
	v_mfma_f32_16x16x32_bf16 v[66:69], v[172:175], v[204:207], v[66:69]
	v_mfma_f32_16x16x32_bf16 v[118:121], v[168:171], v[184:187], v[118:121]
	v_mfma_f32_16x16x32_bf16 v[114:117], v[176:179], v[184:187], v[114:117]
	v_mfma_f32_16x16x32_bf16 v[102:105], v[168:171], v[192:195], v[102:105]
	v_mfma_f32_16x16x32_bf16 v[98:101], v[176:179], v[192:195], v[98:101]
	v_mfma_f32_16x16x32_bf16 v[86:89], v[168:171], v[200:203], v[86:89]
	v_mfma_f32_16x16x32_bf16 v[82:85], v[176:179], v[200:203], v[82:85]
	v_mfma_f32_16x16x32_bf16 v[70:73], v[168:171], v[216:219], v[70:73]
	v_mfma_f32_16x16x32_bf16 v[66:69], v[176:179], v[216:219], v[66:69]
	s_setprio 0
	s_barrier
	s_add_i32 s44, s50, s63
	v_lshl_add_u64 v[208:209], v[208:209], 0, s[56:57]
	s_mov_b32 m0, s44
	ds_read_b128 v[180:183], v147 offset:49152
	ds_read_b128 v[184:187], v147 offset:50176
	ds_read_b128 v[188:191], v147 offset:51200
	ds_read_b128 v[192:195], v147 offset:52224
	ds_read_b128 v[196:199], v147 offset:53248
	ds_read_b128 v[200:203], v147 offset:54272
	ds_read_b128 v[204:207], v147 offset:55296
	ds_read_b128 v[216:219], v147 offset:56320
	global_load_lds_dwordx4 v[208:209], off
	s_add_i32 m0, s44, 0x2000
	s_add_u32 s42, s42, 0x100080
	v_lshl_add_u64 v[208:209], v[220:221], 0, s[56:57]
	s_addc_u32 s43, s43, 0
	s_add_i32 s44, s64, s63
	global_load_lds_dwordx4 v[208:209], off
	s_mov_b32 m0, s44
	v_lshl_add_u64 v[208:209], s[42:43], 0, v[126:127]
	global_load_lds_dwordx4 v[208:209], off
	s_add_i32 m0, s44, 0x2000
	v_lshl_add_u64 v[208:209], s[42:43], 0, v[122:123]
	global_load_lds_dwordx4 v[208:209], off
	s_mov_b32 m0, s76
	v_lshl_add_u64 v[208:209], v[222:223], 0, s[56:57]
	global_load_lds_dwordx4 v[208:209], off
	s_mov_b32 m0, s77
	v_lshl_add_u64 v[208:209], v[240:241], 0, s[56:57]
	global_load_lds_dwordx4 v[208:209], off
	s_waitcnt vmcnt(8)
	s_waitcnt lgkmcnt(0)
	s_barrier
	s_setprio 1
	s_waitcnt lgkmcnt(0)
	v_mfma_f32_16x16x32_bf16 v[62:65], v[148:151], v[180:183], v[62:65]
	v_mfma_f32_16x16x32_bf16 v[58:61], v[156:159], v[180:183], v[58:61]
	v_mfma_f32_16x16x32_bf16 v[46:49], v[148:151], v[188:191], v[46:49]
	v_mfma_f32_16x16x32_bf16 v[42:45], v[156:159], v[188:191], v[42:45]
	v_mfma_f32_16x16x32_bf16 v[30:33], v[148:151], v[196:199], v[30:33]
	v_mfma_f32_16x16x32_bf16 v[26:29], v[156:159], v[196:199], v[26:29]
	v_mfma_f32_16x16x32_bf16 v[14:17], v[148:151], v[204:207], v[14:17]
	v_mfma_f32_16x16x32_bf16 v[10:13], v[156:159], v[204:207], v[10:13]
	v_mfma_f32_16x16x32_bf16 v[62:65], v[152:155], v[184:187], v[62:65]
	v_mfma_f32_16x16x32_bf16 v[58:61], v[160:163], v[184:187], v[58:61]
	v_mfma_f32_16x16x32_bf16 v[46:49], v[152:155], v[192:195], v[46:49]
	v_mfma_f32_16x16x32_bf16 v[42:45], v[160:163], v[192:195], v[42:45]
	v_mfma_f32_16x16x32_bf16 v[30:33], v[152:155], v[200:203], v[30:33]
	v_mfma_f32_16x16x32_bf16 v[26:29], v[160:163], v[200:203], v[26:29]
	v_mfma_f32_16x16x32_bf16 v[14:17], v[152:155], v[216:219], v[14:17]
	v_mfma_f32_16x16x32_bf16 v[10:13], v[160:163], v[216:219], v[10:13]
	s_setprio 0
	s_setprio 1
	v_mfma_f32_16x16x32_bf16 v[54:57], v[164:167], v[180:183], v[54:57]
	v_mfma_f32_16x16x32_bf16 v[50:53], v[172:175], v[180:183], v[50:53]
	v_mfma_f32_16x16x32_bf16 v[38:41], v[164:167], v[188:191], v[38:41]
	v_mfma_f32_16x16x32_bf16 v[34:37], v[172:175], v[188:191], v[34:37]
	v_mfma_f32_16x16x32_bf16 v[22:25], v[164:167], v[196:199], v[22:25]
	v_mfma_f32_16x16x32_bf16 v[18:21], v[172:175], v[196:199], v[18:21]
	v_mfma_f32_16x16x32_bf16 v[6:9], v[164:167], v[204:207], v[6:9]
	v_mfma_f32_16x16x32_bf16 v[2:5], v[172:175], v[204:207], v[2:5]
	v_mfma_f32_16x16x32_bf16 v[54:57], v[168:171], v[184:187], v[54:57]
	v_mfma_f32_16x16x32_bf16 v[50:53], v[176:179], v[184:187], v[50:53]
	v_mfma_f32_16x16x32_bf16 v[38:41], v[168:171], v[192:195], v[38:41]
	v_mfma_f32_16x16x32_bf16 v[34:37], v[176:179], v[192:195], v[34:37]
	v_mfma_f32_16x16x32_bf16 v[22:25], v[168:171], v[200:203], v[22:25]
	v_mfma_f32_16x16x32_bf16 v[18:21], v[176:179], v[200:203], v[18:21]
	v_mfma_f32_16x16x32_bf16 v[6:9], v[168:171], v[216:219], v[6:9]
	v_mfma_f32_16x16x32_bf16 v[2:5], v[176:179], v[216:219], v[2:5]
	s_setprio 0
	s_barrier
	s_add_i32 s82, s82, 2
	s_add_u32 s36, s36, 0x100
	s_addc_u32 s37, s37, 0
	s_cmp_gt_u32 s82, 61
	s_cbranch_scc0 .LBB0_2982
	s_add_u32 s36, s59, 0xffffff00
	s_addc_u32 s37, s79, -1
	s_andn2_b64 vcc, exec, s[40:41]
	s_cbranch_vccnz .LBB0_2985
	v_mov_b32_e32 v2, 0
	s_mov_b32 s20, s26
	s_mov_b32 s78, s28
	s_mov_b64 s[24:25], s[34:35]
	s_mov_b32 s68, s58
	v_mov_b32_e32 v3, v2
	v_mov_b32_e32 v4, v2
	v_mov_b32_e32 v5, v2
	v_mov_b32_e32 v6, v2
	v_mov_b32_e32 v7, v2
	v_mov_b32_e32 v8, v2
	v_mov_b32_e32 v9, v2
	v_mov_b32_e32 v18, v2
	v_mov_b32_e32 v19, v2
	v_mov_b32_e32 v20, v2
	v_mov_b32_e32 v21, v2
	v_mov_b32_e32 v22, v2
	v_mov_b32_e32 v23, v2
	v_mov_b32_e32 v24, v2
	v_mov_b32_e32 v25, v2
	v_mov_b32_e32 v34, v2
	v_mov_b32_e32 v35, v2
	v_mov_b32_e32 v36, v2
	v_mov_b32_e32 v37, v2
	v_mov_b32_e32 v38, v2
	v_mov_b32_e32 v39, v2
	v_mov_b32_e32 v40, v2
	v_mov_b32_e32 v41, v2
	v_mov_b32_e32 v50, v2
	v_mov_b32_e32 v51, v2
	v_mov_b32_e32 v52, v2
	v_mov_b32_e32 v53, v2
	v_mov_b32_e32 v54, v2
	v_mov_b32_e32 v55, v2
	v_mov_b32_e32 v56, v2
	v_mov_b32_e32 v57, v2
	v_mov_b32_e32 v10, v2
	v_mov_b32_e32 v11, v2
	v_mov_b32_e32 v12, v2
	v_mov_b32_e32 v13, v2
	v_mov_b32_e32 v14, v2
	v_mov_b32_e32 v15, v2
	v_mov_b32_e32 v16, v2
	v_mov_b32_e32 v17, v2
	v_mov_b32_e32 v26, v2
	v_mov_b32_e32 v27, v2
	v_mov_b32_e32 v28, v2
	v_mov_b32_e32 v29, v2
	v_mov_b32_e32 v30, v2
	v_mov_b32_e32 v31, v2
	v_mov_b32_e32 v32, v2
	v_mov_b32_e32 v33, v2
	v_mov_b32_e32 v42, v2
	v_mov_b32_e32 v43, v2
	v_mov_b32_e32 v44, v2
	v_mov_b32_e32 v45, v2
	v_mov_b32_e32 v46, v2
	v_mov_b32_e32 v47, v2
	v_mov_b32_e32 v48, v2
	v_mov_b32_e32 v49, v2
	v_mov_b32_e32 v58, v2
	v_mov_b32_e32 v59, v2
	v_mov_b32_e32 v60, v2
	v_mov_b32_e32 v61, v2
	v_mov_b32_e32 v62, v2
	v_mov_b32_e32 v63, v2
	v_mov_b32_e32 v64, v2
	v_mov_b32_e32 v65, v2
	v_mov_b32_e32 v66, v2
	v_mov_b32_e32 v67, v2
	v_mov_b32_e32 v68, v2
	v_mov_b32_e32 v69, v2
	v_mov_b32_e32 v70, v2
	v_mov_b32_e32 v71, v2
	v_mov_b32_e32 v72, v2
	v_mov_b32_e32 v73, v2
	v_mov_b32_e32 v82, v2
	v_mov_b32_e32 v83, v2
	v_mov_b32_e32 v84, v2
	v_mov_b32_e32 v85, v2
	v_mov_b32_e32 v86, v2
	v_mov_b32_e32 v87, v2
	v_mov_b32_e32 v88, v2
	v_mov_b32_e32 v89, v2
	v_mov_b32_e32 v98, v2
	v_mov_b32_e32 v99, v2
	v_mov_b32_e32 v100, v2
	v_mov_b32_e32 v101, v2
	v_mov_b32_e32 v102, v2
	v_mov_b32_e32 v103, v2
	v_mov_b32_e32 v104, v2
	v_mov_b32_e32 v105, v2
	v_mov_b32_e32 v114, v2
	v_mov_b32_e32 v115, v2
	v_mov_b32_e32 v116, v2
	v_mov_b32_e32 v117, v2
	v_mov_b32_e32 v118, v2
	v_mov_b32_e32 v119, v2
	v_mov_b32_e32 v120, v2
	v_mov_b32_e32 v121, v2
	v_mov_b32_e32 v74, v2
	v_mov_b32_e32 v75, v2
	v_mov_b32_e32 v76, v2
	v_mov_b32_e32 v77, v2
	v_mov_b32_e32 v78, v2
	v_mov_b32_e32 v79, v2
	v_mov_b32_e32 v80, v2
	v_mov_b32_e32 v81, v2
	v_mov_b32_e32 v90, v2
	v_mov_b32_e32 v91, v2
	v_mov_b32_e32 v92, v2
	v_mov_b32_e32 v93, v2
	v_mov_b32_e32 v94, v2
	v_mov_b32_e32 v95, v2
	v_mov_b32_e32 v96, v2
	v_mov_b32_e32 v97, v2
	v_mov_b32_e32 v106, v2
	v_mov_b32_e32 v107, v2
	v_mov_b32_e32 v108, v2
	v_mov_b32_e32 v109, v2
	v_mov_b32_e32 v110, v2
	v_mov_b32_e32 v111, v2
	v_mov_b32_e32 v112, v2
	v_mov_b32_e32 v113, v2
	v_mov_b32_e32 v130, v2
	v_mov_b32_e32 v131, v2
	v_mov_b32_e32 v132, v2
	v_mov_b32_e32 v133, v2
	v_mov_b32_e32 v134, v2
	v_mov_b32_e32 v135, v2
	v_mov_b32_e32 v136, v2
	v_mov_b32_e32 v137, v2
	s_andn2_b64 vcc, exec, s[38:39]
	s_cbranch_vccnz .LBB0_2986
	s_branch .LBB0_2987
